# v28 + mid-block s_setprio 0/1 toggle pairs removed from the 48 GEMM MFMA blocks
# baseline (speedup 1.0000x reference)
.LBB0_103:
	ds_read_b128 v[154:157], v151
	ds_read_b128 v[158:161], v151 offset:1024
	ds_read_b128 v[162:165], v151 offset:2048
	ds_read_b128 v[166:169], v151 offset:3072
	ds_read_b128 v[170:173], v152
	ds_read_b128 v[174:177], v152 offset:1024
	ds_read_b128 v[178:181], v152 offset:2048
	ds_read_b128 v[182:185], v152 offset:3072
	s_add_i32 m0, s39, 0xc000
	ds_read_b128 v[186:189], v153
	ds_read_b128 v[190:193], v153 offset:1024
	ds_read_b128 v[194:197], v153 offset:2048
	ds_read_b128 v[198:201], v153 offset:3072
	ds_read_b128 v[202:205], v153 offset:4096
	ds_read_b128 v[206:209], v153 offset:5120
	ds_read_b128 v[210:213], v153 offset:6144
	ds_read_b128 v[214:217], v153 offset:7168
	global_load_lds_dwordx4 v[144:145], off
	s_add_i32 m0, s39, 0xe000
	s_nop 0
	global_load_lds_dwordx4 v[146:147], off
	s_waitcnt vmcnt(8)
	s_waitcnt lgkmcnt(0)
	s_barrier
	s_setprio 1
	s_waitcnt lgkmcnt(0)
	v_mfma_f32_16x16x32_bf16 v[124:127], v[154:157], v[186:189], v[124:127]
	v_mfma_f32_16x16x32_bf16 v[120:123], v[162:165], v[186:189], v[120:123]
	v_mfma_f32_16x16x32_bf16 v[108:111], v[154:157], v[194:197], v[108:111]
	v_mfma_f32_16x16x32_bf16 v[104:107], v[162:165], v[194:197], v[104:107]
	v_mfma_f32_16x16x32_bf16 v[92:95], v[154:157], v[202:205], v[92:95]
	v_mfma_f32_16x16x32_bf16 v[88:91], v[162:165], v[202:205], v[88:91]
	v_mfma_f32_16x16x32_bf16 v[76:79], v[154:157], v[210:213], v[76:79]
	v_mfma_f32_16x16x32_bf16 v[72:75], v[162:165], v[210:213], v[72:75]
	v_mfma_f32_16x16x32_bf16 v[124:127], v[158:161], v[190:193], v[124:127]
	v_mfma_f32_16x16x32_bf16 v[120:123], v[166:169], v[190:193], v[120:123]
	v_mfma_f32_16x16x32_bf16 v[108:111], v[158:161], v[198:201], v[108:111]
	v_mfma_f32_16x16x32_bf16 v[104:107], v[166:169], v[198:201], v[104:107]
	v_mfma_f32_16x16x32_bf16 v[92:95], v[158:161], v[206:209], v[92:95]
	v_mfma_f32_16x16x32_bf16 v[88:91], v[166:169], v[206:209], v[88:91]
	v_mfma_f32_16x16x32_bf16 v[76:79], v[158:161], v[214:217], v[76:79]
	v_mfma_f32_16x16x32_bf16 v[72:75], v[166:169], v[214:217], v[72:75]
	v_mfma_f32_16x16x32_bf16 v[116:119], v[170:173], v[186:189], v[116:119]
	v_mfma_f32_16x16x32_bf16 v[112:115], v[178:181], v[186:189], v[112:115]
	v_mfma_f32_16x16x32_bf16 v[100:103], v[170:173], v[194:197], v[100:103]
	v_mfma_f32_16x16x32_bf16 v[96:99], v[178:181], v[194:197], v[96:99]
	v_mfma_f32_16x16x32_bf16 v[84:87], v[170:173], v[202:205], v[84:87]
	v_mfma_f32_16x16x32_bf16 v[80:83], v[178:181], v[202:205], v[80:83]
	v_mfma_f32_16x16x32_bf16 v[68:71], v[170:173], v[210:213], v[68:71]
	v_mfma_f32_16x16x32_bf16 v[64:67], v[178:181], v[210:213], v[64:67]
	v_mfma_f32_16x16x32_bf16 v[116:119], v[174:177], v[190:193], v[116:119]
	v_mfma_f32_16x16x32_bf16 v[112:115], v[182:185], v[190:193], v[112:115]
	v_mfma_f32_16x16x32_bf16 v[100:103], v[174:177], v[198:201], v[100:103]
	v_mfma_f32_16x16x32_bf16 v[96:99], v[182:185], v[198:201], v[96:99]
	v_mfma_f32_16x16x32_bf16 v[84:87], v[174:177], v[206:209], v[84:87]
	v_mfma_f32_16x16x32_bf16 v[80:83], v[182:185], v[206:209], v[80:83]
	v_mfma_f32_16x16x32_bf16 v[68:71], v[174:177], v[214:217], v[68:71]
	v_mfma_f32_16x16x32_bf16 v[64:67], v[182:185], v[214:217], v[64:67]
	s_setprio 0
	s_barrier
	s_cmp_gt_u32 s11, 13
	s_cselect_b64 s[90:91], -1, 0
	s_and_b64 s[36:37], s[90:91], exec
	v_sub_co_u32_e64 v218, s[36:37], s11, 14
	s_nop 0
	v_readfirstlane_b32 s94, v218
	s_cselect_b32 s29, s35, s57
	s_cselect_b32 s89, s34, s56
	s_add_i32 s95, s94, 16
	s_and_b64 s[92:93], s[90:91], exec
	s_cselect_b32 s92, s94, s95
	s_ashr_i32 s93, s92, 31
	s_lshl_b64 s[92:93], s[92:93], 7
	s_add_u32 s94, s89, s92
	s_addc_u32 s95, s29, s93
	s_add_i32 s29, s86, s78
	v_lshl_add_u64 v[218:219], s[94:95], 0, v[130:131]
	s_mov_b32 m0, s29
	ds_read_b128 v[186:189], v153 offset:16384
	ds_read_b128 v[190:193], v153 offset:17408
	ds_read_b128 v[194:197], v153 offset:18432
	ds_read_b128 v[198:201], v153 offset:19456
	ds_read_b128 v[202:205], v153 offset:20480
	ds_read_b128 v[206:209], v153 offset:21504
	ds_read_b128 v[210:213], v153 offset:22528
	ds_read_b128 v[214:217], v153 offset:23552
	global_load_lds_dwordx4 v[218:219], off
	s_add_i32 m0, s29, 0x2000
	v_lshl_add_u64 v[218:219], s[94:95], 0, v[134:135]
	s_add_u32 s94, s94, 0x40000
	s_addc_u32 s95, s95, 0
	s_add_i32 s29, s87, s78
	global_load_lds_dwordx4 v[218:219], off
	v_lshl_add_u64 v[218:219], s[94:95], 0, v[130:131]
	s_mov_b32 m0, s29
	s_nop 0
	global_load_lds_dwordx4 v[218:219], off
	s_add_i32 m0, s29, 0x2000
	s_and_b64 s[90:91], s[90:91], exec
	s_cselect_b32 s89, s30, s60
	s_cselect_b32 s29, s31, s61
	s_add_u32 s90, s89, s92
	v_lshl_add_u64 v[218:219], s[94:95], 0, v[134:135]
	s_addc_u32 s91, s29, s93
	global_load_lds_dwordx4 v[218:219], off
	v_lshl_add_u64 v[218:219], s[90:91], 0, v[128:129]
	s_mov_b32 m0, s39
	s_nop 0
	global_load_lds_dwordx4 v[218:219], off
	v_lshl_add_u64 v[218:219], s[90:91], 0, v[132:133]
	s_mov_b32 m0, s79
	s_nop 0
	global_load_lds_dwordx4 v[218:219], off
	s_waitcnt vmcnt(8)
	s_waitcnt lgkmcnt(0)
	s_barrier
	s_setprio 1
	s_waitcnt lgkmcnt(0)
	v_mfma_f32_16x16x32_bf16 v[60:63], v[154:157], v[186:189], v[60:63]
	v_mfma_f32_16x16x32_bf16 v[56:59], v[162:165], v[186:189], v[56:59]
	v_mfma_f32_16x16x32_bf16 v[44:47], v[154:157], v[194:197], v[44:47]
	v_mfma_f32_16x16x32_bf16 v[40:43], v[162:165], v[194:197], v[40:43]
	v_mfma_f32_16x16x32_bf16 v[20:23], v[154:157], v[202:205], v[20:23]
	v_mfma_f32_16x16x32_bf16 v[16:19], v[162:165], v[202:205], v[16:19]
	v_mfma_f32_16x16x32_bf16 v[4:7], v[154:157], v[210:213], v[4:7]
	v_mfma_f32_16x16x32_bf16 v[0:3], v[162:165], v[210:213], v[0:3]
	v_mfma_f32_16x16x32_bf16 v[60:63], v[158:161], v[190:193], v[60:63]
	v_mfma_f32_16x16x32_bf16 v[56:59], v[166:169], v[190:193], v[56:59]
	v_mfma_f32_16x16x32_bf16 v[44:47], v[158:161], v[198:201], v[44:47]
	v_mfma_f32_16x16x32_bf16 v[40:43], v[166:169], v[198:201], v[40:43]
	v_mfma_f32_16x16x32_bf16 v[20:23], v[158:161], v[206:209], v[20:23]
	v_mfma_f32_16x16x32_bf16 v[16:19], v[166:169], v[206:209], v[16:19]
	v_mfma_f32_16x16x32_bf16 v[4:7], v[158:161], v[214:217], v[4:7]
	v_mfma_f32_16x16x32_bf16 v[0:3], v[166:169], v[214:217], v[0:3]
	v_mfma_f32_16x16x32_bf16 v[52:55], v[170:173], v[186:189], v[52:55]
	v_mfma_f32_16x16x32_bf16 v[48:51], v[178:181], v[186:189], v[48:51]
	v_mfma_f32_16x16x32_bf16 v[36:39], v[170:173], v[194:197], v[36:39]
	v_mfma_f32_16x16x32_bf16 v[32:35], v[178:181], v[194:197], v[32:35]
	v_mfma_f32_16x16x32_bf16 v[28:31], v[170:173], v[202:205], v[28:31]
	v_mfma_f32_16x16x32_bf16 v[24:27], v[178:181], v[202:205], v[24:27]
	v_mfma_f32_16x16x32_bf16 v[12:15], v[170:173], v[210:213], v[12:15]
	v_mfma_f32_16x16x32_bf16 v[8:11], v[178:181], v[210:213], v[8:11]
	v_mfma_f32_16x16x32_bf16 v[52:55], v[174:177], v[190:193], v[52:55]
	v_mfma_f32_16x16x32_bf16 v[48:51], v[182:185], v[190:193], v[48:51]
	v_mfma_f32_16x16x32_bf16 v[36:39], v[174:177], v[198:201], v[36:39]
	v_mfma_f32_16x16x32_bf16 v[32:35], v[182:185], v[198:201], v[32:35]
	v_mfma_f32_16x16x32_bf16 v[28:31], v[174:177], v[206:209], v[28:31]
	v_mfma_f32_16x16x32_bf16 v[24:27], v[182:185], v[206:209], v[24:27]
	v_mfma_f32_16x16x32_bf16 v[12:15], v[174:177], v[214:217], v[12:15]
	v_mfma_f32_16x16x32_bf16 v[8:11], v[182:185], v[214:217], v[8:11]
	s_setprio 0
	s_barrier
	s_add_i32 s29, 0, 0x18000
	s_add_i32 s89, 0, 0x1c000
	v_add_u32_e32 v166, s29, v149
	v_add_u32_e32 v182, s89, v149
	ds_read_b128 v[154:157], v166
	ds_read_b128 v[158:161], v166 offset:1024
	ds_read_b128 v[162:165], v166 offset:2048
	ds_read_b128 v[166:169], v166 offset:3072
	ds_read_b128 v[170:173], v182
	ds_read_b128 v[174:177], v182 offset:1024
	ds_read_b128 v[178:181], v182 offset:2048
	ds_read_b128 v[182:185], v182 offset:3072
	s_add_u32 s90, s90, 0x40000
	s_addc_u32 s91, s91, 0
	s_mov_b32 m0, s80
	v_lshl_add_u64 v[218:219], s[90:91], 0, v[128:129]
	ds_read_b128 v[186:189], v153 offset:32768
	ds_read_b128 v[190:193], v153 offset:33792
	ds_read_b128 v[194:197], v153 offset:34816
	ds_read_b128 v[198:201], v153 offset:35840
	ds_read_b128 v[202:205], v153 offset:36864
	ds_read_b128 v[206:209], v153 offset:37888
	ds_read_b128 v[210:213], v153 offset:38912
	ds_read_b128 v[214:217], v153 offset:39936
	global_load_lds_dwordx4 v[218:219], off
	v_lshl_add_u64 v[218:219], s[90:91], 0, v[132:133]
	s_mov_b32 m0, s81
	s_nop 0
	global_load_lds_dwordx4 v[218:219], off
	s_waitcnt vmcnt(8)
	s_waitcnt lgkmcnt(0)
	s_barrier
	s_setprio 1
	s_waitcnt lgkmcnt(0)
	v_mfma_f32_16x16x32_bf16 v[124:127], v[154:157], v[186:189], v[124:127]
	v_mfma_f32_16x16x32_bf16 v[120:123], v[162:165], v[186:189], v[120:123]
	v_mfma_f32_16x16x32_bf16 v[108:111], v[154:157], v[194:197], v[108:111]
	v_mfma_f32_16x16x32_bf16 v[104:107], v[162:165], v[194:197], v[104:107]
	v_mfma_f32_16x16x32_bf16 v[92:95], v[154:157], v[202:205], v[92:95]
	v_mfma_f32_16x16x32_bf16 v[88:91], v[162:165], v[202:205], v[88:91]
	v_mfma_f32_16x16x32_bf16 v[76:79], v[154:157], v[210:213], v[76:79]
	v_mfma_f32_16x16x32_bf16 v[72:75], v[162:165], v[210:213], v[72:75]
	v_mfma_f32_16x16x32_bf16 v[124:127], v[158:161], v[190:193], v[124:127]
	v_mfma_f32_16x16x32_bf16 v[120:123], v[166:169], v[190:193], v[120:123]
	v_mfma_f32_16x16x32_bf16 v[108:111], v[158:161], v[198:201], v[108:111]
	v_mfma_f32_16x16x32_bf16 v[104:107], v[166:169], v[198:201], v[104:107]
	v_mfma_f32_16x16x32_bf16 v[92:95], v[158:161], v[206:209], v[92:95]
	v_mfma_f32_16x16x32_bf16 v[88:91], v[166:169], v[206:209], v[88:91]
	v_mfma_f32_16x16x32_bf16 v[76:79], v[158:161], v[214:217], v[76:79]
	v_mfma_f32_16x16x32_bf16 v[72:75], v[166:169], v[214:217], v[72:75]
	v_mfma_f32_16x16x32_bf16 v[116:119], v[170:173], v[186:189], v[116:119]
	v_mfma_f32_16x16x32_bf16 v[112:115], v[178:181], v[186:189], v[112:115]
	v_mfma_f32_16x16x32_bf16 v[100:103], v[170:173], v[194:197], v[100:103]
	v_mfma_f32_16x16x32_bf16 v[96:99], v[178:181], v[194:197], v[96:99]
	v_mfma_f32_16x16x32_bf16 v[84:87], v[170:173], v[202:205], v[84:87]
	v_mfma_f32_16x16x32_bf16 v[80:83], v[178:181], v[202:205], v[80:83]
	v_mfma_f32_16x16x32_bf16 v[68:71], v[170:173], v[210:213], v[68:71]
	v_mfma_f32_16x16x32_bf16 v[64:67], v[178:181], v[210:213], v[64:67]
	v_mfma_f32_16x16x32_bf16 v[116:119], v[174:177], v[190:193], v[116:119]
	v_mfma_f32_16x16x32_bf16 v[112:115], v[182:185], v[190:193], v[112:115]
	v_mfma_f32_16x16x32_bf16 v[100:103], v[174:177], v[198:201], v[100:103]
	v_mfma_f32_16x16x32_bf16 v[96:99], v[182:185], v[198:201], v[96:99]
	v_mfma_f32_16x16x32_bf16 v[84:87], v[174:177], v[206:209], v[84:87]
	v_mfma_f32_16x16x32_bf16 v[80:83], v[182:185], v[206:209], v[80:83]
	v_mfma_f32_16x16x32_bf16 v[68:71], v[174:177], v[214:217], v[68:71]
	v_mfma_f32_16x16x32_bf16 v[64:67], v[182:185], v[214:217], v[64:67]
	s_setprio 0
	s_barrier
	s_cmp_gt_u32 s11, 12
	s_cselect_b64 s[90:91], -1, 0
	s_and_b64 s[92:93], s[90:91], exec
	s_cselect_b32 s92, -13, 3
	s_cselect_b32 s95, s35, s57
	s_cselect_b32 s94, s34, s56
	s_add_i32 s92, s92, s11
	s_ashr_i32 s93, s92, 31
	s_lshl_b64 s[92:93], s[92:93], 7
	s_add_u32 s94, s94, s92
	s_addc_u32 s95, s95, s93
	s_add_i32 s29, s29, s78
	v_lshl_add_u64 v[218:219], s[94:95], 0, v[130:131]
	s_mov_b32 m0, s29
	ds_read_b128 v[186:189], v153 offset:49152
	ds_read_b128 v[190:193], v153 offset:50176
	ds_read_b128 v[194:197], v153 offset:51200
	ds_read_b128 v[198:201], v153 offset:52224
	ds_read_b128 v[202:205], v153 offset:53248
	ds_read_b128 v[206:209], v153 offset:54272
	ds_read_b128 v[210:213], v153 offset:55296
	ds_read_b128 v[214:217], v153 offset:56320
	global_load_lds_dwordx4 v[218:219], off
	s_add_i32 m0, s29, 0x2000
	v_lshl_add_u64 v[218:219], s[94:95], 0, v[134:135]
	s_add_u32 s94, s94, 0x40000
	s_addc_u32 s95, s95, 0
	s_add_i32 s29, s89, s78
	global_load_lds_dwordx4 v[218:219], off
	v_lshl_add_u64 v[218:219], s[94:95], 0, v[130:131]
	s_mov_b32 m0, s29
	s_nop 0
	global_load_lds_dwordx4 v[218:219], off
	s_add_i32 m0, s29, 0x2000
	s_and_b64 s[90:91], s[90:91], exec
	s_cselect_b32 s89, s30, s60
	s_cselect_b32 s29, s31, s61
	s_add_u32 s90, s89, s92
	v_lshl_add_u64 v[218:219], s[94:95], 0, v[134:135]
	s_addc_u32 s91, s29, s93
	global_load_lds_dwordx4 v[218:219], off
	v_lshl_add_u64 v[218:219], s[90:91], 0, v[128:129]
	s_mov_b32 m0, s83
	s_nop 0
	global_load_lds_dwordx4 v[218:219], off
	v_lshl_add_u64 v[218:219], s[90:91], 0, v[132:133]
	s_mov_b32 m0, s84
	s_nop 0
	global_load_lds_dwordx4 v[218:219], off
	s_waitcnt vmcnt(8)
	s_waitcnt lgkmcnt(0)
	s_barrier
	s_setprio 1
	s_waitcnt lgkmcnt(0)
	v_mfma_f32_16x16x32_bf16 v[60:63], v[154:157], v[186:189], v[60:63]
	v_mfma_f32_16x16x32_bf16 v[56:59], v[162:165], v[186:189], v[56:59]
	v_mfma_f32_16x16x32_bf16 v[44:47], v[154:157], v[194:197], v[44:47]
	v_mfma_f32_16x16x32_bf16 v[40:43], v[162:165], v[194:197], v[40:43]
	v_mfma_f32_16x16x32_bf16 v[20:23], v[154:157], v[202:205], v[20:23]
	v_mfma_f32_16x16x32_bf16 v[16:19], v[162:165], v[202:205], v[16:19]
	v_mfma_f32_16x16x32_bf16 v[4:7], v[154:157], v[210:213], v[4:7]
	v_mfma_f32_16x16x32_bf16 v[0:3], v[162:165], v[210:213], v[0:3]
	v_mfma_f32_16x16x32_bf16 v[60:63], v[158:161], v[190:193], v[60:63]
	v_mfma_f32_16x16x32_bf16 v[56:59], v[166:169], v[190:193], v[56:59]
	v_mfma_f32_16x16x32_bf16 v[44:47], v[158:161], v[198:201], v[44:47]
	v_mfma_f32_16x16x32_bf16 v[40:43], v[166:169], v[198:201], v[40:43]
	v_mfma_f32_16x16x32_bf16 v[20:23], v[158:161], v[206:209], v[20:23]
	v_mfma_f32_16x16x32_bf16 v[16:19], v[166:169], v[206:209], v[16:19]
	v_mfma_f32_16x16x32_bf16 v[4:7], v[158:161], v[214:217], v[4:7]
	v_mfma_f32_16x16x32_bf16 v[0:3], v[166:169], v[214:217], v[0:3]
	v_mfma_f32_16x16x32_bf16 v[52:55], v[170:173], v[186:189], v[52:55]
	v_mfma_f32_16x16x32_bf16 v[48:51], v[178:181], v[186:189], v[48:51]
	v_mfma_f32_16x16x32_bf16 v[36:39], v[170:173], v[194:197], v[36:39]
	v_mfma_f32_16x16x32_bf16 v[32:35], v[178:181], v[194:197], v[32:35]
	v_mfma_f32_16x16x32_bf16 v[28:31], v[170:173], v[202:205], v[28:31]
	v_mfma_f32_16x16x32_bf16 v[24:27], v[178:181], v[202:205], v[24:27]
	v_mfma_f32_16x16x32_bf16 v[12:15], v[170:173], v[210:213], v[12:15]
	v_mfma_f32_16x16x32_bf16 v[8:11], v[178:181], v[210:213], v[8:11]
	v_mfma_f32_16x16x32_bf16 v[52:55], v[174:177], v[190:193], v[52:55]
	v_mfma_f32_16x16x32_bf16 v[48:51], v[182:185], v[190:193], v[48:51]
	v_mfma_f32_16x16x32_bf16 v[36:39], v[174:177], v[198:201], v[36:39]
	v_mfma_f32_16x16x32_bf16 v[32:35], v[182:185], v[198:201], v[32:35]
	v_mfma_f32_16x16x32_bf16 v[28:31], v[174:177], v[206:209], v[28:31]
	v_mfma_f32_16x16x32_bf16 v[24:27], v[182:185], v[206:209], v[24:27]
	v_mfma_f32_16x16x32_bf16 v[12:15], v[174:177], v[214:217], v[12:15]
	v_mfma_f32_16x16x32_bf16 v[8:11], v[182:185], v[214:217], v[8:11]
	s_setprio 0
	s_barrier
	v_lshl_add_u64 v[144:145], v[144:145], 0, s[8:9]
	v_lshl_add_u64 v[146:147], v[146:147], 0, s[8:9]
	s_add_i32 s11, s11, 2
	s_and_b64 vcc, exec, s[36:37]
	s_cbranch_vccnz .LBB0_103
	s_andn2_b64 vcc, exec, s[6:7]
	s_cbranch_vccnz .LBB0_106
	s_barrier

.LBB0_124:
	ds_read_b128 v[152:155], v164
	ds_read_b128 v[156:159], v164 offset:1024
	ds_read_b128 v[168:171], v164 offset:2048
	ds_read_b128 v[172:175], v164 offset:3072
	ds_read_b128 v[176:179], v165
	ds_read_b128 v[180:183], v165 offset:1024
	ds_read_b128 v[184:187], v165 offset:2048
	ds_read_b128 v[188:191], v165 offset:3072
	s_add_i32 m0, s79, 0xc000
	ds_read_b128 v[192:195], v166
	ds_read_b128 v[196:199], v166 offset:1024
	ds_read_b128 v[200:203], v166 offset:2048
	ds_read_b128 v[204:207], v166 offset:3072
	ds_read_b128 v[208:211], v166 offset:4096
	ds_read_b128 v[212:215], v166 offset:5120
	ds_read_b128 v[216:219], v166 offset:6144
	ds_read_b128 v[220:223], v166 offset:7168
	global_load_lds_dwordx4 v[128:129], off
	s_add_i32 m0, s79, 0xe000
	s_nop 0
	global_load_lds_dwordx4 v[130:131], off
	s_waitcnt vmcnt(8)
	s_waitcnt lgkmcnt(0)
	s_barrier
	s_setprio 1
	s_waitcnt lgkmcnt(0)
	v_mfma_f32_16x16x32_bf16 v[124:127], v[152:155], v[192:195], v[124:127]
	v_mfma_f32_16x16x32_bf16 v[120:123], v[168:171], v[192:195], v[120:123]
	v_mfma_f32_16x16x32_bf16 v[108:111], v[152:155], v[200:203], v[108:111]
	v_mfma_f32_16x16x32_bf16 v[104:107], v[168:171], v[200:203], v[104:107]
	v_mfma_f32_16x16x32_bf16 v[92:95], v[152:155], v[208:211], v[92:95]
	v_mfma_f32_16x16x32_bf16 v[88:91], v[168:171], v[208:211], v[88:91]
	v_mfma_f32_16x16x32_bf16 v[76:79], v[152:155], v[216:219], v[76:79]
	v_mfma_f32_16x16x32_bf16 v[72:75], v[168:171], v[216:219], v[72:75]
	v_mfma_f32_16x16x32_bf16 v[124:127], v[156:159], v[196:199], v[124:127]
	v_mfma_f32_16x16x32_bf16 v[120:123], v[172:175], v[196:199], v[120:123]
	v_mfma_f32_16x16x32_bf16 v[108:111], v[156:159], v[204:207], v[108:111]
	v_mfma_f32_16x16x32_bf16 v[104:107], v[172:175], v[204:207], v[104:107]
	v_mfma_f32_16x16x32_bf16 v[92:95], v[156:159], v[212:215], v[92:95]
	v_mfma_f32_16x16x32_bf16 v[88:91], v[172:175], v[212:215], v[88:91]
	v_mfma_f32_16x16x32_bf16 v[76:79], v[156:159], v[220:223], v[76:79]
	v_mfma_f32_16x16x32_bf16 v[72:75], v[172:175], v[220:223], v[72:75]
	v_mfma_f32_16x16x32_bf16 v[116:119], v[176:179], v[192:195], v[116:119]
	v_mfma_f32_16x16x32_bf16 v[112:115], v[184:187], v[192:195], v[112:115]
	v_mfma_f32_16x16x32_bf16 v[100:103], v[176:179], v[200:203], v[100:103]
	v_mfma_f32_16x16x32_bf16 v[96:99], v[184:187], v[200:203], v[96:99]
	v_mfma_f32_16x16x32_bf16 v[84:87], v[176:179], v[208:211], v[84:87]
	v_mfma_f32_16x16x32_bf16 v[80:83], v[184:187], v[208:211], v[80:83]
	v_mfma_f32_16x16x32_bf16 v[68:71], v[176:179], v[216:219], v[68:71]
	v_mfma_f32_16x16x32_bf16 v[64:67], v[184:187], v[216:219], v[64:67]
	v_mfma_f32_16x16x32_bf16 v[116:119], v[180:183], v[196:199], v[116:119]
	v_mfma_f32_16x16x32_bf16 v[112:115], v[188:191], v[196:199], v[112:115]
	v_mfma_f32_16x16x32_bf16 v[100:103], v[180:183], v[204:207], v[100:103]
	v_mfma_f32_16x16x32_bf16 v[96:99], v[188:191], v[204:207], v[96:99]
	v_mfma_f32_16x16x32_bf16 v[84:87], v[180:183], v[212:215], v[84:87]
	v_mfma_f32_16x16x32_bf16 v[80:83], v[188:191], v[212:215], v[80:83]
	v_mfma_f32_16x16x32_bf16 v[68:71], v[180:183], v[220:223], v[68:71]
	v_mfma_f32_16x16x32_bf16 v[64:67], v[188:191], v[220:223], v[64:67]
	s_setprio 0
	s_barrier
	s_cmp_gt_u32 s0, 13
	s_cselect_b64 vcc, -1, 0
	s_and_b64 s[36:37], vcc, exec
	v_sub_co_u32_e64 v160, s[36:37], s0, 14
	s_nop 0
	v_readfirstlane_b32 s39, v160
	s_cselect_b32 s7, s75, s83
	s_cselect_b32 s6, s74, s82
	s_add_i32 s57, s39, 16
	s_and_b64 s[34:35], vcc, exec
	s_cselect_b32 s34, s39, s57
	s_ashr_i32 s35, s34, 31
	s_lshl_b64 s[34:35], s[34:35], 7
	s_add_u32 s6, s6, s34
	s_addc_u32 s7, s7, s35
	s_add_i32 s39, s76, s29
	v_lshl_add_u64 v[160:161], s[6:7], 0, v[134:135]
	s_mov_b32 m0, s39
	ds_read_b128 v[192:195], v166 offset:16384
	ds_read_b128 v[196:199], v166 offset:17408
	ds_read_b128 v[200:203], v166 offset:18432
	ds_read_b128 v[204:207], v166 offset:19456
	ds_read_b128 v[208:211], v166 offset:20480
	ds_read_b128 v[212:215], v166 offset:21504
	ds_read_b128 v[216:219], v166 offset:22528
	ds_read_b128 v[220:223], v166 offset:23552
	global_load_lds_dwordx4 v[160:161], off
	s_add_i32 m0, s39, 0x2000
	v_lshl_add_u64 v[160:161], s[6:7], 0, v[138:139]
	s_add_u32 s6, s6, 0x40000
	s_addc_u32 s7, s7, 0
	s_add_i32 s39, s4, s29
	global_load_lds_dwordx4 v[160:161], off
	v_lshl_add_u64 v[160:161], s[6:7], 0, v[134:135]
	s_mov_b32 m0, s39
	s_nop 0
	global_load_lds_dwordx4 v[160:161], off
	s_add_i32 m0, s39, 0x2000
	v_lshl_add_u64 v[160:161], s[6:7], 0, v[138:139]
	s_and_b64 s[6:7], vcc, exec
	s_cselect_b32 s6, s60, s80
	s_cselect_b32 s7, s61, s81
	s_add_u32 s6, s6, s34
	s_addc_u32 s7, s7, s35
	global_load_lds_dwordx4 v[160:161], off
	v_lshl_add_u64 v[160:161], s[6:7], 0, v[132:133]
	s_mov_b32 m0, s79
	s_nop 0
	global_load_lds_dwordx4 v[160:161], off
	v_lshl_add_u64 v[160:161], s[6:7], 0, v[136:137]
	s_mov_b32 m0, s87
	s_nop 0
	global_load_lds_dwordx4 v[160:161], off
	s_waitcnt vmcnt(8)
	s_waitcnt lgkmcnt(0)
	s_barrier
	s_setprio 1
	s_waitcnt lgkmcnt(0)
	v_mfma_f32_16x16x32_bf16 v[60:63], v[152:155], v[192:195], v[60:63]
	v_mfma_f32_16x16x32_bf16 v[56:59], v[168:171], v[192:195], v[56:59]
	v_mfma_f32_16x16x32_bf16 v[44:47], v[152:155], v[200:203], v[44:47]
	v_mfma_f32_16x16x32_bf16 v[40:43], v[168:171], v[200:203], v[40:43]
	v_mfma_f32_16x16x32_bf16 v[28:31], v[152:155], v[208:211], v[28:31]
	v_mfma_f32_16x16x32_bf16 v[16:19], v[168:171], v[208:211], v[16:19]
	v_mfma_f32_16x16x32_bf16 v[8:11], v[152:155], v[216:219], v[8:11]
	v_mfma_f32_16x16x32_bf16 v[0:3], v[168:171], v[216:219], v[0:3]
	v_mfma_f32_16x16x32_bf16 v[60:63], v[156:159], v[196:199], v[60:63]
	v_mfma_f32_16x16x32_bf16 v[56:59], v[172:175], v[196:199], v[56:59]
	v_mfma_f32_16x16x32_bf16 v[44:47], v[156:159], v[204:207], v[44:47]
	v_mfma_f32_16x16x32_bf16 v[40:43], v[172:175], v[204:207], v[40:43]
	v_mfma_f32_16x16x32_bf16 v[28:31], v[156:159], v[212:215], v[28:31]
	v_mfma_f32_16x16x32_bf16 v[16:19], v[172:175], v[212:215], v[16:19]
	v_mfma_f32_16x16x32_bf16 v[8:11], v[156:159], v[220:223], v[8:11]
	v_mfma_f32_16x16x32_bf16 v[0:3], v[172:175], v[220:223], v[0:3]
	v_mfma_f32_16x16x32_bf16 v[52:55], v[176:179], v[192:195], v[52:55]
	v_mfma_f32_16x16x32_bf16 v[48:51], v[184:187], v[192:195], v[48:51]
	v_mfma_f32_16x16x32_bf16 v[36:39], v[176:179], v[200:203], v[36:39]
	v_mfma_f32_16x16x32_bf16 v[32:35], v[184:187], v[200:203], v[32:35]
	v_mfma_f32_16x16x32_bf16 v[24:27], v[176:179], v[208:211], v[24:27]
	v_mfma_f32_16x16x32_bf16 v[20:23], v[184:187], v[208:211], v[20:23]
	v_mfma_f32_16x16x32_bf16 v[12:15], v[176:179], v[216:219], v[12:15]
	v_mfma_f32_16x16x32_bf16 v[4:7], v[184:187], v[216:219], v[4:7]
	v_mfma_f32_16x16x32_bf16 v[52:55], v[180:183], v[196:199], v[52:55]
	v_mfma_f32_16x16x32_bf16 v[48:51], v[188:191], v[196:199], v[48:51]
	v_mfma_f32_16x16x32_bf16 v[36:39], v[180:183], v[204:207], v[36:39]
	v_mfma_f32_16x16x32_bf16 v[32:35], v[188:191], v[204:207], v[32:35]
	v_mfma_f32_16x16x32_bf16 v[24:27], v[180:183], v[212:215], v[24:27]
	v_mfma_f32_16x16x32_bf16 v[20:23], v[188:191], v[212:215], v[20:23]
	v_mfma_f32_16x16x32_bf16 v[12:15], v[180:183], v[220:223], v[12:15]
	v_mfma_f32_16x16x32_bf16 v[4:7], v[188:191], v[220:223], v[4:7]
	s_setprio 0
	s_barrier
	s_add_i32 s39, 0, 0x18000
	v_add_u32_e32 v160, s39, v162
	s_add_i32 s57, 0, 0x1c000
	ds_read_b128 v[152:155], v160
	ds_read_b128 v[156:159], v160 offset:1024
	ds_read_b128 v[168:171], v160 offset:2048
	ds_read_b128 v[172:175], v160 offset:3072
	v_add_u32_e32 v160, s57, v162
	ds_read_b128 v[176:179], v160
	ds_read_b128 v[180:183], v160 offset:1024
	ds_read_b128 v[184:187], v160 offset:2048
	ds_read_b128 v[188:191], v160 offset:3072
	s_add_u32 s6, s6, 0x40000
	s_addc_u32 s7, s7, 0
	s_mov_b32 m0, s88
	v_lshl_add_u64 v[160:161], s[6:7], 0, v[132:133]
	ds_read_b128 v[192:195], v166 offset:32768
	ds_read_b128 v[196:199], v166 offset:33792
	ds_read_b128 v[200:203], v166 offset:34816
	ds_read_b128 v[204:207], v166 offset:35840
	ds_read_b128 v[208:211], v166 offset:36864
	ds_read_b128 v[212:215], v166 offset:37888
	ds_read_b128 v[216:219], v166 offset:38912
	ds_read_b128 v[220:223], v166 offset:39936
	global_load_lds_dwordx4 v[160:161], off
	v_lshl_add_u64 v[160:161], s[6:7], 0, v[136:137]
	s_mov_b32 m0, s89
	s_nop 0
	global_load_lds_dwordx4 v[160:161], off
	s_waitcnt vmcnt(8)
	s_waitcnt lgkmcnt(0)
	s_barrier
	s_setprio 1
	s_waitcnt lgkmcnt(0)
	v_mfma_f32_16x16x32_bf16 v[124:127], v[152:155], v[192:195], v[124:127]
	v_mfma_f32_16x16x32_bf16 v[120:123], v[168:171], v[192:195], v[120:123]
	v_mfma_f32_16x16x32_bf16 v[108:111], v[152:155], v[200:203], v[108:111]
	v_mfma_f32_16x16x32_bf16 v[104:107], v[168:171], v[200:203], v[104:107]
	v_mfma_f32_16x16x32_bf16 v[92:95], v[152:155], v[208:211], v[92:95]
	v_mfma_f32_16x16x32_bf16 v[88:91], v[168:171], v[208:211], v[88:91]
	v_mfma_f32_16x16x32_bf16 v[76:79], v[152:155], v[216:219], v[76:79]
	v_mfma_f32_16x16x32_bf16 v[72:75], v[168:171], v[216:219], v[72:75]
	v_mfma_f32_16x16x32_bf16 v[124:127], v[156:159], v[196:199], v[124:127]
	v_mfma_f32_16x16x32_bf16 v[120:123], v[172:175], v[196:199], v[120:123]
	v_mfma_f32_16x16x32_bf16 v[108:111], v[156:159], v[204:207], v[108:111]
	v_mfma_f32_16x16x32_bf16 v[104:107], v[172:175], v[204:207], v[104:107]
	v_mfma_f32_16x16x32_bf16 v[92:95], v[156:159], v[212:215], v[92:95]
	v_mfma_f32_16x16x32_bf16 v[88:91], v[172:175], v[212:215], v[88:91]
	v_mfma_f32_16x16x32_bf16 v[76:79], v[156:159], v[220:223], v[76:79]
	v_mfma_f32_16x16x32_bf16 v[72:75], v[172:175], v[220:223], v[72:75]
	v_mfma_f32_16x16x32_bf16 v[116:119], v[176:179], v[192:195], v[116:119]
	v_mfma_f32_16x16x32_bf16 v[112:115], v[184:187], v[192:195], v[112:115]
	v_mfma_f32_16x16x32_bf16 v[100:103], v[176:179], v[200:203], v[100:103]
	v_mfma_f32_16x16x32_bf16 v[96:99], v[184:187], v[200:203], v[96:99]
	v_mfma_f32_16x16x32_bf16 v[84:87], v[176:179], v[208:211], v[84:87]
	v_mfma_f32_16x16x32_bf16 v[80:83], v[184:187], v[208:211], v[80:83]
	v_mfma_f32_16x16x32_bf16 v[68:71], v[176:179], v[216:219], v[68:71]
	v_mfma_f32_16x16x32_bf16 v[64:67], v[184:187], v[216:219], v[64:67]
	v_mfma_f32_16x16x32_bf16 v[116:119], v[180:183], v[196:199], v[116:119]
	v_mfma_f32_16x16x32_bf16 v[112:115], v[188:191], v[196:199], v[112:115]
	v_mfma_f32_16x16x32_bf16 v[100:103], v[180:183], v[204:207], v[100:103]
	v_mfma_f32_16x16x32_bf16 v[96:99], v[188:191], v[204:207], v[96:99]
	v_mfma_f32_16x16x32_bf16 v[84:87], v[180:183], v[212:215], v[84:87]
	v_mfma_f32_16x16x32_bf16 v[80:83], v[188:191], v[212:215], v[80:83]
	v_mfma_f32_16x16x32_bf16 v[68:71], v[180:183], v[220:223], v[68:71]
	v_mfma_f32_16x16x32_bf16 v[64:67], v[188:191], v[220:223], v[64:67]
	s_setprio 0
	s_barrier
	s_cmp_gt_u32 s0, 12
	s_cselect_b64 s[6:7], -1, 0
	s_and_b64 s[34:35], s[6:7], exec
	s_cselect_b32 s34, -13, 3
	s_cselect_b32 vcc_hi, s75, s83
	s_cselect_b32 vcc_lo, s74, s82
	s_add_i32 s34, s34, s0
	s_ashr_i32 s35, s34, 31
	s_lshl_b64 s[34:35], s[34:35], 7
	s_add_u32 vcc_lo, vcc_lo, s34
	s_addc_u32 vcc_hi, vcc_hi, s35
	s_add_i32 s39, s39, s29
	v_lshl_add_u64 v[160:161], vcc, 0, v[134:135]
	s_mov_b32 m0, s39
	ds_read_b128 v[192:195], v166 offset:49152
	ds_read_b128 v[196:199], v166 offset:50176
	ds_read_b128 v[200:203], v166 offset:51200
	ds_read_b128 v[204:207], v166 offset:52224
	ds_read_b128 v[208:211], v166 offset:53248
	ds_read_b128 v[212:215], v166 offset:54272
	ds_read_b128 v[216:219], v166 offset:55296
	ds_read_b128 v[220:223], v166 offset:56320
	global_load_lds_dwordx4 v[160:161], off
	s_add_i32 m0, s39, 0x2000
	v_lshl_add_u64 v[160:161], vcc, 0, v[138:139]
	s_add_u32 vcc_lo, vcc_lo, 0x40000
	s_addc_u32 vcc_hi, vcc_hi, 0
	s_add_i32 s39, s57, s29
	global_load_lds_dwordx4 v[160:161], off
	v_lshl_add_u64 v[160:161], vcc, 0, v[134:135]
	s_mov_b32 m0, s39
	s_nop 0
	global_load_lds_dwordx4 v[160:161], off
	s_add_i32 m0, s39, 0x2000
	s_and_b64 s[6:7], s[6:7], exec
	s_cselect_b32 s6, s60, s80
	s_cselect_b32 s7, s61, s81
	s_add_u32 s6, s6, s34
	v_lshl_add_u64 v[160:161], vcc, 0, v[138:139]
	s_addc_u32 s7, s7, s35
	global_load_lds_dwordx4 v[160:161], off
	v_lshl_add_u64 v[160:161], s[6:7], 0, v[132:133]
	s_mov_b32 m0, s93
	s_nop 0
	global_load_lds_dwordx4 v[160:161], off
	v_lshl_add_u64 v[160:161], s[6:7], 0, v[136:137]
	s_mov_b32 m0, s94
	s_nop 0
	global_load_lds_dwordx4 v[160:161], off
	s_waitcnt vmcnt(8)
	s_waitcnt lgkmcnt(0)
	s_barrier
	s_setprio 1
	s_waitcnt lgkmcnt(0)
	v_mfma_f32_16x16x32_bf16 v[60:63], v[152:155], v[192:195], v[60:63]
	v_mfma_f32_16x16x32_bf16 v[56:59], v[168:171], v[192:195], v[56:59]
	v_mfma_f32_16x16x32_bf16 v[44:47], v[152:155], v[200:203], v[44:47]
	v_mfma_f32_16x16x32_bf16 v[40:43], v[168:171], v[200:203], v[40:43]
	v_mfma_f32_16x16x32_bf16 v[28:31], v[152:155], v[208:211], v[28:31]
	v_mfma_f32_16x16x32_bf16 v[16:19], v[168:171], v[208:211], v[16:19]
	v_mfma_f32_16x16x32_bf16 v[8:11], v[152:155], v[216:219], v[8:11]
	v_mfma_f32_16x16x32_bf16 v[0:3], v[168:171], v[216:219], v[0:3]
	v_mfma_f32_16x16x32_bf16 v[60:63], v[156:159], v[196:199], v[60:63]
	v_mfma_f32_16x16x32_bf16 v[56:59], v[172:175], v[196:199], v[56:59]
	v_mfma_f32_16x16x32_bf16 v[44:47], v[156:159], v[204:207], v[44:47]
	v_mfma_f32_16x16x32_bf16 v[40:43], v[172:175], v[204:207], v[40:43]
	v_mfma_f32_16x16x32_bf16 v[28:31], v[156:159], v[212:215], v[28:31]
	v_mfma_f32_16x16x32_bf16 v[16:19], v[172:175], v[212:215], v[16:19]
	v_mfma_f32_16x16x32_bf16 v[8:11], v[156:159], v[220:223], v[8:11]
	v_mfma_f32_16x16x32_bf16 v[0:3], v[172:175], v[220:223], v[0:3]
	v_mfma_f32_16x16x32_bf16 v[52:55], v[176:179], v[192:195], v[52:55]
	v_mfma_f32_16x16x32_bf16 v[48:51], v[184:187], v[192:195], v[48:51]
	v_mfma_f32_16x16x32_bf16 v[36:39], v[176:179], v[200:203], v[36:39]
	v_mfma_f32_16x16x32_bf16 v[32:35], v[184:187], v[200:203], v[32:35]
	v_mfma_f32_16x16x32_bf16 v[24:27], v[176:179], v[208:211], v[24:27]
	v_mfma_f32_16x16x32_bf16 v[20:23], v[184:187], v[208:211], v[20:23]
	v_mfma_f32_16x16x32_bf16 v[12:15], v[176:179], v[216:219], v[12:15]
	v_mfma_f32_16x16x32_bf16 v[4:7], v[184:187], v[216:219], v[4:7]
	v_mfma_f32_16x16x32_bf16 v[52:55], v[180:183], v[196:199], v[52:55]
	v_mfma_f32_16x16x32_bf16 v[48:51], v[188:191], v[196:199], v[48:51]
	v_mfma_f32_16x16x32_bf16 v[36:39], v[180:183], v[204:207], v[36:39]
	v_mfma_f32_16x16x32_bf16 v[32:35], v[188:191], v[204:207], v[32:35]
	v_mfma_f32_16x16x32_bf16 v[24:27], v[180:183], v[212:215], v[24:27]
	v_mfma_f32_16x16x32_bf16 v[20:23], v[188:191], v[212:215], v[20:23]
	v_mfma_f32_16x16x32_bf16 v[12:15], v[180:183], v[220:223], v[12:15]
	v_mfma_f32_16x16x32_bf16 v[4:7], v[188:191], v[220:223], v[4:7]
	s_setprio 0
	s_barrier
	v_lshl_add_u64 v[128:129], v[128:129], 0, s[30:31]
	v_lshl_add_u64 v[130:131], v[130:131], 0, s[30:31]
	s_add_i32 s0, s0, 2
	s_and_b64 vcc, exec, s[36:37]
	s_cbranch_vccnz .LBB0_124
	s_andn2_b64 vcc, exec, s[10:11]
	s_cbranch_vccnz .LBB0_127
	s_barrier

.LBB0_517:
	ds_read_b128 v[76:79], v207
	ds_read_b128 v[88:91], v207 offset:1024
	ds_read_b128 v[92:95], v207 offset:2048
	ds_read_b128 v[144:147], v207 offset:3072
	ds_read_b128 v[148:151], v211
	ds_read_b128 v[152:155], v211 offset:1024
	ds_read_b128 v[156:159], v211 offset:2048
	ds_read_b128 v[160:163], v211 offset:3072
	s_add_i32 m0, s60, 0xc000
	ds_read_b128 v[198:201], v212
	ds_read_b128 v[214:217], v212 offset:1024
	ds_read_b128 v[218:221], v212 offset:2048
	ds_read_b128 v[222:225], v212 offset:3072
	ds_read_b128 v[226:229], v212 offset:4096
	ds_read_b128 v[230:233], v212 offset:5120
	ds_read_b128 v[234:237], v212 offset:6144
	ds_read_b128 v[238:241], v212 offset:7168
	global_load_lds_dwordx4 v[72:73], off
	s_add_i32 m0, s60, 0xe000
	s_nop 0
	global_load_lds_dwordx4 v[74:75], off
	s_waitcnt vmcnt(8)
	s_waitcnt lgkmcnt(0)
	s_barrier
	s_setprio 1
	s_waitcnt lgkmcnt(0)
	v_mfma_f32_16x16x32_bf16 v[140:143], v[76:79], v[198:201], v[140:143]
	v_mfma_f32_16x16x32_bf16 v[136:139], v[92:95], v[198:201], v[136:139]
	v_mfma_f32_16x16x32_bf16 v[124:127], v[76:79], v[218:221], v[124:127]
	v_mfma_f32_16x16x32_bf16 v[120:123], v[92:95], v[218:221], v[120:123]
	v_mfma_f32_16x16x32_bf16 v[108:111], v[76:79], v[226:229], v[108:111]
	v_mfma_f32_16x16x32_bf16 v[104:107], v[92:95], v[226:229], v[104:107]
	v_mfma_f32_16x16x32_bf16 v[84:87], v[76:79], v[234:237], v[84:87]
	v_mfma_f32_16x16x32_bf16 v[80:83], v[92:95], v[234:237], v[80:83]
	v_mfma_f32_16x16x32_bf16 v[140:143], v[88:91], v[214:217], v[140:143]
	v_mfma_f32_16x16x32_bf16 v[136:139], v[144:147], v[214:217], v[136:139]
	v_mfma_f32_16x16x32_bf16 v[124:127], v[88:91], v[222:225], v[124:127]
	v_mfma_f32_16x16x32_bf16 v[120:123], v[144:147], v[222:225], v[120:123]
	v_mfma_f32_16x16x32_bf16 v[108:111], v[88:91], v[230:233], v[108:111]
	v_mfma_f32_16x16x32_bf16 v[104:107], v[144:147], v[230:233], v[104:107]
	v_mfma_f32_16x16x32_bf16 v[84:87], v[88:91], v[238:241], v[84:87]
	v_mfma_f32_16x16x32_bf16 v[80:83], v[144:147], v[238:241], v[80:83]
	v_mfma_f32_16x16x32_bf16 v[132:135], v[148:151], v[198:201], v[132:135]
	v_mfma_f32_16x16x32_bf16 v[128:131], v[156:159], v[198:201], v[128:131]
	v_mfma_f32_16x16x32_bf16 v[116:119], v[148:151], v[218:221], v[116:119]
	v_mfma_f32_16x16x32_bf16 v[112:115], v[156:159], v[218:221], v[112:115]
	v_mfma_f32_16x16x32_bf16 v[100:103], v[148:151], v[226:229], v[100:103]
	v_mfma_f32_16x16x32_bf16 v[96:99], v[156:159], v[226:229], v[96:99]
	v_mfma_f32_16x16x32_bf16 v[68:71], v[148:151], v[234:237], v[68:71]
	v_mfma_f32_16x16x32_bf16 v[64:67], v[156:159], v[234:237], v[64:67]
	v_mfma_f32_16x16x32_bf16 v[132:135], v[152:155], v[214:217], v[132:135]
	v_mfma_f32_16x16x32_bf16 v[128:131], v[160:163], v[214:217], v[128:131]
	v_mfma_f32_16x16x32_bf16 v[116:119], v[152:155], v[222:225], v[116:119]
	v_mfma_f32_16x16x32_bf16 v[112:115], v[160:163], v[222:225], v[112:115]
	v_mfma_f32_16x16x32_bf16 v[100:103], v[152:155], v[230:233], v[100:103]
	v_mfma_f32_16x16x32_bf16 v[96:99], v[160:163], v[230:233], v[96:99]
	v_mfma_f32_16x16x32_bf16 v[68:71], v[152:155], v[238:241], v[68:71]
	v_mfma_f32_16x16x32_bf16 v[64:67], v[160:163], v[238:241], v[64:67]
	s_setprio 0
	s_barrier
	s_cmp_gt_u32 s35, 13
	s_cselect_b64 s[76:77], -1, 0
	s_and_b64 s[36:37], s[76:77], exec
	v_sub_co_u32_e64 v182, s[36:37], s35, 14
	s_nop 0
	v_readfirstlane_b32 s80, v182
	s_cselect_b32 s39, s43, s47
	s_cselect_b32 s75, s42, s46
	s_add_i32 s81, s80, 16
	s_and_b64 s[78:79], s[76:77], exec
	s_cselect_b32 s78, s80, s81
	s_ashr_i32 s79, s78, 31
	s_lshl_b64 s[78:79], s[78:79], 7
	s_add_u32 s80, s75, s78
	s_addc_u32 s81, s39, s79
	s_add_i32 s39, s73, s59
	v_lshl_add_u64 v[182:183], s[80:81], 0, v[166:167]
	s_mov_b32 m0, s39
	ds_read_b128 v[198:201], v212 offset:16384
	ds_read_b128 v[214:217], v212 offset:17408
	ds_read_b128 v[218:221], v212 offset:18432
	ds_read_b128 v[222:225], v212 offset:19456
	ds_read_b128 v[226:229], v212 offset:20480
	ds_read_b128 v[230:233], v212 offset:21504
	ds_read_b128 v[234:237], v212 offset:22528
	ds_read_b128 v[238:241], v212 offset:23552
	global_load_lds_dwordx4 v[182:183], off
	s_add_i32 m0, s39, 0x2000
	v_lshl_add_u64 v[182:183], s[80:81], 0, v[170:171]
	s_add_u32 s80, s80, 0x40000
	s_addc_u32 s81, s81, 0
	s_add_i32 s39, s74, s59
	global_load_lds_dwordx4 v[182:183], off
	v_lshl_add_u64 v[182:183], s[80:81], 0, v[166:167]
	s_mov_b32 m0, s39
	s_nop 0
	global_load_lds_dwordx4 v[182:183], off
	s_add_i32 m0, s39, 0x2000
	s_and_b64 s[76:77], s[76:77], exec
	s_cselect_b32 s75, s40, s48
	s_cselect_b32 s39, s41, s49
	s_add_u32 s76, s75, s78
	v_lshl_add_u64 v[182:183], s[80:81], 0, v[170:171]
	s_addc_u32 s77, s39, s79
	global_load_lds_dwordx4 v[182:183], off
	v_lshl_add_u64 v[182:183], s[76:77], 0, v[164:165]
	s_mov_b32 m0, s60
	s_nop 0
	global_load_lds_dwordx4 v[182:183], off
	v_lshl_add_u64 v[182:183], s[76:77], 0, v[168:169]
	s_mov_b32 m0, s61
	s_nop 0
	global_load_lds_dwordx4 v[182:183], off
	s_waitcnt vmcnt(8)
	s_waitcnt lgkmcnt(0)
	s_barrier
	s_setprio 1
	s_waitcnt lgkmcnt(0)
	v_mfma_f32_16x16x32_bf16 v[60:63], v[76:79], v[198:201], v[60:63]
	v_mfma_f32_16x16x32_bf16 v[56:59], v[92:95], v[198:201], v[56:59]
	v_mfma_f32_16x16x32_bf16 v[44:47], v[76:79], v[218:221], v[44:47]
	v_mfma_f32_16x16x32_bf16 v[40:43], v[92:95], v[218:221], v[40:43]
	v_mfma_f32_16x16x32_bf16 v[28:31], v[76:79], v[226:229], v[28:31]
	v_mfma_f32_16x16x32_bf16 v[16:19], v[92:95], v[226:229], v[16:19]
	v_mfma_f32_16x16x32_bf16 v[4:7], v[76:79], v[234:237], v[4:7]
	v_mfma_f32_16x16x32_bf16 v[0:3], v[92:95], v[234:237], v[0:3]
	v_mfma_f32_16x16x32_bf16 v[60:63], v[88:91], v[214:217], v[60:63]
	v_mfma_f32_16x16x32_bf16 v[56:59], v[144:147], v[214:217], v[56:59]
	v_mfma_f32_16x16x32_bf16 v[44:47], v[88:91], v[222:225], v[44:47]
	v_mfma_f32_16x16x32_bf16 v[40:43], v[144:147], v[222:225], v[40:43]
	v_mfma_f32_16x16x32_bf16 v[28:31], v[88:91], v[230:233], v[28:31]
	v_mfma_f32_16x16x32_bf16 v[16:19], v[144:147], v[230:233], v[16:19]
	v_mfma_f32_16x16x32_bf16 v[4:7], v[88:91], v[238:241], v[4:7]
	v_mfma_f32_16x16x32_bf16 v[0:3], v[144:147], v[238:241], v[0:3]
	v_mfma_f32_16x16x32_bf16 v[52:55], v[148:151], v[198:201], v[52:55]
	v_mfma_f32_16x16x32_bf16 v[48:51], v[156:159], v[198:201], v[48:51]
	v_mfma_f32_16x16x32_bf16 v[36:39], v[148:151], v[218:221], v[36:39]
	v_mfma_f32_16x16x32_bf16 v[32:35], v[156:159], v[218:221], v[32:35]
	v_mfma_f32_16x16x32_bf16 v[20:23], v[148:151], v[226:229], v[20:23]
	v_mfma_f32_16x16x32_bf16 v[24:27], v[156:159], v[226:229], v[24:27]
	v_mfma_f32_16x16x32_bf16 v[8:11], v[148:151], v[234:237], v[8:11]
	v_mfma_f32_16x16x32_bf16 v[12:15], v[156:159], v[234:237], v[12:15]
	v_mfma_f32_16x16x32_bf16 v[52:55], v[152:155], v[214:217], v[52:55]
	v_mfma_f32_16x16x32_bf16 v[48:51], v[160:163], v[214:217], v[48:51]
	v_mfma_f32_16x16x32_bf16 v[36:39], v[152:155], v[222:225], v[36:39]
	v_mfma_f32_16x16x32_bf16 v[32:35], v[160:163], v[222:225], v[32:35]
	v_mfma_f32_16x16x32_bf16 v[20:23], v[152:155], v[230:233], v[20:23]
	v_mfma_f32_16x16x32_bf16 v[24:27], v[160:163], v[230:233], v[24:27]
	v_mfma_f32_16x16x32_bf16 v[8:11], v[152:155], v[238:241], v[8:11]
	v_mfma_f32_16x16x32_bf16 v[12:15], v[160:163], v[238:241], v[12:15]
	s_setprio 0
	s_barrier
	s_add_i32 s39, 0, 0x18000
	s_add_i32 s75, 0, 0x1c000
	v_add_u32_e32 v144, s39, v189
	v_add_u32_e32 v160, s75, v189
	ds_read_b128 v[76:79], v144
	ds_read_b128 v[88:91], v144 offset:1024
	ds_read_b128 v[92:95], v144 offset:2048
	ds_read_b128 v[144:147], v144 offset:3072
	ds_read_b128 v[148:151], v160
	ds_read_b128 v[152:155], v160 offset:1024
	ds_read_b128 v[156:159], v160 offset:2048
	ds_read_b128 v[160:163], v160 offset:3072
	s_add_u32 s76, s76, 0x40000
	s_addc_u32 s77, s77, 0
	s_mov_b32 m0, s62
	v_lshl_add_u64 v[182:183], s[76:77], 0, v[164:165]
	ds_read_b128 v[198:201], v212 offset:32768
	ds_read_b128 v[214:217], v212 offset:33792
	ds_read_b128 v[218:221], v212 offset:34816
	ds_read_b128 v[222:225], v212 offset:35840
	ds_read_b128 v[226:229], v212 offset:36864
	ds_read_b128 v[230:233], v212 offset:37888
	ds_read_b128 v[234:237], v212 offset:38912
	ds_read_b128 v[238:241], v212 offset:39936
	global_load_lds_dwordx4 v[182:183], off
	v_lshl_add_u64 v[182:183], s[76:77], 0, v[168:169]
	s_mov_b32 m0, s63
	s_nop 0
	global_load_lds_dwordx4 v[182:183], off
	s_waitcnt vmcnt(8)
	s_waitcnt lgkmcnt(0)
	s_barrier
	s_setprio 1
	s_waitcnt lgkmcnt(0)
	v_mfma_f32_16x16x32_bf16 v[140:143], v[76:79], v[198:201], v[140:143]
	v_mfma_f32_16x16x32_bf16 v[136:139], v[92:95], v[198:201], v[136:139]
	v_mfma_f32_16x16x32_bf16 v[124:127], v[76:79], v[218:221], v[124:127]
	v_mfma_f32_16x16x32_bf16 v[120:123], v[92:95], v[218:221], v[120:123]
	v_mfma_f32_16x16x32_bf16 v[108:111], v[76:79], v[226:229], v[108:111]
	v_mfma_f32_16x16x32_bf16 v[104:107], v[92:95], v[226:229], v[104:107]
	v_mfma_f32_16x16x32_bf16 v[84:87], v[76:79], v[234:237], v[84:87]
	v_mfma_f32_16x16x32_bf16 v[80:83], v[92:95], v[234:237], v[80:83]
	v_mfma_f32_16x16x32_bf16 v[140:143], v[88:91], v[214:217], v[140:143]
	v_mfma_f32_16x16x32_bf16 v[136:139], v[144:147], v[214:217], v[136:139]
	v_mfma_f32_16x16x32_bf16 v[124:127], v[88:91], v[222:225], v[124:127]
	v_mfma_f32_16x16x32_bf16 v[120:123], v[144:147], v[222:225], v[120:123]
	v_mfma_f32_16x16x32_bf16 v[108:111], v[88:91], v[230:233], v[108:111]
	v_mfma_f32_16x16x32_bf16 v[104:107], v[144:147], v[230:233], v[104:107]
	v_mfma_f32_16x16x32_bf16 v[84:87], v[88:91], v[238:241], v[84:87]
	v_mfma_f32_16x16x32_bf16 v[80:83], v[144:147], v[238:241], v[80:83]
	v_mfma_f32_16x16x32_bf16 v[132:135], v[148:151], v[198:201], v[132:135]
	v_mfma_f32_16x16x32_bf16 v[128:131], v[156:159], v[198:201], v[128:131]
	v_mfma_f32_16x16x32_bf16 v[116:119], v[148:151], v[218:221], v[116:119]
	v_mfma_f32_16x16x32_bf16 v[112:115], v[156:159], v[218:221], v[112:115]
	v_mfma_f32_16x16x32_bf16 v[100:103], v[148:151], v[226:229], v[100:103]
	v_mfma_f32_16x16x32_bf16 v[96:99], v[156:159], v[226:229], v[96:99]
	v_mfma_f32_16x16x32_bf16 v[68:71], v[148:151], v[234:237], v[68:71]
	v_mfma_f32_16x16x32_bf16 v[64:67], v[156:159], v[234:237], v[64:67]
	v_mfma_f32_16x16x32_bf16 v[132:135], v[152:155], v[214:217], v[132:135]
	v_mfma_f32_16x16x32_bf16 v[128:131], v[160:163], v[214:217], v[128:131]
	v_mfma_f32_16x16x32_bf16 v[116:119], v[152:155], v[222:225], v[116:119]
	v_mfma_f32_16x16x32_bf16 v[112:115], v[160:163], v[222:225], v[112:115]
	v_mfma_f32_16x16x32_bf16 v[100:103], v[152:155], v[230:233], v[100:103]
	v_mfma_f32_16x16x32_bf16 v[96:99], v[160:163], v[230:233], v[96:99]
	v_mfma_f32_16x16x32_bf16 v[68:71], v[152:155], v[238:241], v[68:71]
	v_mfma_f32_16x16x32_bf16 v[64:67], v[160:163], v[238:241], v[64:67]
	s_setprio 0
	s_barrier
	s_cmp_gt_u32 s35, 12
	s_cselect_b64 s[76:77], -1, 0
	s_and_b64 s[78:79], s[76:77], exec
	s_cselect_b32 s78, -13, 3
	s_cselect_b32 s81, s43, s47
	s_cselect_b32 s80, s42, s46
	s_add_i32 s78, s78, s35
	s_ashr_i32 s79, s78, 31
	s_lshl_b64 s[78:79], s[78:79], 7
	s_add_u32 s80, s80, s78
	s_addc_u32 s81, s81, s79
	s_add_i32 s39, s39, s59
	v_lshl_add_u64 v[182:183], s[80:81], 0, v[166:167]
	s_mov_b32 m0, s39
	ds_read_b128 v[198:201], v212 offset:49152
	ds_read_b128 v[214:217], v212 offset:50176
	ds_read_b128 v[218:221], v212 offset:51200
	ds_read_b128 v[222:225], v212 offset:52224
	ds_read_b128 v[226:229], v212 offset:53248
	ds_read_b128 v[230:233], v212 offset:54272
	ds_read_b128 v[234:237], v212 offset:55296
	ds_read_b128 v[238:241], v212 offset:56320
	global_load_lds_dwordx4 v[182:183], off
	s_add_i32 m0, s39, 0x2000
	v_lshl_add_u64 v[182:183], s[80:81], 0, v[170:171]
	s_add_u32 s80, s80, 0x40000
	s_addc_u32 s81, s81, 0
	s_add_i32 s39, s75, s59
	global_load_lds_dwordx4 v[182:183], off
	v_lshl_add_u64 v[182:183], s[80:81], 0, v[166:167]
	s_mov_b32 m0, s39
	s_nop 0
	global_load_lds_dwordx4 v[182:183], off
	s_add_i32 m0, s39, 0x2000
	s_and_b64 s[76:77], s[76:77], exec
	s_cselect_b32 s75, s40, s48
	s_cselect_b32 s39, s41, s49
	s_add_u32 s76, s75, s78
	v_lshl_add_u64 v[182:183], s[80:81], 0, v[170:171]
	s_addc_u32 s77, s39, s79
	global_load_lds_dwordx4 v[182:183], off
	v_lshl_add_u64 v[182:183], s[76:77], 0, v[164:165]
	s_mov_b32 m0, s65
	s_nop 0
	global_load_lds_dwordx4 v[182:183], off
	v_lshl_add_u64 v[182:183], s[76:77], 0, v[168:169]
	s_mov_b32 m0, s66
	s_nop 0
	global_load_lds_dwordx4 v[182:183], off
	s_waitcnt vmcnt(8)
	s_waitcnt lgkmcnt(0)
	s_barrier
	s_setprio 1
	s_waitcnt lgkmcnt(0)
	v_mfma_f32_16x16x32_bf16 v[60:63], v[76:79], v[198:201], v[60:63]
	v_mfma_f32_16x16x32_bf16 v[56:59], v[92:95], v[198:201], v[56:59]
	v_mfma_f32_16x16x32_bf16 v[44:47], v[76:79], v[218:221], v[44:47]
	v_mfma_f32_16x16x32_bf16 v[40:43], v[92:95], v[218:221], v[40:43]
	v_mfma_f32_16x16x32_bf16 v[28:31], v[76:79], v[226:229], v[28:31]
	v_mfma_f32_16x16x32_bf16 v[16:19], v[92:95], v[226:229], v[16:19]
	v_mfma_f32_16x16x32_bf16 v[4:7], v[76:79], v[234:237], v[4:7]
	v_mfma_f32_16x16x32_bf16 v[0:3], v[92:95], v[234:237], v[0:3]
	v_mfma_f32_16x16x32_bf16 v[60:63], v[88:91], v[214:217], v[60:63]
	v_mfma_f32_16x16x32_bf16 v[56:59], v[144:147], v[214:217], v[56:59]
	v_mfma_f32_16x16x32_bf16 v[44:47], v[88:91], v[222:225], v[44:47]
	v_mfma_f32_16x16x32_bf16 v[40:43], v[144:147], v[222:225], v[40:43]
	v_mfma_f32_16x16x32_bf16 v[28:31], v[88:91], v[230:233], v[28:31]
	v_mfma_f32_16x16x32_bf16 v[16:19], v[144:147], v[230:233], v[16:19]
	v_mfma_f32_16x16x32_bf16 v[4:7], v[88:91], v[238:241], v[4:7]
	v_mfma_f32_16x16x32_bf16 v[0:3], v[144:147], v[238:241], v[0:3]
	v_mfma_f32_16x16x32_bf16 v[52:55], v[148:151], v[198:201], v[52:55]
	v_mfma_f32_16x16x32_bf16 v[48:51], v[156:159], v[198:201], v[48:51]
	v_mfma_f32_16x16x32_bf16 v[36:39], v[148:151], v[218:221], v[36:39]
	v_mfma_f32_16x16x32_bf16 v[32:35], v[156:159], v[218:221], v[32:35]
	v_mfma_f32_16x16x32_bf16 v[20:23], v[148:151], v[226:229], v[20:23]
	v_mfma_f32_16x16x32_bf16 v[24:27], v[156:159], v[226:229], v[24:27]
	v_mfma_f32_16x16x32_bf16 v[8:11], v[148:151], v[234:237], v[8:11]
	v_mfma_f32_16x16x32_bf16 v[12:15], v[156:159], v[234:237], v[12:15]
	v_mfma_f32_16x16x32_bf16 v[52:55], v[152:155], v[214:217], v[52:55]
	v_mfma_f32_16x16x32_bf16 v[48:51], v[160:163], v[214:217], v[48:51]
	v_mfma_f32_16x16x32_bf16 v[36:39], v[152:155], v[222:225], v[36:39]
	v_mfma_f32_16x16x32_bf16 v[32:35], v[160:163], v[222:225], v[32:35]
	v_mfma_f32_16x16x32_bf16 v[20:23], v[152:155], v[230:233], v[20:23]
	v_mfma_f32_16x16x32_bf16 v[24:27], v[160:163], v[230:233], v[24:27]
	v_mfma_f32_16x16x32_bf16 v[8:11], v[152:155], v[238:241], v[8:11]
	v_mfma_f32_16x16x32_bf16 v[12:15], v[160:163], v[238:241], v[12:15]
	s_setprio 0
	s_barrier
	v_lshl_add_u64 v[72:73], v[72:73], 0, s[30:31]
	v_lshl_add_u64 v[74:75], v[74:75], 0, s[30:31]
	s_add_i32 s35, s35, 2
	s_and_b64 vcc, exec, s[36:37]
	s_cbranch_vccnz .LBB0_517
	s_andn2_b64 vcc, exec, s[26:27]
	s_cbranch_vccnz .LBB0_520
	s_barrier

.LBB0_594:
	ds_read_b128 v[24:27], v186
	ds_read_b128 v[28:31], v186 offset:1024
	ds_read_b128 v[16:19], v186 offset:2048
	ds_read_b128 v[20:23], v186 offset:3072
	ds_read_b128 v[8:11], v187
	ds_read_b128 v[12:15], v187 offset:1024
	ds_read_b128 v[0:3], v187 offset:2048
	ds_read_b128 v[4:7], v187 offset:3072
	s_add_i32 m0, s31, 0xc000
	ds_read_b128 v[192:195], v188
	ds_read_b128 v[196:199], v188 offset:1024
	ds_read_b128 v[200:203], v188 offset:2048
	ds_read_b128 v[204:207], v188 offset:3072
	ds_read_b128 v[208:211], v188 offset:4096
	ds_read_b128 v[212:215], v188 offset:5120
	ds_read_b128 v[224:227], v188 offset:6144
	ds_read_b128 v[228:231], v188 offset:7168
	global_load_lds_dwordx4 v[178:179], off
	s_add_i32 m0, s31, 0xe000
	s_nop 0
	global_load_lds_dwordx4 v[180:181], off
	s_waitcnt vmcnt(8)
	s_waitcnt lgkmcnt(0)
	s_barrier
	s_setprio 1
	s_waitcnt lgkmcnt(0)
	v_mfma_f32_16x16x128_f8f6f4 v[156:159], v[24:31], v[192:199], v[156:159]
	v_mfma_f32_16x16x128_f8f6f4 v[148:151], v[16:23], v[192:199], v[148:151]
	v_mfma_f32_16x16x128_f8f6f4 v[140:143], v[24:31], v[200:207], v[140:143]
	v_mfma_f32_16x16x128_f8f6f4 v[132:135], v[16:23], v[200:207], v[132:135]
	v_mfma_f32_16x16x128_f8f6f4 v[124:127], v[24:31], v[208:215], v[124:127]
	v_mfma_f32_16x16x128_f8f6f4 v[116:119], v[16:23], v[208:215], v[116:119]
	v_mfma_f32_16x16x128_f8f6f4 v[108:111], v[24:31], v[224:231], v[108:111]
	v_mfma_f32_16x16x128_f8f6f4 v[100:103], v[16:23], v[224:231], v[100:103]
	v_mfma_f32_16x16x128_f8f6f4 v[152:155], v[8:15], v[192:199], v[152:155]
	v_mfma_f32_16x16x128_f8f6f4 v[144:147], v[0:7], v[192:199], v[144:147]
	v_mfma_f32_16x16x128_f8f6f4 v[136:139], v[8:15], v[200:207], v[136:139]
	v_mfma_f32_16x16x128_f8f6f4 v[128:131], v[0:7], v[200:207], v[128:131]
	v_mfma_f32_16x16x128_f8f6f4 v[120:123], v[8:15], v[208:215], v[120:123]
	v_mfma_f32_16x16x128_f8f6f4 v[112:115], v[0:7], v[208:215], v[112:115]
	v_mfma_f32_16x16x128_f8f6f4 v[104:107], v[8:15], v[224:231], v[104:107]
	v_mfma_f32_16x16x128_f8f6f4 v[96:99], v[0:7], v[224:231], v[96:99]
	s_setprio 0
	s_barrier
	s_cmp_gt_u32 s15, 5
	s_cselect_b64 s[36:37], -1, 0
	s_and_b64 s[40:41], s[36:37], exec
	v_sub_co_u32_e64 v216, s[40:41], s15, 6
	s_nop 0
	v_readfirstlane_b32 s73, v216
	s_cselect_b32 s17, s27, s39
	s_cselect_b32 s67, s26, s38
	s_add_i32 s76, s73, 8
	s_and_b64 s[74:75], s[36:37], exec
	s_cselect_b32 s74, s73, s76
	s_ashr_i32 s75, s74, 31
	s_lshl_b64 s[74:75], s[74:75], 7
	s_add_u32 s76, s67, s74
	s_addc_u32 s77, s17, s75
	s_add_i32 s17, s61, s29
	s_mov_b32 m0, s17
	ds_read_b128 v[192:195], v188 offset:16384
	ds_read_b128 v[196:199], v188 offset:17408
	ds_read_b128 v[200:203], v188 offset:18432
	ds_read_b128 v[204:207], v188 offset:19456
	ds_read_b128 v[208:211], v188 offset:20480
	ds_read_b128 v[212:215], v188 offset:21504
	ds_read_b128 v[224:227], v188 offset:22528
	ds_read_b128 v[228:231], v188 offset:23552
	global_load_lds_dwordx4 v162, s[76:77]
	s_add_i32 m0, s17, 0x2000
	s_add_i32 s17, s62, s29
	global_load_lds_dwordx4 v166, s[76:77]
	s_add_u32 s76, s76, 0x20000
	s_addc_u32 s77, s77, 0
	s_mov_b32 m0, s17
	s_nop 0
	global_load_lds_dwordx4 v162, s[76:77]
	s_add_i32 m0, s17, 0x2000
	s_and_b64 s[36:37], s[36:37], exec
	s_cselect_b32 s36, s22, s34
	s_cselect_b32 s17, s23, s35
	s_add_u32 s36, s36, s74
	s_addc_u32 s37, s17, s75
	global_load_lds_dwordx4 v166, s[76:77]
	s_mov_b32 m0, s31
	s_nop 0
	global_load_lds_dwordx4 v160, s[36:37]
	s_mov_b32 m0, s49
	s_nop 0
	global_load_lds_dwordx4 v164, s[36:37]
	s_waitcnt vmcnt(8)
	s_waitcnt lgkmcnt(0)
	s_barrier
	s_setprio 1
	s_waitcnt lgkmcnt(0)
	v_mfma_f32_16x16x128_f8f6f4 v[92:95], v[24:31], v[192:199], v[92:95]
	v_mfma_f32_16x16x128_f8f6f4 v[84:87], v[16:23], v[192:199], v[84:87]
	v_mfma_f32_16x16x128_f8f6f4 v[76:79], v[24:31], v[200:207], v[76:79]
	v_mfma_f32_16x16x128_f8f6f4 v[64:67], v[16:23], v[200:207], v[64:67]
	v_mfma_f32_16x16x128_f8f6f4 v[52:55], v[24:31], v[208:215], v[52:55]
	v_mfma_f32_16x16x128_f8f6f4 v[44:47], v[16:23], v[208:215], v[44:47]
	v_mfma_f32_16x16x128_f8f6f4 v[36:39], v[24:31], v[224:231], v[36:39]
	v_mfma_f32_16x16x128_f8f6f4 v[32:35], v[16:23], v[224:231], v[32:35]
	v_mfma_f32_16x16x128_f8f6f4 v[88:91], v[8:15], v[192:199], v[88:91]
	v_mfma_f32_16x16x128_f8f6f4 v[80:83], v[0:7], v[192:199], v[80:83]
	v_mfma_f32_16x16x128_f8f6f4 v[68:71], v[8:15], v[200:207], v[68:71]
	v_mfma_f32_16x16x128_f8f6f4 v[56:59], v[0:7], v[200:207], v[56:59]
	v_mfma_f32_16x16x128_f8f6f4 v[72:75], v[8:15], v[208:215], v[72:75]
	v_mfma_f32_16x16x128_f8f6f4 v[60:63], v[0:7], v[208:215], v[60:63]
	v_mfma_f32_16x16x128_f8f6f4 v[48:51], v[8:15], v[224:231], v[48:51]
	v_mfma_f32_16x16x128_f8f6f4 v[40:43], v[0:7], v[224:231], v[40:43]
	s_setprio 0
	s_barrier
	s_add_i32 s17, 0, 0x18000
	s_add_i32 s67, 0, 0x1c000
	v_add_u32_e32 v0, s17, v183
	v_add_u32_e32 v4, s67, v183
	ds_read_b128 v[24:27], v0
	ds_read_b128 v[28:31], v0 offset:1024
	ds_read_b128 v[16:19], v0 offset:2048
	ds_read_b128 v[20:23], v0 offset:3072
	ds_read_b128 v[8:11], v4
	ds_read_b128 v[12:15], v4 offset:1024
	ds_read_b128 v[0:3], v4 offset:2048
	ds_read_b128 v[4:7], v4 offset:3072
	s_add_u32 s36, s36, 0x20000
	s_addc_u32 s37, s37, 0
	s_mov_b32 m0, s50
	ds_read_b128 v[192:195], v188 offset:32768
	ds_read_b128 v[196:199], v188 offset:33792
	ds_read_b128 v[200:203], v188 offset:34816
	ds_read_b128 v[204:207], v188 offset:35840
	ds_read_b128 v[208:211], v188 offset:36864
	ds_read_b128 v[212:215], v188 offset:37888
	ds_read_b128 v[224:227], v188 offset:38912
	ds_read_b128 v[228:231], v188 offset:39936
	global_load_lds_dwordx4 v160, s[36:37]
	s_mov_b32 m0, s51
	s_nop 0
	global_load_lds_dwordx4 v164, s[36:37]
	s_waitcnt vmcnt(8)
	s_waitcnt lgkmcnt(0)
	s_barrier
	s_setprio 1
	s_waitcnt lgkmcnt(0)
	v_mfma_f32_16x16x128_f8f6f4 v[156:159], v[24:31], v[192:199], v[156:159]
	v_mfma_f32_16x16x128_f8f6f4 v[148:151], v[16:23], v[192:199], v[148:151]
	v_mfma_f32_16x16x128_f8f6f4 v[140:143], v[24:31], v[200:207], v[140:143]
	v_mfma_f32_16x16x128_f8f6f4 v[132:135], v[16:23], v[200:207], v[132:135]
	v_mfma_f32_16x16x128_f8f6f4 v[124:127], v[24:31], v[208:215], v[124:127]
	v_mfma_f32_16x16x128_f8f6f4 v[116:119], v[16:23], v[208:215], v[116:119]
	v_mfma_f32_16x16x128_f8f6f4 v[108:111], v[24:31], v[224:231], v[108:111]
	v_mfma_f32_16x16x128_f8f6f4 v[100:103], v[16:23], v[224:231], v[100:103]
	v_mfma_f32_16x16x128_f8f6f4 v[152:155], v[8:15], v[192:199], v[152:155]
	v_mfma_f32_16x16x128_f8f6f4 v[144:147], v[0:7], v[192:199], v[144:147]
	v_mfma_f32_16x16x128_f8f6f4 v[136:139], v[8:15], v[200:207], v[136:139]
	v_mfma_f32_16x16x128_f8f6f4 v[128:131], v[0:7], v[200:207], v[128:131]
	v_mfma_f32_16x16x128_f8f6f4 v[120:123], v[8:15], v[208:215], v[120:123]
	v_mfma_f32_16x16x128_f8f6f4 v[112:115], v[0:7], v[208:215], v[112:115]
	v_mfma_f32_16x16x128_f8f6f4 v[104:107], v[8:15], v[224:231], v[104:107]
	v_mfma_f32_16x16x128_f8f6f4 v[96:99], v[0:7], v[224:231], v[96:99]
	s_setprio 0
	s_barrier
	s_cmp_gt_u32 s15, 4
	s_cselect_b64 s[36:37], -1, 0
	s_and_b64 s[74:75], s[36:37], exec
	s_cselect_b32 s74, -5, 3
	s_cselect_b32 s73, s27, s39
	s_cselect_b32 s76, s26, s38
	s_add_i32 s74, s74, s15
	s_ashr_i32 s75, s74, 31
	s_lshl_b64 s[74:75], s[74:75], 7
	s_add_u32 s76, s76, s74
	s_addc_u32 s77, s73, s75
	s_add_i32 s17, s17, s29
	s_mov_b32 m0, s17
	ds_read_b128 v[192:195], v188 offset:49152
	ds_read_b128 v[196:199], v188 offset:50176
	ds_read_b128 v[200:203], v188 offset:51200
	ds_read_b128 v[204:207], v188 offset:52224
	ds_read_b128 v[208:211], v188 offset:53248
	ds_read_b128 v[212:215], v188 offset:54272
	ds_read_b128 v[224:227], v188 offset:55296
	ds_read_b128 v[228:231], v188 offset:56320
	global_load_lds_dwordx4 v162, s[76:77]
	s_add_i32 m0, s17, 0x2000
	s_add_i32 s17, s67, s29
	global_load_lds_dwordx4 v166, s[76:77]
	s_add_u32 s76, s76, 0x20000
	s_addc_u32 s77, s77, 0
	s_mov_b32 m0, s17
	s_nop 0
	global_load_lds_dwordx4 v162, s[76:77]
	s_add_i32 m0, s17, 0x2000
	s_and_b64 s[36:37], s[36:37], exec
	s_cselect_b32 s36, s22, s34
	s_cselect_b32 s17, s23, s35
	s_add_u32 s36, s36, s74
	s_addc_u32 s37, s17, s75
	global_load_lds_dwordx4 v166, s[76:77]
	s_mov_b32 m0, s56
	s_nop 0
	global_load_lds_dwordx4 v160, s[36:37]
	s_mov_b32 m0, s57
	s_nop 0
	global_load_lds_dwordx4 v164, s[36:37]
	s_waitcnt vmcnt(8)
	s_waitcnt lgkmcnt(0)
	s_barrier
	s_setprio 1
	s_waitcnt lgkmcnt(0)
	v_mfma_f32_16x16x128_f8f6f4 v[92:95], v[24:31], v[192:199], v[92:95]
	v_mfma_f32_16x16x128_f8f6f4 v[84:87], v[16:23], v[192:199], v[84:87]
	v_mfma_f32_16x16x128_f8f6f4 v[76:79], v[24:31], v[200:207], v[76:79]
	v_mfma_f32_16x16x128_f8f6f4 v[64:67], v[16:23], v[200:207], v[64:67]
	v_mfma_f32_16x16x128_f8f6f4 v[52:55], v[24:31], v[208:215], v[52:55]
	v_mfma_f32_16x16x128_f8f6f4 v[44:47], v[16:23], v[208:215], v[44:47]
	v_mfma_f32_16x16x128_f8f6f4 v[36:39], v[24:31], v[224:231], v[36:39]
	v_mfma_f32_16x16x128_f8f6f4 v[32:35], v[16:23], v[224:231], v[32:35]
	v_mfma_f32_16x16x128_f8f6f4 v[88:91], v[8:15], v[192:199], v[88:91]
	v_mfma_f32_16x16x128_f8f6f4 v[80:83], v[0:7], v[192:199], v[80:83]
	v_mfma_f32_16x16x128_f8f6f4 v[68:71], v[8:15], v[200:207], v[68:71]
	v_mfma_f32_16x16x128_f8f6f4 v[56:59], v[0:7], v[200:207], v[56:59]
	v_mfma_f32_16x16x128_f8f6f4 v[72:75], v[8:15], v[208:215], v[72:75]
	v_mfma_f32_16x16x128_f8f6f4 v[60:63], v[0:7], v[208:215], v[60:63]
	v_mfma_f32_16x16x128_f8f6f4 v[48:51], v[8:15], v[224:231], v[48:51]
	v_mfma_f32_16x16x128_f8f6f4 v[40:43], v[0:7], v[224:231], v[40:43]
	s_setprio 0
	s_barrier
	v_lshl_add_u64 v[178:179], v[178:179], 0, s[6:7]
	v_lshl_add_u64 v[180:181], v[180:181], 0, s[6:7]
	s_add_i32 s15, s15, 2
	s_and_b64 vcc, exec, s[40:41]
	s_cbranch_vccnz .LBB0_594
	s_andn2_b64 vcc, exec, s[12:13]
	s_cbranch_vccnz .LBB0_597
	s_barrier

.LBB0_673:
	ds_read_b128 v[24:27], v187
	ds_read_b128 v[28:31], v187 offset:1024
	ds_read_b128 v[16:19], v187 offset:2048
	ds_read_b128 v[20:23], v187 offset:3072
	s_waitcnt lgkmcnt(0)
	ds_read_b128 v[8:11], v188
	ds_read_b128 v[12:15], v188 offset:1024
	ds_read_b128 v[0:3], v188 offset:2048
	ds_read_b128 v[4:7], v188 offset:3072
	s_add_i32 m0, s49, 0xc000
	ds_read_b128 v[192:195], v189
	ds_read_b128 v[196:199], v189 offset:1024
	ds_read_b128 v[200:203], v189 offset:2048
	ds_read_b128 v[204:207], v189 offset:3072
	ds_read_b128 v[208:211], v189 offset:4096
	ds_read_b128 v[212:215], v189 offset:5120
	ds_read_b128 v[224:227], v189 offset:6144
	ds_read_b128 v[228:231], v189 offset:7168
	global_load_lds_dwordx4 v[178:179], off
	s_add_i32 m0, s49, 0xe000
	s_nop 0
	global_load_lds_dwordx4 v[180:181], off
	s_waitcnt vmcnt(8)
	s_waitcnt lgkmcnt(0)
	s_barrier
	s_setprio 1
	s_waitcnt lgkmcnt(0)
	v_mfma_f32_16x16x128_f8f6f4 v[156:159], v[24:31], v[192:199], v[156:159]
	v_mfma_f32_16x16x128_f8f6f4 v[152:155], v[16:23], v[192:199], v[152:155]
	v_mfma_f32_16x16x128_f8f6f4 v[140:143], v[24:31], v[200:207], v[140:143]
	v_mfma_f32_16x16x128_f8f6f4 v[136:139], v[16:23], v[200:207], v[136:139]
	v_mfma_f32_16x16x128_f8f6f4 v[124:127], v[24:31], v[208:215], v[124:127]
	v_mfma_f32_16x16x128_f8f6f4 v[120:123], v[16:23], v[208:215], v[120:123]
	v_mfma_f32_16x16x128_f8f6f4 v[108:111], v[24:31], v[224:231], v[108:111]
	v_mfma_f32_16x16x128_f8f6f4 v[104:107], v[16:23], v[224:231], v[104:107]
	v_mfma_f32_16x16x128_f8f6f4 v[148:151], v[8:15], v[192:199], v[148:151]
	v_mfma_f32_16x16x128_f8f6f4 v[144:147], v[0:7], v[192:199], v[144:147]
	v_mfma_f32_16x16x128_f8f6f4 v[132:135], v[8:15], v[200:207], v[132:135]
	v_mfma_f32_16x16x128_f8f6f4 v[128:131], v[0:7], v[200:207], v[128:131]
	v_mfma_f32_16x16x128_f8f6f4 v[116:119], v[8:15], v[208:215], v[116:119]
	v_mfma_f32_16x16x128_f8f6f4 v[112:115], v[0:7], v[208:215], v[112:115]
	v_mfma_f32_16x16x128_f8f6f4 v[100:103], v[8:15], v[224:231], v[100:103]
	v_mfma_f32_16x16x128_f8f6f4 v[96:99], v[0:7], v[224:231], v[96:99]
	s_setprio 0
	s_barrier
	s_add_i32 s73, s67, 2
	s_cmp_lt_u32 s67, 20
	s_cselect_b64 s[36:37], -1, 0
	s_and_b64 s[74:75], s[36:37], exec
	s_cselect_b32 s0, 0, 0xffffffea
	s_cselect_b32 s77, s29, s39
	s_cselect_b32 s76, s28, s38
	s_add_i32 s0, s73, s0
	s_lshl_b64 s[74:75], s[0:1], 7
	s_add_u32 s76, s76, s74
	s_addc_u32 s77, s77, s75
	s_add_i32 s0, s60, s48
	v_lshl_add_u64 v[216:217], s[76:77], 0, v[162:163]
	s_mov_b32 m0, s0
	ds_read_b128 v[192:195], v189 offset:16384
	ds_read_b128 v[196:199], v189 offset:17408
	ds_read_b128 v[200:203], v189 offset:18432
	ds_read_b128 v[204:207], v189 offset:19456
	ds_read_b128 v[208:211], v189 offset:20480
	ds_read_b128 v[212:215], v189 offset:21504
	ds_read_b128 v[224:227], v189 offset:22528
	ds_read_b128 v[228:231], v189 offset:23552
	global_load_lds_dwordx4 v[216:217], off
	s_add_i32 m0, s0, 0x2000
	v_lshl_add_u64 v[216:217], s[76:77], 0, v[166:167]
	s_add_u32 s76, s76, 0x58000
	s_addc_u32 s77, s77, 0
	s_add_i32 s0, s61, s48
	global_load_lds_dwordx4 v[216:217], off
	v_lshl_add_u64 v[216:217], s[76:77], 0, v[162:163]
	s_mov_b32 m0, s0
	s_nop 0
	global_load_lds_dwordx4 v[216:217], off
	s_add_i32 m0, s0, 0x2000
	s_and_b64 vcc, s[36:37], exec
	s_cselect_b32 s36, s40, s34
	s_cselect_b32 s0, s41, s35
	s_add_u32 s36, s36, s74
	v_lshl_add_u64 v[216:217], s[76:77], 0, v[166:167]
	s_addc_u32 s37, s0, s75
	global_load_lds_dwordx4 v[216:217], off
	v_lshl_add_u64 v[216:217], s[36:37], 0, v[160:161]
	s_mov_b32 m0, s49
	s_nop 0
	global_load_lds_dwordx4 v[216:217], off
	v_lshl_add_u64 v[216:217], s[36:37], 0, v[164:165]
	s_mov_b32 m0, s50
	s_nop 0
	global_load_lds_dwordx4 v[216:217], off
	s_waitcnt vmcnt(8)
	s_waitcnt lgkmcnt(0)
	s_barrier
	s_setprio 1
	s_waitcnt lgkmcnt(0)
	v_mfma_f32_16x16x128_f8f6f4 v[92:95], v[24:31], v[192:199], v[92:95]
	v_mfma_f32_16x16x128_f8f6f4 v[88:91], v[16:23], v[192:199], v[88:91]
	v_mfma_f32_16x16x128_f8f6f4 v[76:79], v[24:31], v[200:207], v[76:79]
	v_mfma_f32_16x16x128_f8f6f4 v[72:75], v[16:23], v[200:207], v[72:75]
	v_mfma_f32_16x16x128_f8f6f4 v[56:59], v[24:31], v[208:215], v[56:59]
	v_mfma_f32_16x16x128_f8f6f4 v[48:51], v[16:23], v[208:215], v[48:51]
	v_mfma_f32_16x16x128_f8f6f4 v[36:39], v[24:31], v[224:231], v[36:39]
	v_mfma_f32_16x16x128_f8f6f4 v[32:35], v[16:23], v[224:231], v[32:35]
	v_mfma_f32_16x16x128_f8f6f4 v[84:87], v[8:15], v[192:199], v[84:87]
	v_mfma_f32_16x16x128_f8f6f4 v[80:83], v[0:7], v[192:199], v[80:83]
	v_mfma_f32_16x16x128_f8f6f4 v[68:71], v[8:15], v[200:207], v[68:71]
	v_mfma_f32_16x16x128_f8f6f4 v[64:67], v[0:7], v[200:207], v[64:67]
	v_mfma_f32_16x16x128_f8f6f4 v[60:63], v[8:15], v[208:215], v[60:63]
	v_mfma_f32_16x16x128_f8f6f4 v[52:55], v[0:7], v[208:215], v[52:55]
	v_mfma_f32_16x16x128_f8f6f4 v[44:47], v[8:15], v[224:231], v[44:47]
	v_mfma_f32_16x16x128_f8f6f4 v[40:43], v[0:7], v[224:231], v[40:43]
	s_setprio 0
	s_barrier
	s_add_i32 s78, 0, 0x18000
	s_add_i32 s79, 0, 0x1c000
	v_add_u32_e32 v0, s78, v183
	v_add_u32_e32 v4, s79, v183
	ds_read_b128 v[24:27], v0
	ds_read_b128 v[28:31], v0 offset:1024
	ds_read_b128 v[16:19], v0 offset:2048
	ds_read_b128 v[20:23], v0 offset:3072
	ds_read_b128 v[8:11], v4
	ds_read_b128 v[12:15], v4 offset:1024
	ds_read_b128 v[0:3], v4 offset:2048
	ds_read_b128 v[4:7], v4 offset:3072
	s_add_u32 s36, s36, 0x58000
	s_addc_u32 s37, s37, 0
	s_mov_b32 m0, s51
	v_lshl_add_u64 v[216:217], s[36:37], 0, v[160:161]
	ds_read_b128 v[192:195], v189 offset:32768
	ds_read_b128 v[196:199], v189 offset:33792
	ds_read_b128 v[200:203], v189 offset:34816
	ds_read_b128 v[204:207], v189 offset:35840
	ds_read_b128 v[208:211], v189 offset:36864
	ds_read_b128 v[212:215], v189 offset:37888
	ds_read_b128 v[224:227], v189 offset:38912
	ds_read_b128 v[228:231], v189 offset:39936
	global_load_lds_dwordx4 v[216:217], off
	v_lshl_add_u64 v[216:217], s[36:37], 0, v[164:165]
	s_mov_b32 m0, s56
	s_nop 0
	global_load_lds_dwordx4 v[216:217], off
	s_waitcnt vmcnt(8)
	s_waitcnt lgkmcnt(0)
	s_barrier
	s_setprio 1
	s_waitcnt lgkmcnt(0)
	v_mfma_f32_16x16x128_f8f6f4 v[156:159], v[24:31], v[192:199], v[156:159]
	v_mfma_f32_16x16x128_f8f6f4 v[152:155], v[16:23], v[192:199], v[152:155]
	v_mfma_f32_16x16x128_f8f6f4 v[140:143], v[24:31], v[200:207], v[140:143]
	v_mfma_f32_16x16x128_f8f6f4 v[136:139], v[16:23], v[200:207], v[136:139]
	v_mfma_f32_16x16x128_f8f6f4 v[124:127], v[24:31], v[208:215], v[124:127]
	v_mfma_f32_16x16x128_f8f6f4 v[120:123], v[16:23], v[208:215], v[120:123]
	v_mfma_f32_16x16x128_f8f6f4 v[108:111], v[24:31], v[224:231], v[108:111]
	v_mfma_f32_16x16x128_f8f6f4 v[104:107], v[16:23], v[224:231], v[104:107]
	v_mfma_f32_16x16x128_f8f6f4 v[148:151], v[8:15], v[192:199], v[148:151]
	v_mfma_f32_16x16x128_f8f6f4 v[144:147], v[0:7], v[192:199], v[144:147]
	v_mfma_f32_16x16x128_f8f6f4 v[132:135], v[8:15], v[200:207], v[132:135]
	v_mfma_f32_16x16x128_f8f6f4 v[128:131], v[0:7], v[200:207], v[128:131]
	v_mfma_f32_16x16x128_f8f6f4 v[116:119], v[8:15], v[208:215], v[116:119]
	v_mfma_f32_16x16x128_f8f6f4 v[112:115], v[0:7], v[208:215], v[112:115]
	v_mfma_f32_16x16x128_f8f6f4 v[100:103], v[8:15], v[224:231], v[100:103]
	v_mfma_f32_16x16x128_f8f6f4 v[96:99], v[0:7], v[224:231], v[96:99]
	s_setprio 0
	s_barrier
	s_cmp_lt_u32 s67, 19
	s_cselect_b64 s[36:37], -1, 0
	s_and_b64 s[74:75], s[36:37], exec
	s_cselect_b32 s0, 0, 0xffffffea
	s_cselect_b32 s77, s29, s39
	s_cselect_b32 s76, s28, s38
	s_add_i32 s0, s0, s67
	s_add_i32 s0, s0, 3
	s_lshl_b64 s[74:75], s[0:1], 7
	s_add_u32 s76, s76, s74
	s_addc_u32 s77, s77, s75
	s_add_i32 s0, s78, s48
	v_lshl_add_u64 v[216:217], s[76:77], 0, v[162:163]
	s_mov_b32 m0, s0
	ds_read_b128 v[192:195], v189 offset:49152
	ds_read_b128 v[196:199], v189 offset:50176
	ds_read_b128 v[200:203], v189 offset:51200
	ds_read_b128 v[204:207], v189 offset:52224
	ds_read_b128 v[208:211], v189 offset:53248
	ds_read_b128 v[212:215], v189 offset:54272
	ds_read_b128 v[224:227], v189 offset:55296
	ds_read_b128 v[228:231], v189 offset:56320
	global_load_lds_dwordx4 v[216:217], off
	s_add_i32 m0, s0, 0x2000
	v_lshl_add_u64 v[216:217], s[76:77], 0, v[166:167]
	s_add_u32 s76, s76, 0x58000
	s_addc_u32 s77, s77, 0
	s_add_i32 s0, s79, s48
	global_load_lds_dwordx4 v[216:217], off
	v_lshl_add_u64 v[216:217], s[76:77], 0, v[162:163]
	s_mov_b32 m0, s0
	s_nop 0
	global_load_lds_dwordx4 v[216:217], off
	s_add_i32 m0, s0, 0x2000
	s_and_b64 s[36:37], s[36:37], exec
	s_cselect_b32 s36, s40, s34
	s_cselect_b32 s0, s41, s35
	s_add_u32 s36, s36, s74
	v_lshl_add_u64 v[216:217], s[76:77], 0, v[166:167]
	s_addc_u32 s37, s0, s75
	global_load_lds_dwordx4 v[216:217], off
	v_lshl_add_u64 v[216:217], s[36:37], 0, v[160:161]
	s_mov_b32 m0, s57
	s_nop 0
	global_load_lds_dwordx4 v[216:217], off
	v_lshl_add_u64 v[216:217], s[36:37], 0, v[164:165]
	s_mov_b32 m0, s58
	s_nop 0
	global_load_lds_dwordx4 v[216:217], off
	s_waitcnt vmcnt(8)
	s_waitcnt lgkmcnt(0)
	s_barrier
	s_setprio 1
	s_waitcnt lgkmcnt(0)
	v_mfma_f32_16x16x128_f8f6f4 v[92:95], v[24:31], v[192:199], v[92:95]
	v_mfma_f32_16x16x128_f8f6f4 v[88:91], v[16:23], v[192:199], v[88:91]
	v_mfma_f32_16x16x128_f8f6f4 v[76:79], v[24:31], v[200:207], v[76:79]
	v_mfma_f32_16x16x128_f8f6f4 v[72:75], v[16:23], v[200:207], v[72:75]
	v_mfma_f32_16x16x128_f8f6f4 v[56:59], v[24:31], v[208:215], v[56:59]
	v_mfma_f32_16x16x128_f8f6f4 v[48:51], v[16:23], v[208:215], v[48:51]
	v_mfma_f32_16x16x128_f8f6f4 v[36:39], v[24:31], v[224:231], v[36:39]
	v_mfma_f32_16x16x128_f8f6f4 v[32:35], v[16:23], v[224:231], v[32:35]
	v_mfma_f32_16x16x128_f8f6f4 v[84:87], v[8:15], v[192:199], v[84:87]
	v_mfma_f32_16x16x128_f8f6f4 v[80:83], v[0:7], v[192:199], v[80:83]
	v_mfma_f32_16x16x128_f8f6f4 v[68:71], v[8:15], v[200:207], v[68:71]
	v_mfma_f32_16x16x128_f8f6f4 v[64:67], v[0:7], v[200:207], v[64:67]
	v_mfma_f32_16x16x128_f8f6f4 v[60:63], v[8:15], v[208:215], v[60:63]
	v_mfma_f32_16x16x128_f8f6f4 v[52:55], v[0:7], v[208:215], v[52:55]
	v_mfma_f32_16x16x128_f8f6f4 v[44:47], v[8:15], v[224:231], v[44:47]
	v_mfma_f32_16x16x128_f8f6f4 v[40:43], v[0:7], v[224:231], v[40:43]
	s_setprio 0
	s_barrier
	v_lshl_add_u64 v[178:179], v[178:179], 0, s[26:27]
	v_lshl_add_u64 v[180:181], v[180:181], 0, s[26:27]
	s_mov_b32 s67, s73
	s_cbranch_vccnz .LBB0_673
	s_andn2_b64 vcc, exec, s[22:23]
	s_cbranch_vccnz .LBB0_676
	s_barrier

.LBB0_746:
	ds_read_b128 v[24:27], v191
	ds_read_b128 v[28:31], v191 offset:1024
	ds_read_b128 v[16:19], v191 offset:2048
	ds_read_b128 v[20:23], v191 offset:3072
	ds_read_b128 v[8:11], v192
	ds_read_b128 v[12:15], v192 offset:1024
	ds_read_b128 v[0:3], v192 offset:2048
	ds_read_b128 v[4:7], v192 offset:3072
	s_add_i32 m0, s29, 0xc000
	ds_read_b128 v[196:199], v193
	ds_read_b128 v[200:203], v193 offset:1024
	ds_read_b128 v[204:207], v193 offset:2048
	ds_read_b128 v[208:211], v193 offset:3072
	ds_read_b128 v[212:215], v193 offset:4096
	ds_read_b128 v[216:219], v193 offset:5120
	ds_read_b128 v[224:227], v193 offset:6144
	ds_read_b128 v[228:231], v193 offset:7168
	global_load_lds_dwordx4 v[180:181], off
	s_add_i32 m0, s29, 0xe000
	s_nop 0
	global_load_lds_dwordx4 v[182:183], off
	s_waitcnt vmcnt(8)
	s_waitcnt lgkmcnt(0)
	s_barrier
	s_setprio 1
	s_waitcnt lgkmcnt(0)
	v_mfma_f32_16x16x128_f8f6f4 v[156:159], v[24:31], v[196:203], v[156:159]
	v_mfma_f32_16x16x128_f8f6f4 v[152:155], v[16:23], v[196:203], v[152:155]
	v_mfma_f32_16x16x128_f8f6f4 v[140:143], v[24:31], v[204:211], v[140:143]
	v_mfma_f32_16x16x128_f8f6f4 v[136:139], v[16:23], v[204:211], v[136:139]
	v_mfma_f32_16x16x128_f8f6f4 v[124:127], v[24:31], v[212:219], v[124:127]
	v_mfma_f32_16x16x128_f8f6f4 v[120:123], v[16:23], v[212:219], v[120:123]
	v_mfma_f32_16x16x128_f8f6f4 v[108:111], v[24:31], v[224:231], v[108:111]
	v_mfma_f32_16x16x128_f8f6f4 v[104:107], v[16:23], v[224:231], v[104:107]
	v_mfma_f32_16x16x128_f8f6f4 v[148:151], v[8:15], v[196:203], v[148:151]
	v_mfma_f32_16x16x128_f8f6f4 v[144:147], v[0:7], v[196:203], v[144:147]
	v_mfma_f32_16x16x128_f8f6f4 v[132:135], v[8:15], v[204:211], v[132:135]
	v_mfma_f32_16x16x128_f8f6f4 v[128:131], v[0:7], v[204:211], v[128:131]
	v_mfma_f32_16x16x128_f8f6f4 v[116:119], v[8:15], v[212:219], v[116:119]
	v_mfma_f32_16x16x128_f8f6f4 v[112:115], v[0:7], v[212:219], v[112:115]
	v_mfma_f32_16x16x128_f8f6f4 v[100:103], v[8:15], v[224:231], v[100:103]
	v_mfma_f32_16x16x128_f8f6f4 v[96:99], v[0:7], v[224:231], v[96:99]
	s_setprio 0
	s_barrier
	s_cmp_gt_u32 s15, 5
	s_cselect_b64 s[36:37], -1, 0
	s_and_b64 s[38:39], s[36:37], exec
	v_sub_co_u32_e64 v168, s[38:39], s15, 6
	s_nop 0
	v_readfirstlane_b32 s74, v168
	s_cselect_b32 s17, s27, s31
	s_cselect_b32 s73, s26, s30
	s_add_i32 s75, s74, 8
	s_and_b64 s[66:67], s[36:37], exec
	s_cselect_b32 s66, s74, s75
	s_ashr_i32 s67, s66, 31
	s_lshl_b64 s[66:67], s[66:67], 7
	s_add_u32 s74, s73, s66
	s_addc_u32 s75, s17, s67
	s_add_i32 s17, s63, s46
	v_lshl_add_u64 v[186:187], s[74:75], 0, v[164:165]
	s_mov_b32 m0, s17
	ds_read_b128 v[196:199], v193 offset:16384
	ds_read_b128 v[200:203], v193 offset:17408
	ds_read_b128 v[204:207], v193 offset:18432
	ds_read_b128 v[208:211], v193 offset:19456
	ds_read_b128 v[212:215], v193 offset:20480
	ds_read_b128 v[216:219], v193 offset:21504
	ds_read_b128 v[224:227], v193 offset:22528
	ds_read_b128 v[228:231], v193 offset:23552
	global_load_lds_dwordx4 v[186:187], off
	s_add_i32 m0, s17, 0x2000
	v_lshl_add_u64 v[186:187], s[74:75], 0, v[160:161]
	s_add_u32 s74, s74, 0x20000
	s_addc_u32 s75, s75, 0
	s_add_i32 s17, s64, s46
	global_load_lds_dwordx4 v[186:187], off
	v_lshl_add_u64 v[186:187], s[74:75], 0, v[164:165]
	s_mov_b32 m0, s17
	s_nop 0
	global_load_lds_dwordx4 v[186:187], off
	s_add_i32 m0, s17, 0x2000
	s_and_b64 s[36:37], s[36:37], exec
	s_cselect_b32 s36, s22, s34
	s_cselect_b32 s17, s23, s35
	s_add_u32 s36, s36, s66
	v_lshl_add_u64 v[186:187], s[74:75], 0, v[160:161]
	s_addc_u32 s37, s17, s67
	global_load_lds_dwordx4 v[186:187], off
	v_lshl_add_u64 v[186:187], s[36:37], 0, v[166:167]
	s_mov_b32 m0, s29
	s_nop 0
	global_load_lds_dwordx4 v[186:187], off
	v_lshl_add_u64 v[186:187], s[36:37], 0, v[162:163]
	s_mov_b32 m0, s49
	s_nop 0
	global_load_lds_dwordx4 v[186:187], off
	s_waitcnt vmcnt(8)
	s_waitcnt lgkmcnt(0)
	s_barrier
	s_setprio 1
	s_waitcnt lgkmcnt(0)
	v_mfma_f32_16x16x128_f8f6f4 v[92:95], v[24:31], v[196:203], v[92:95]
	v_mfma_f32_16x16x128_f8f6f4 v[88:91], v[16:23], v[196:203], v[88:91]
	v_mfma_f32_16x16x128_f8f6f4 v[76:79], v[24:31], v[204:211], v[76:79]
	v_mfma_f32_16x16x128_f8f6f4 v[72:75], v[16:23], v[204:211], v[72:75]
	v_mfma_f32_16x16x128_f8f6f4 v[52:55], v[24:31], v[212:219], v[52:55]
	v_mfma_f32_16x16x128_f8f6f4 v[48:51], v[16:23], v[212:219], v[48:51]
	v_mfma_f32_16x16x128_f8f6f4 v[36:39], v[24:31], v[224:231], v[36:39]
	v_mfma_f32_16x16x128_f8f6f4 v[32:35], v[16:23], v[224:231], v[32:35]
	v_mfma_f32_16x16x128_f8f6f4 v[84:87], v[8:15], v[196:203], v[84:87]
	v_mfma_f32_16x16x128_f8f6f4 v[80:83], v[0:7], v[196:203], v[80:83]
	v_mfma_f32_16x16x128_f8f6f4 v[68:71], v[8:15], v[204:211], v[68:71]
	v_mfma_f32_16x16x128_f8f6f4 v[60:63], v[0:7], v[204:211], v[60:63]
	v_mfma_f32_16x16x128_f8f6f4 v[64:67], v[8:15], v[212:219], v[64:67]
	v_mfma_f32_16x16x128_f8f6f4 v[56:59], v[0:7], v[212:219], v[56:59]
	v_mfma_f32_16x16x128_f8f6f4 v[44:47], v[8:15], v[224:231], v[44:47]
	v_mfma_f32_16x16x128_f8f6f4 v[40:43], v[0:7], v[224:231], v[40:43]
	s_setprio 0
	s_barrier
	s_add_i32 s17, 0, 0x18000
	s_add_i32 s73, 0, 0x1c000
	v_add_u32_e32 v0, s17, v188
	v_add_u32_e32 v4, s73, v188
	ds_read_b128 v[24:27], v0
	ds_read_b128 v[28:31], v0 offset:1024
	ds_read_b128 v[16:19], v0 offset:2048
	ds_read_b128 v[20:23], v0 offset:3072
	ds_read_b128 v[8:11], v4
	ds_read_b128 v[12:15], v4 offset:1024
	ds_read_b128 v[0:3], v4 offset:2048
	ds_read_b128 v[4:7], v4 offset:3072
	s_add_u32 s36, s36, 0x20000
	s_addc_u32 s37, s37, 0
	s_mov_b32 m0, s50
	v_lshl_add_u64 v[186:187], s[36:37], 0, v[166:167]
	ds_read_b128 v[196:199], v193 offset:32768
	ds_read_b128 v[200:203], v193 offset:33792
	ds_read_b128 v[204:207], v193 offset:34816
	ds_read_b128 v[208:211], v193 offset:35840
	ds_read_b128 v[212:215], v193 offset:36864
	ds_read_b128 v[216:219], v193 offset:37888
	ds_read_b128 v[224:227], v193 offset:38912
	ds_read_b128 v[228:231], v193 offset:39936
	global_load_lds_dwordx4 v[186:187], off
	v_lshl_add_u64 v[186:187], s[36:37], 0, v[162:163]
	s_mov_b32 m0, s51
	s_nop 0
	global_load_lds_dwordx4 v[186:187], off
	s_waitcnt vmcnt(8)
	s_waitcnt lgkmcnt(0)
	s_barrier
	s_setprio 1
	s_waitcnt lgkmcnt(0)
	v_mfma_f32_16x16x128_f8f6f4 v[156:159], v[24:31], v[196:203], v[156:159]
	v_mfma_f32_16x16x128_f8f6f4 v[152:155], v[16:23], v[196:203], v[152:155]
	v_mfma_f32_16x16x128_f8f6f4 v[140:143], v[24:31], v[204:211], v[140:143]
	v_mfma_f32_16x16x128_f8f6f4 v[136:139], v[16:23], v[204:211], v[136:139]
	v_mfma_f32_16x16x128_f8f6f4 v[124:127], v[24:31], v[212:219], v[124:127]
	v_mfma_f32_16x16x128_f8f6f4 v[120:123], v[16:23], v[212:219], v[120:123]
	v_mfma_f32_16x16x128_f8f6f4 v[108:111], v[24:31], v[224:231], v[108:111]
	v_mfma_f32_16x16x128_f8f6f4 v[104:107], v[16:23], v[224:231], v[104:107]
	v_mfma_f32_16x16x128_f8f6f4 v[148:151], v[8:15], v[196:203], v[148:151]
	v_mfma_f32_16x16x128_f8f6f4 v[144:147], v[0:7], v[196:203], v[144:147]
	v_mfma_f32_16x16x128_f8f6f4 v[132:135], v[8:15], v[204:211], v[132:135]
	v_mfma_f32_16x16x128_f8f6f4 v[128:131], v[0:7], v[204:211], v[128:131]
	v_mfma_f32_16x16x128_f8f6f4 v[116:119], v[8:15], v[212:219], v[116:119]
	v_mfma_f32_16x16x128_f8f6f4 v[112:115], v[0:7], v[212:219], v[112:115]
	v_mfma_f32_16x16x128_f8f6f4 v[100:103], v[8:15], v[224:231], v[100:103]
	v_mfma_f32_16x16x128_f8f6f4 v[96:99], v[0:7], v[224:231], v[96:99]
	s_setprio 0
	s_barrier
	s_cmp_gt_u32 s15, 4
	s_cselect_b64 s[36:37], -1, 0
	s_and_b64 s[66:67], s[36:37], exec
	s_cselect_b32 s66, -5, 3
	s_cselect_b32 s75, s27, s31
	s_cselect_b32 s74, s26, s30
	s_add_i32 s66, s66, s15
	s_ashr_i32 s67, s66, 31
	s_lshl_b64 s[66:67], s[66:67], 7
	s_add_u32 s74, s74, s66
	s_addc_u32 s75, s75, s67
	s_add_i32 s17, s17, s46
	v_lshl_add_u64 v[186:187], s[74:75], 0, v[164:165]
	s_mov_b32 m0, s17
	ds_read_b128 v[196:199], v193 offset:49152
	ds_read_b128 v[200:203], v193 offset:50176
	ds_read_b128 v[204:207], v193 offset:51200
	ds_read_b128 v[208:211], v193 offset:52224
	ds_read_b128 v[212:215], v193 offset:53248
	ds_read_b128 v[216:219], v193 offset:54272
	ds_read_b128 v[224:227], v193 offset:55296
	ds_read_b128 v[228:231], v193 offset:56320
	global_load_lds_dwordx4 v[186:187], off
	s_add_i32 m0, s17, 0x2000
	v_lshl_add_u64 v[186:187], s[74:75], 0, v[160:161]
	s_add_u32 s74, s74, 0x20000
	s_addc_u32 s75, s75, 0
	s_add_i32 s17, s73, s46
	global_load_lds_dwordx4 v[186:187], off
	v_lshl_add_u64 v[186:187], s[74:75], 0, v[164:165]
	s_mov_b32 m0, s17
	s_nop 0
	global_load_lds_dwordx4 v[186:187], off
	s_add_i32 m0, s17, 0x2000
	s_and_b64 s[36:37], s[36:37], exec
	s_cselect_b32 s36, s22, s34
	s_cselect_b32 s17, s23, s35
	s_add_u32 s36, s36, s66
	v_lshl_add_u64 v[186:187], s[74:75], 0, v[160:161]
	s_addc_u32 s37, s17, s67
	global_load_lds_dwordx4 v[186:187], off
	v_lshl_add_u64 v[186:187], s[36:37], 0, v[166:167]
	s_mov_b32 m0, s59
	s_nop 0
	global_load_lds_dwordx4 v[186:187], off
	v_lshl_add_u64 v[186:187], s[36:37], 0, v[162:163]
	s_mov_b32 m0, s60
	s_nop 0
	global_load_lds_dwordx4 v[186:187], off
	s_waitcnt vmcnt(8)
	s_waitcnt lgkmcnt(0)
	s_barrier
	s_setprio 1
	s_waitcnt lgkmcnt(0)
	v_mfma_f32_16x16x128_f8f6f4 v[92:95], v[24:31], v[196:203], v[92:95]
	v_mfma_f32_16x16x128_f8f6f4 v[88:91], v[16:23], v[196:203], v[88:91]
	v_mfma_f32_16x16x128_f8f6f4 v[76:79], v[24:31], v[204:211], v[76:79]
	v_mfma_f32_16x16x128_f8f6f4 v[72:75], v[16:23], v[204:211], v[72:75]
	v_mfma_f32_16x16x128_f8f6f4 v[52:55], v[24:31], v[212:219], v[52:55]
	v_mfma_f32_16x16x128_f8f6f4 v[48:51], v[16:23], v[212:219], v[48:51]
	v_mfma_f32_16x16x128_f8f6f4 v[36:39], v[24:31], v[224:231], v[36:39]
	v_mfma_f32_16x16x128_f8f6f4 v[32:35], v[16:23], v[224:231], v[32:35]
	v_mfma_f32_16x16x128_f8f6f4 v[84:87], v[8:15], v[196:203], v[84:87]
	v_mfma_f32_16x16x128_f8f6f4 v[80:83], v[0:7], v[196:203], v[80:83]
	v_mfma_f32_16x16x128_f8f6f4 v[68:71], v[8:15], v[204:211], v[68:71]
	v_mfma_f32_16x16x128_f8f6f4 v[60:63], v[0:7], v[204:211], v[60:63]
	v_mfma_f32_16x16x128_f8f6f4 v[64:67], v[8:15], v[212:219], v[64:67]
	v_mfma_f32_16x16x128_f8f6f4 v[56:59], v[0:7], v[212:219], v[56:59]
	v_mfma_f32_16x16x128_f8f6f4 v[44:47], v[8:15], v[224:231], v[44:47]
	v_mfma_f32_16x16x128_f8f6f4 v[40:43], v[0:7], v[224:231], v[40:43]
	s_setprio 0
	s_barrier
	v_lshl_add_u64 v[180:181], v[180:181], 0, s[12:13]
	v_lshl_add_u64 v[182:183], v[182:183], 0, s[12:13]
	s_add_i32 s15, s15, 2
	s_and_b64 vcc, exec, s[38:39]
	s_cbranch_vccnz .LBB0_746
	s_andn2_b64 vcc, exec, s[8:9]
	s_cbranch_vccnz .LBB0_749
	s_barrier

.LBB0_773:
	ds_read_b128 v[24:27], v200
	ds_read_b128 v[28:31], v200 offset:1024
	ds_read_b128 v[16:19], v200 offset:2048
	ds_read_b128 v[20:23], v200 offset:3072
	ds_read_b128 v[8:11], v201
	ds_read_b128 v[12:15], v201 offset:1024
	ds_read_b128 v[0:3], v201 offset:2048
	ds_read_b128 v[4:7], v201 offset:3072
	s_add_i32 m0, s39, 0xc000
	ds_read_b128 v[206:209], v202
	ds_read_b128 v[210:213], v202 offset:1024
	ds_read_b128 v[214:217], v202 offset:2048
	ds_read_b128 v[218:221], v202 offset:3072
	ds_read_b128 v[224:227], v202 offset:4096
	ds_read_b128 v[228:231], v202 offset:5120
	ds_read_b128 v[232:235], v202 offset:6144
	ds_read_b128 v[236:239], v202 offset:7168
	global_load_lds_dwordx4 v[194:195], off
	s_add_i32 m0, s39, 0xe000
	s_nop 0
	global_load_lds_dwordx4 v[196:197], off
	s_waitcnt vmcnt(8)
	s_waitcnt lgkmcnt(0)
	s_barrier
	s_setprio 1
	s_waitcnt lgkmcnt(0)
	v_mfma_f32_16x16x128_f8f6f4 v[156:159], v[24:31], v[206:213], v[156:159]
	v_mfma_f32_16x16x128_f8f6f4 v[152:155], v[16:23], v[206:213], v[152:155]
	v_mfma_f32_16x16x128_f8f6f4 v[144:147], v[24:31], v[214:221], v[144:147]
	v_mfma_f32_16x16x128_f8f6f4 v[136:139], v[16:23], v[214:221], v[136:139]
	v_mfma_f32_16x16x128_f8f6f4 v[128:131], v[24:31], v[224:231], v[128:131]
	v_mfma_f32_16x16x128_f8f6f4 v[120:123], v[16:23], v[224:231], v[120:123]
	v_mfma_f32_16x16x128_f8f6f4 v[112:115], v[24:31], v[232:239], v[112:115]
	v_mfma_f32_16x16x128_f8f6f4 v[104:107], v[16:23], v[232:239], v[104:107]
	v_mfma_f32_16x16x128_f8f6f4 v[148:151], v[8:15], v[206:213], v[148:151]
	v_mfma_f32_16x16x128_f8f6f4 v[140:143], v[0:7], v[206:213], v[140:143]
	v_mfma_f32_16x16x128_f8f6f4 v[132:135], v[8:15], v[214:221], v[132:135]
	v_mfma_f32_16x16x128_f8f6f4 v[124:127], v[0:7], v[214:221], v[124:127]
	v_mfma_f32_16x16x128_f8f6f4 v[116:119], v[8:15], v[224:231], v[116:119]
	v_mfma_f32_16x16x128_f8f6f4 v[108:111], v[0:7], v[224:231], v[108:111]
	v_mfma_f32_16x16x128_f8f6f4 v[100:103], v[8:15], v[232:239], v[100:103]
	v_mfma_f32_16x16x128_f8f6f4 v[96:99], v[0:7], v[232:239], v[96:99]
	s_setprio 0
	s_barrier
	s_cmp_gt_u32 s9, 5
	s_cselect_b64 s[34:35], -1, 0
	s_and_b64 s[30:31], s[34:35], exec
	v_sub_co_u32_e64 v205, s[30:31], s9, 6
	s_nop 0
	v_readfirstlane_b32 s63, v205
	s_cselect_b32 s17, s23, s27
	s_cselect_b32 s62, s22, s26
	s_add_i32 s64, s63, 8
	s_and_b64 s[60:61], s[34:35], exec
	s_cselect_b32 s60, s63, s64
	s_ashr_i32 s61, s60, 31
	s_lshl_b64 s[60:61], s[60:61], 7
	s_add_u32 s62, s62, s60
	s_addc_u32 s63, s17, s61
	s_add_i32 s17, s57, s38
	v_lshl_add_u64 v[222:223], s[62:63], 0, v[162:163]
	s_mov_b32 m0, s17
	ds_read_b128 v[206:209], v202 offset:16384
	ds_read_b128 v[210:213], v202 offset:17408
	ds_read_b128 v[214:217], v202 offset:18432
	ds_read_b128 v[218:221], v202 offset:19456
	ds_read_b128 v[224:227], v202 offset:20480
	ds_read_b128 v[228:231], v202 offset:21504
	ds_read_b128 v[232:235], v202 offset:22528
	ds_read_b128 v[236:239], v202 offset:23552
	global_load_lds_dwordx4 v[222:223], off
	s_add_i32 m0, s17, 0x2000
	v_lshl_add_u64 v[222:223], s[62:63], 0, v[166:167]
	s_add_u32 s62, s62, 0x20000
	s_addc_u32 s63, s63, 0
	s_add_i32 s17, s58, s38
	global_load_lds_dwordx4 v[222:223], off
	v_lshl_add_u64 v[222:223], s[62:63], 0, v[162:163]
	s_mov_b32 m0, s17
	s_nop 0
	global_load_lds_dwordx4 v[222:223], off
	s_add_i32 m0, s17, 0x2000
	s_and_b64 s[34:35], s[34:35], exec
	s_cselect_b32 s34, s18, s28
	s_cselect_b32 s17, s19, s29
	s_add_u32 s34, s34, s60
	v_lshl_add_u64 v[222:223], s[62:63], 0, v[166:167]
	s_addc_u32 s35, s17, s61
	global_load_lds_dwordx4 v[222:223], off
	v_lshl_add_u64 v[222:223], s[34:35], 0, v[160:161]
	s_mov_b32 m0, s39
	s_nop 0
	global_load_lds_dwordx4 v[222:223], off
	v_lshl_add_u64 v[222:223], s[34:35], 0, v[164:165]
	s_mov_b32 m0, s42
	s_nop 0
	global_load_lds_dwordx4 v[222:223], off
	s_waitcnt vmcnt(8)
	s_waitcnt lgkmcnt(0)
	s_barrier
	s_setprio 1
	s_waitcnt lgkmcnt(0)
	v_mfma_f32_16x16x128_f8f6f4 v[92:95], v[24:31], v[206:213], v[92:95]
	v_mfma_f32_16x16x128_f8f6f4 v[88:91], v[16:23], v[206:213], v[88:91]
	v_mfma_f32_16x16x128_f8f6f4 v[80:83], v[24:31], v[214:221], v[80:83]
	v_mfma_f32_16x16x128_f8f6f4 v[64:67], v[16:23], v[214:221], v[64:67]
	v_mfma_f32_16x16x128_f8f6f4 v[48:51], v[24:31], v[224:231], v[48:51]
	v_mfma_f32_16x16x128_f8f6f4 v[40:43], v[16:23], v[224:231], v[40:43]
	v_mfma_f32_16x16x128_f8f6f4 v[36:39], v[24:31], v[232:239], v[36:39]
	v_mfma_f32_16x16x128_f8f6f4 v[32:35], v[16:23], v[232:239], v[32:35]
	v_mfma_f32_16x16x128_f8f6f4 v[84:87], v[8:15], v[206:213], v[84:87]
	v_mfma_f32_16x16x128_f8f6f4 v[76:79], v[0:7], v[206:213], v[76:79]
	v_mfma_f32_16x16x128_f8f6f4 v[52:55], v[8:15], v[214:221], v[52:55]
	v_mfma_f32_16x16x128_f8f6f4 v[44:47], v[0:7], v[214:221], v[44:47]
	v_mfma_f32_16x16x128_f8f6f4 v[72:75], v[8:15], v[224:231], v[72:75]
	v_mfma_f32_16x16x128_f8f6f4 v[68:71], v[0:7], v[224:231], v[68:71]
	v_mfma_f32_16x16x128_f8f6f4 v[60:63], v[8:15], v[232:239], v[60:63]
	v_mfma_f32_16x16x128_f8f6f4 v[56:59], v[0:7], v[232:239], v[56:59]
	s_setprio 0
	s_barrier
	s_add_i32 s17, 0, 0x18000
	s_add_i32 s64, 0, 0x1c000
	v_add_u32_e32 v0, s17, v198
	v_add_u32_e32 v4, s64, v198
	ds_read_b128 v[24:27], v0
	ds_read_b128 v[28:31], v0 offset:1024
	ds_read_b128 v[16:19], v0 offset:2048
	ds_read_b128 v[20:23], v0 offset:3072
	ds_read_b128 v[8:11], v4
	ds_read_b128 v[12:15], v4 offset:1024
	ds_read_b128 v[0:3], v4 offset:2048
	ds_read_b128 v[4:7], v4 offset:3072
	s_add_u32 s34, s34, 0x20000
	s_addc_u32 s35, s35, 0
	s_mov_b32 m0, s43
	v_lshl_add_u64 v[222:223], s[34:35], 0, v[160:161]
	ds_read_b128 v[206:209], v202 offset:32768
	ds_read_b128 v[210:213], v202 offset:33792
	ds_read_b128 v[214:217], v202 offset:34816
	ds_read_b128 v[218:221], v202 offset:35840
	ds_read_b128 v[224:227], v202 offset:36864
	ds_read_b128 v[228:231], v202 offset:37888
	ds_read_b128 v[232:235], v202 offset:38912
	ds_read_b128 v[236:239], v202 offset:39936
	global_load_lds_dwordx4 v[222:223], off
	v_lshl_add_u64 v[222:223], s[34:35], 0, v[164:165]
	s_mov_b32 m0, s46
	s_nop 0
	global_load_lds_dwordx4 v[222:223], off
	s_waitcnt vmcnt(8)
	s_waitcnt lgkmcnt(0)
	s_barrier
	s_setprio 1
	s_waitcnt lgkmcnt(0)
	v_mfma_f32_16x16x128_f8f6f4 v[156:159], v[24:31], v[206:213], v[156:159]
	v_mfma_f32_16x16x128_f8f6f4 v[152:155], v[16:23], v[206:213], v[152:155]
	v_mfma_f32_16x16x128_f8f6f4 v[144:147], v[24:31], v[214:221], v[144:147]
	v_mfma_f32_16x16x128_f8f6f4 v[136:139], v[16:23], v[214:221], v[136:139]
	v_mfma_f32_16x16x128_f8f6f4 v[128:131], v[24:31], v[224:231], v[128:131]
	v_mfma_f32_16x16x128_f8f6f4 v[120:123], v[16:23], v[224:231], v[120:123]
	v_mfma_f32_16x16x128_f8f6f4 v[112:115], v[24:31], v[232:239], v[112:115]
	v_mfma_f32_16x16x128_f8f6f4 v[104:107], v[16:23], v[232:239], v[104:107]
	v_mfma_f32_16x16x128_f8f6f4 v[148:151], v[8:15], v[206:213], v[148:151]
	v_mfma_f32_16x16x128_f8f6f4 v[140:143], v[0:7], v[206:213], v[140:143]
	v_mfma_f32_16x16x128_f8f6f4 v[132:135], v[8:15], v[214:221], v[132:135]
	v_mfma_f32_16x16x128_f8f6f4 v[124:127], v[0:7], v[214:221], v[124:127]
	v_mfma_f32_16x16x128_f8f6f4 v[116:119], v[8:15], v[224:231], v[116:119]
	v_mfma_f32_16x16x128_f8f6f4 v[108:111], v[0:7], v[224:231], v[108:111]
	v_mfma_f32_16x16x128_f8f6f4 v[100:103], v[8:15], v[232:239], v[100:103]
	v_mfma_f32_16x16x128_f8f6f4 v[96:99], v[0:7], v[232:239], v[96:99]
	s_setprio 0
	s_barrier
	s_cmp_gt_u32 s9, 4
	s_cselect_b64 s[34:35], -1, 0
	s_and_b64 s[60:61], s[34:35], exec
	s_cselect_b32 s60, -5, 3
	s_cselect_b32 s63, s23, s27
	s_cselect_b32 s62, s22, s26
	s_add_i32 s60, s60, s9
	s_ashr_i32 s61, s60, 31
	s_lshl_b64 s[60:61], s[60:61], 7
	s_add_u32 s62, s62, s60
	s_addc_u32 s63, s63, s61
	s_add_i32 s17, s17, s38
	v_lshl_add_u64 v[222:223], s[62:63], 0, v[162:163]
	s_mov_b32 m0, s17
	ds_read_b128 v[206:209], v202 offset:49152
	ds_read_b128 v[210:213], v202 offset:50176
	ds_read_b128 v[214:217], v202 offset:51200
	ds_read_b128 v[218:221], v202 offset:52224
	ds_read_b128 v[224:227], v202 offset:53248
	ds_read_b128 v[228:231], v202 offset:54272
	ds_read_b128 v[232:235], v202 offset:55296
	ds_read_b128 v[236:239], v202 offset:56320
	global_load_lds_dwordx4 v[222:223], off
	s_add_i32 m0, s17, 0x2000
	v_lshl_add_u64 v[222:223], s[62:63], 0, v[166:167]
	s_add_u32 s62, s62, 0x20000
	s_addc_u32 s63, s63, 0
	s_add_i32 s17, s64, s38
	global_load_lds_dwordx4 v[222:223], off
	v_lshl_add_u64 v[222:223], s[62:63], 0, v[162:163]
	s_mov_b32 m0, s17
	s_nop 0
	global_load_lds_dwordx4 v[222:223], off
	s_add_i32 m0, s17, 0x2000
	s_and_b64 s[34:35], s[34:35], exec
	s_cselect_b32 s34, s18, s28
	s_cselect_b32 s17, s19, s29
	s_add_u32 s34, s34, s60
	v_lshl_add_u64 v[222:223], s[62:63], 0, v[166:167]
	s_addc_u32 s35, s17, s61
	global_load_lds_dwordx4 v[222:223], off
	v_lshl_add_u64 v[222:223], s[34:35], 0, v[160:161]
	s_mov_b32 m0, s49
	s_nop 0
	global_load_lds_dwordx4 v[222:223], off
	v_lshl_add_u64 v[222:223], s[34:35], 0, v[164:165]
	s_mov_b32 m0, s50
	s_nop 0
	global_load_lds_dwordx4 v[222:223], off
	s_waitcnt vmcnt(8)
	s_waitcnt lgkmcnt(0)
	s_barrier
	s_setprio 1
	s_waitcnt lgkmcnt(0)
	v_mfma_f32_16x16x128_f8f6f4 v[92:95], v[24:31], v[206:213], v[92:95]
	v_mfma_f32_16x16x128_f8f6f4 v[88:91], v[16:23], v[206:213], v[88:91]
	v_mfma_f32_16x16x128_f8f6f4 v[80:83], v[24:31], v[214:221], v[80:83]
	v_mfma_f32_16x16x128_f8f6f4 v[64:67], v[16:23], v[214:221], v[64:67]
	v_mfma_f32_16x16x128_f8f6f4 v[48:51], v[24:31], v[224:231], v[48:51]
	v_mfma_f32_16x16x128_f8f6f4 v[40:43], v[16:23], v[224:231], v[40:43]
	v_mfma_f32_16x16x128_f8f6f4 v[36:39], v[24:31], v[232:239], v[36:39]
	v_mfma_f32_16x16x128_f8f6f4 v[32:35], v[16:23], v[232:239], v[32:35]
	v_mfma_f32_16x16x128_f8f6f4 v[84:87], v[8:15], v[206:213], v[84:87]
	v_mfma_f32_16x16x128_f8f6f4 v[76:79], v[0:7], v[206:213], v[76:79]
	v_mfma_f32_16x16x128_f8f6f4 v[52:55], v[8:15], v[214:221], v[52:55]
	v_mfma_f32_16x16x128_f8f6f4 v[44:47], v[0:7], v[214:221], v[44:47]
	v_mfma_f32_16x16x128_f8f6f4 v[72:75], v[8:15], v[224:231], v[72:75]
	v_mfma_f32_16x16x128_f8f6f4 v[68:71], v[0:7], v[224:231], v[68:71]
	v_mfma_f32_16x16x128_f8f6f4 v[60:63], v[8:15], v[232:239], v[60:63]
	v_mfma_f32_16x16x128_f8f6f4 v[56:59], v[0:7], v[232:239], v[56:59]
	s_setprio 0
	s_barrier
	v_lshl_add_u64 v[194:195], v[194:195], 0, s[12:13]
	v_lshl_add_u64 v[196:197], v[196:197], 0, s[12:13]
	s_add_i32 s9, s9, 2
	s_and_b64 vcc, exec, s[30:31]
	s_cbranch_vccnz .LBB0_773
	s_andn2_b64 vcc, exec, s[10:11]
	s_cbranch_vccnz .LBB0_776
	s_barrier

.LBB0_959:
	ds_read_b128 v[24:27], v187
	ds_read_b128 v[28:31], v187 offset:1024
	ds_read_b128 v[16:19], v187 offset:2048
	ds_read_b128 v[20:23], v187 offset:3072
	s_waitcnt lgkmcnt(0)
	ds_read_b128 v[8:11], v188
	ds_read_b128 v[12:15], v188 offset:1024
	ds_read_b128 v[0:3], v188 offset:2048
	ds_read_b128 v[4:7], v188 offset:3072
	s_add_i32 m0, s49, 0xc000
	ds_read_b128 v[192:195], v189
	ds_read_b128 v[196:199], v189 offset:1024
	ds_read_b128 v[200:203], v189 offset:2048
	ds_read_b128 v[204:207], v189 offset:3072
	ds_read_b128 v[208:211], v189 offset:4096
	ds_read_b128 v[212:215], v189 offset:5120
	ds_read_b128 v[224:227], v189 offset:6144
	ds_read_b128 v[228:231], v189 offset:7168
	global_load_lds_dwordx4 v[178:179], off
	s_add_i32 m0, s49, 0xe000
	s_nop 0
	global_load_lds_dwordx4 v[180:181], off
	s_waitcnt vmcnt(8)
	s_waitcnt lgkmcnt(0)
	s_barrier
	s_setprio 1
	s_waitcnt lgkmcnt(0)
	v_mfma_f32_16x16x128_f8f6f4 v[156:159], v[24:31], v[192:199], v[156:159]
	v_mfma_f32_16x16x128_f8f6f4 v[152:155], v[16:23], v[192:199], v[152:155]
	v_mfma_f32_16x16x128_f8f6f4 v[140:143], v[24:31], v[200:207], v[140:143]
	v_mfma_f32_16x16x128_f8f6f4 v[136:139], v[16:23], v[200:207], v[136:139]
	v_mfma_f32_16x16x128_f8f6f4 v[124:127], v[24:31], v[208:215], v[124:127]
	v_mfma_f32_16x16x128_f8f6f4 v[120:123], v[16:23], v[208:215], v[120:123]
	v_mfma_f32_16x16x128_f8f6f4 v[108:111], v[24:31], v[224:231], v[108:111]
	v_mfma_f32_16x16x128_f8f6f4 v[104:107], v[16:23], v[224:231], v[104:107]
	v_mfma_f32_16x16x128_f8f6f4 v[148:151], v[8:15], v[192:199], v[148:151]
	v_mfma_f32_16x16x128_f8f6f4 v[144:147], v[0:7], v[192:199], v[144:147]
	v_mfma_f32_16x16x128_f8f6f4 v[132:135], v[8:15], v[200:207], v[132:135]
	v_mfma_f32_16x16x128_f8f6f4 v[128:131], v[0:7], v[200:207], v[128:131]
	v_mfma_f32_16x16x128_f8f6f4 v[116:119], v[8:15], v[208:215], v[116:119]
	v_mfma_f32_16x16x128_f8f6f4 v[112:115], v[0:7], v[208:215], v[112:115]
	v_mfma_f32_16x16x128_f8f6f4 v[100:103], v[8:15], v[224:231], v[100:103]
	v_mfma_f32_16x16x128_f8f6f4 v[96:99], v[0:7], v[224:231], v[96:99]
	s_setprio 0
	s_barrier
	s_add_i32 s23, s21, 2
	s_cmp_lt_u32 s21, 6
	s_cselect_b64 s[36:37], -1, 0
	s_and_b64 s[64:65], s[36:37], exec
	s_cselect_b32 s0, 0, -8
	s_cselect_b32 s63, s39, s35
	s_cselect_b32 s66, s38, s34
	s_add_i32 s0, s23, s0
	s_lshl_b64 s[64:65], s[0:1], 7
	s_add_u32 s66, s66, s64
	s_addc_u32 s67, s63, s65
	s_add_i32 s0, s60, s48
	v_lshl_add_u64 v[216:217], s[66:67], 0, v[162:163]
	s_mov_b32 m0, s0
	ds_read_b128 v[192:195], v189 offset:16384
	ds_read_b128 v[196:199], v189 offset:17408
	ds_read_b128 v[200:203], v189 offset:18432
	ds_read_b128 v[204:207], v189 offset:19456
	ds_read_b128 v[208:211], v189 offset:20480
	ds_read_b128 v[212:215], v189 offset:21504
	ds_read_b128 v[224:227], v189 offset:22528
	ds_read_b128 v[228:231], v189 offset:23552
	global_load_lds_dwordx4 v[216:217], off
	s_add_i32 m0, s0, 0x2000
	v_lshl_add_u64 v[216:217], s[66:67], 0, v[166:167]
	s_add_u32 s66, s66, 0x20000
	s_addc_u32 s67, s67, 0
	s_add_i32 s0, s61, s48
	global_load_lds_dwordx4 v[216:217], off
	v_lshl_add_u64 v[216:217], s[66:67], 0, v[162:163]
	s_mov_b32 m0, s0
	s_nop 0
	global_load_lds_dwordx4 v[216:217], off
	s_add_i32 m0, s0, 0x2000
	s_and_b64 vcc, s[36:37], exec
	s_cselect_b32 s36, s40, s30
	s_cselect_b32 s0, s41, s31
	s_add_u32 s36, s36, s64
	v_lshl_add_u64 v[216:217], s[66:67], 0, v[166:167]
	s_addc_u32 s37, s0, s65
	global_load_lds_dwordx4 v[216:217], off
	v_lshl_add_u64 v[216:217], s[36:37], 0, v[160:161]
	s_mov_b32 m0, s49
	s_nop 0
	global_load_lds_dwordx4 v[216:217], off
	v_lshl_add_u64 v[216:217], s[36:37], 0, v[164:165]
	s_mov_b32 m0, s50
	s_nop 0
	global_load_lds_dwordx4 v[216:217], off
	s_waitcnt vmcnt(8)
	s_waitcnt lgkmcnt(0)
	s_barrier
	s_setprio 1
	s_waitcnt lgkmcnt(0)
	v_mfma_f32_16x16x128_f8f6f4 v[92:95], v[24:31], v[192:199], v[92:95]
	v_mfma_f32_16x16x128_f8f6f4 v[88:91], v[16:23], v[192:199], v[88:91]
	v_mfma_f32_16x16x128_f8f6f4 v[76:79], v[24:31], v[200:207], v[76:79]
	v_mfma_f32_16x16x128_f8f6f4 v[72:75], v[16:23], v[200:207], v[72:75]
	v_mfma_f32_16x16x128_f8f6f4 v[56:59], v[24:31], v[208:215], v[56:59]
	v_mfma_f32_16x16x128_f8f6f4 v[48:51], v[16:23], v[208:215], v[48:51]
	v_mfma_f32_16x16x128_f8f6f4 v[36:39], v[24:31], v[224:231], v[36:39]
	v_mfma_f32_16x16x128_f8f6f4 v[32:35], v[16:23], v[224:231], v[32:35]
	v_mfma_f32_16x16x128_f8f6f4 v[84:87], v[8:15], v[192:199], v[84:87]
	v_mfma_f32_16x16x128_f8f6f4 v[80:83], v[0:7], v[192:199], v[80:83]
	v_mfma_f32_16x16x128_f8f6f4 v[68:71], v[8:15], v[200:207], v[68:71]
	v_mfma_f32_16x16x128_f8f6f4 v[64:67], v[0:7], v[200:207], v[64:67]
	v_mfma_f32_16x16x128_f8f6f4 v[60:63], v[8:15], v[208:215], v[60:63]
	v_mfma_f32_16x16x128_f8f6f4 v[52:55], v[0:7], v[208:215], v[52:55]
	v_mfma_f32_16x16x128_f8f6f4 v[44:47], v[8:15], v[224:231], v[44:47]
	v_mfma_f32_16x16x128_f8f6f4 v[40:43], v[0:7], v[224:231], v[40:43]
	s_setprio 0
	s_barrier
	s_add_i32 s63, 0, 0x18000
	s_add_i32 s68, 0, 0x1c000
	v_add_u32_e32 v0, s63, v183
	v_add_u32_e32 v4, s68, v183
	ds_read_b128 v[24:27], v0
	ds_read_b128 v[28:31], v0 offset:1024
	ds_read_b128 v[16:19], v0 offset:2048
	ds_read_b128 v[20:23], v0 offset:3072
	ds_read_b128 v[8:11], v4
	ds_read_b128 v[12:15], v4 offset:1024
	ds_read_b128 v[0:3], v4 offset:2048
	ds_read_b128 v[4:7], v4 offset:3072
	s_add_u32 s36, s36, 0x20000
	s_addc_u32 s37, s37, 0
	s_mov_b32 m0, s51
	v_lshl_add_u64 v[216:217], s[36:37], 0, v[160:161]
	ds_read_b128 v[192:195], v189 offset:32768
	ds_read_b128 v[196:199], v189 offset:33792
	ds_read_b128 v[200:203], v189 offset:34816
	ds_read_b128 v[204:207], v189 offset:35840
	ds_read_b128 v[208:211], v189 offset:36864
	ds_read_b128 v[212:215], v189 offset:37888
	ds_read_b128 v[224:227], v189 offset:38912
	ds_read_b128 v[228:231], v189 offset:39936
	global_load_lds_dwordx4 v[216:217], off
	v_lshl_add_u64 v[216:217], s[36:37], 0, v[164:165]
	s_mov_b32 m0, s56
	s_nop 0
	global_load_lds_dwordx4 v[216:217], off
	s_waitcnt vmcnt(8)
	s_waitcnt lgkmcnt(0)
	s_barrier
	s_setprio 1
	s_waitcnt lgkmcnt(0)
	v_mfma_f32_16x16x128_f8f6f4 v[156:159], v[24:31], v[192:199], v[156:159]
	v_mfma_f32_16x16x128_f8f6f4 v[152:155], v[16:23], v[192:199], v[152:155]
	v_mfma_f32_16x16x128_f8f6f4 v[140:143], v[24:31], v[200:207], v[140:143]
	v_mfma_f32_16x16x128_f8f6f4 v[136:139], v[16:23], v[200:207], v[136:139]
	v_mfma_f32_16x16x128_f8f6f4 v[124:127], v[24:31], v[208:215], v[124:127]
	v_mfma_f32_16x16x128_f8f6f4 v[120:123], v[16:23], v[208:215], v[120:123]
	v_mfma_f32_16x16x128_f8f6f4 v[108:111], v[24:31], v[224:231], v[108:111]
	v_mfma_f32_16x16x128_f8f6f4 v[104:107], v[16:23], v[224:231], v[104:107]
	v_mfma_f32_16x16x128_f8f6f4 v[148:151], v[8:15], v[192:199], v[148:151]
	v_mfma_f32_16x16x128_f8f6f4 v[144:147], v[0:7], v[192:199], v[144:147]
	v_mfma_f32_16x16x128_f8f6f4 v[132:135], v[8:15], v[200:207], v[132:135]
	v_mfma_f32_16x16x128_f8f6f4 v[128:131], v[0:7], v[200:207], v[128:131]
	v_mfma_f32_16x16x128_f8f6f4 v[116:119], v[8:15], v[208:215], v[116:119]
	v_mfma_f32_16x16x128_f8f6f4 v[112:115], v[0:7], v[208:215], v[112:115]
	v_mfma_f32_16x16x128_f8f6f4 v[100:103], v[8:15], v[224:231], v[100:103]
	v_mfma_f32_16x16x128_f8f6f4 v[96:99], v[0:7], v[224:231], v[96:99]
	s_setprio 0
	s_barrier
	s_cmp_lt_u32 s21, 5
	s_cselect_b64 s[36:37], -1, 0
	s_and_b64 s[64:65], s[36:37], exec
	s_cselect_b32 s0, 0, -8
	s_cselect_b32 s67, s39, s35
	s_cselect_b32 s66, s38, s34
	s_add_i32 s0, s0, s21
	s_add_i32 s0, s0, 3
	s_lshl_b64 s[64:65], s[0:1], 7
	s_add_u32 s66, s66, s64
	s_addc_u32 s67, s67, s65
	s_add_i32 s0, s63, s48
	v_lshl_add_u64 v[216:217], s[66:67], 0, v[162:163]
	s_mov_b32 m0, s0
	ds_read_b128 v[192:195], v189 offset:49152
	ds_read_b128 v[196:199], v189 offset:50176
	ds_read_b128 v[200:203], v189 offset:51200
	ds_read_b128 v[204:207], v189 offset:52224
	ds_read_b128 v[208:211], v189 offset:53248
	ds_read_b128 v[212:215], v189 offset:54272
	ds_read_b128 v[224:227], v189 offset:55296
	ds_read_b128 v[228:231], v189 offset:56320
	global_load_lds_dwordx4 v[216:217], off
	s_add_i32 m0, s0, 0x2000
	v_lshl_add_u64 v[216:217], s[66:67], 0, v[166:167]
	s_add_u32 s66, s66, 0x20000
	s_addc_u32 s67, s67, 0
	s_add_i32 s0, s68, s48
	global_load_lds_dwordx4 v[216:217], off
	v_lshl_add_u64 v[216:217], s[66:67], 0, v[162:163]
	s_mov_b32 m0, s0
	s_nop 0
	global_load_lds_dwordx4 v[216:217], off
	s_add_i32 m0, s0, 0x2000
	s_and_b64 s[36:37], s[36:37], exec
	s_cselect_b32 s21, s40, s30
	s_cselect_b32 s0, s41, s31
	s_add_u32 s36, s21, s64
	v_lshl_add_u64 v[216:217], s[66:67], 0, v[166:167]
	s_addc_u32 s37, s0, s65
	global_load_lds_dwordx4 v[216:217], off
	v_lshl_add_u64 v[216:217], s[36:37], 0, v[160:161]
	s_mov_b32 m0, s57
	s_nop 0
	global_load_lds_dwordx4 v[216:217], off
	v_lshl_add_u64 v[216:217], s[36:37], 0, v[164:165]
	s_mov_b32 m0, s58
	s_nop 0
	global_load_lds_dwordx4 v[216:217], off
	s_waitcnt vmcnt(8)
	s_waitcnt lgkmcnt(0)
	s_barrier
	s_setprio 1
	s_waitcnt lgkmcnt(0)
	v_mfma_f32_16x16x128_f8f6f4 v[92:95], v[24:31], v[192:199], v[92:95]
	v_mfma_f32_16x16x128_f8f6f4 v[88:91], v[16:23], v[192:199], v[88:91]
	v_mfma_f32_16x16x128_f8f6f4 v[76:79], v[24:31], v[200:207], v[76:79]
	v_mfma_f32_16x16x128_f8f6f4 v[72:75], v[16:23], v[200:207], v[72:75]
	v_mfma_f32_16x16x128_f8f6f4 v[56:59], v[24:31], v[208:215], v[56:59]
	v_mfma_f32_16x16x128_f8f6f4 v[48:51], v[16:23], v[208:215], v[48:51]
	v_mfma_f32_16x16x128_f8f6f4 v[36:39], v[24:31], v[224:231], v[36:39]
	v_mfma_f32_16x16x128_f8f6f4 v[32:35], v[16:23], v[224:231], v[32:35]
	v_mfma_f32_16x16x128_f8f6f4 v[84:87], v[8:15], v[192:199], v[84:87]
	v_mfma_f32_16x16x128_f8f6f4 v[80:83], v[0:7], v[192:199], v[80:83]
	v_mfma_f32_16x16x128_f8f6f4 v[68:71], v[8:15], v[200:207], v[68:71]
	v_mfma_f32_16x16x128_f8f6f4 v[64:67], v[0:7], v[200:207], v[64:67]
	v_mfma_f32_16x16x128_f8f6f4 v[60:63], v[8:15], v[208:215], v[60:63]
	v_mfma_f32_16x16x128_f8f6f4 v[52:55], v[0:7], v[208:215], v[52:55]
	v_mfma_f32_16x16x128_f8f6f4 v[44:47], v[8:15], v[224:231], v[44:47]
	v_mfma_f32_16x16x128_f8f6f4 v[40:43], v[0:7], v[224:231], v[40:43]
	s_setprio 0
	s_barrier
	v_lshl_add_u64 v[178:179], v[178:179], 0, s[16:17]
	v_lshl_add_u64 v[180:181], v[180:181], 0, s[16:17]
	s_mov_b32 s21, s23
	s_cbranch_vccnz .LBB0_959
	s_andn2_b64 vcc, exec, s[14:15]
	s_cbranch_vccnz .LBB0_962
	s_barrier

.LBB0_1182:
	v_add_u32_e32 v0, s69, v222
	v_add_u32_e32 v4, s70, v222
	ds_read_b128 v[24:27], v0
	ds_read_b128 v[28:31], v0 offset:1024
	ds_read_b128 v[16:19], v0 offset:2048
	ds_read_b128 v[20:23], v0 offset:3072
	ds_read_b128 v[8:11], v4
	ds_read_b128 v[12:15], v4 offset:1024
	ds_read_b128 v[0:3], v4 offset:2048
	ds_read_b128 v[4:7], v4 offset:3072
	v_lshl_add_u64 v[214:215], s[34:35], 0, v[192:193]
	s_add_i32 m0, s29, 0xc000
	ds_read_b128 v[32:35], v226
	ds_read_b128 v[36:39], v226 offset:1024
	ds_read_b128 v[40:43], v226 offset:2048
	ds_read_b128 v[44:47], v226 offset:3072
	ds_read_b128 v[48:51], v226 offset:4096
	ds_read_b128 v[52:55], v226 offset:5120
	ds_read_b128 v[56:59], v226 offset:6144
	ds_read_b128 v[60:63], v226 offset:7168
	global_load_lds_dwordx4 v[214:215], off
	v_lshl_add_u64 v[214:215], s[34:35], 0, v[210:211]
	s_add_i32 m0, s29, 0xe000
	s_nop 0
	global_load_lds_dwordx4 v[214:215], off
	s_waitcnt vmcnt(8)
	s_waitcnt lgkmcnt(0)
	s_barrier
	s_setprio 1
	s_waitcnt lgkmcnt(0)
	v_mfma_f32_16x16x128_f8f6f4 v[188:191], v[24:31], v[32:39], v[188:191]
	v_mfma_f32_16x16x128_f8f6f4 v[180:183], v[16:23], v[32:39], v[180:183]
	v_mfma_f32_16x16x128_f8f6f4 v[172:175], v[24:31], v[40:47], v[172:175]
	v_mfma_f32_16x16x128_f8f6f4 v[164:167], v[16:23], v[40:47], v[164:167]
	v_mfma_f32_16x16x128_f8f6f4 v[156:159], v[24:31], v[48:55], v[156:159]
	v_mfma_f32_16x16x128_f8f6f4 v[148:151], v[16:23], v[48:55], v[148:151]
	v_mfma_f32_16x16x128_f8f6f4 v[140:143], v[24:31], v[56:63], v[140:143]
	v_mfma_f32_16x16x128_f8f6f4 v[132:135], v[16:23], v[56:63], v[132:135]
	v_mfma_f32_16x16x128_f8f6f4 v[184:187], v[8:15], v[32:39], v[184:187]
	v_mfma_f32_16x16x128_f8f6f4 v[176:179], v[0:7], v[32:39], v[176:179]
	v_mfma_f32_16x16x128_f8f6f4 v[168:171], v[8:15], v[40:47], v[168:171]
	v_mfma_f32_16x16x128_f8f6f4 v[160:163], v[0:7], v[40:47], v[160:163]
	v_mfma_f32_16x16x128_f8f6f4 v[152:155], v[8:15], v[48:55], v[152:155]
	v_mfma_f32_16x16x128_f8f6f4 v[144:147], v[0:7], v[48:55], v[144:147]
	v_mfma_f32_16x16x128_f8f6f4 v[136:139], v[8:15], v[56:63], v[136:139]
	v_mfma_f32_16x16x128_f8f6f4 v[128:131], v[0:7], v[56:63], v[128:131]
	s_setprio 0
	s_barrier
	s_cmp_gt_u32 s25, 5
	v_sub_co_u32_e64 v216, s[40:41], s25, 6
	s_cselect_b64 vcc, -1, 0
	v_add_u32_e32 v217, 8, v216
	v_cndmask_b32_e32 v216, v217, v216, vcc
	v_ashrrev_i32_e32 v217, 31, v216
	v_cndmask_b32_e32 v215, v213, v205, vcc
	v_cndmask_b32_e32 v214, v212, v204, vcc
	v_lshlrev_b64 v[216:217], 7, v[216:217]
	v_lshl_add_u64 v[214:215], v[214:215], 0, v[216:217]
	s_add_i32 s26, s69, s7
	s_add_i32 s38, s26, 0x2000
	v_lshl_add_u64 v[236:237], v[214:215], 0, v[194:195]
	s_mov_b32 m0, s26
	ds_read_b128 v[56:59], v226 offset:16384
	ds_read_b128 v[60:63], v226 offset:17408
	ds_read_b128 v[48:51], v226 offset:18432
	ds_read_b128 v[52:55], v226 offset:19456
	ds_read_b128 v[40:43], v226 offset:20480
	ds_read_b128 v[44:47], v226 offset:21504
	ds_read_b128 v[32:35], v226 offset:22528
	ds_read_b128 v[36:39], v226 offset:23552
	v_lshl_add_u64 v[234:235], v[214:215], 0, s[0:1]
	s_add_i32 s39, s70, s7
	global_load_lds_dwordx4 v[236:237], off
	v_lshl_add_u64 v[214:215], v[214:215], 0, v[196:197]
	s_mov_b32 m0, s38
	s_add_i32 s42, s39, 0x2000
	global_load_lds_dwordx4 v[214:215], off
	v_lshl_add_u64 v[214:215], v[234:235], 0, v[194:195]
	s_mov_b32 m0, s39
	v_lshl_add_u64 v[216:217], s[8:9], 0, v[216:217]
	global_load_lds_dwordx4 v[214:215], off
	v_lshl_add_u64 v[214:215], v[234:235], 0, v[196:197]
	s_mov_b32 m0, s42
	v_readfirstlane_b32 s44, v216
	global_load_lds_dwordx4 v[214:215], off
	v_cndmask_b32_e32 v214, v206, v229, vcc
	v_readfirstlane_b32 s45, v217
	s_mov_b32 m0, s29
	v_cndmask_b32_e32 v215, v208, v230, vcc
	s_add_i32 s85, 0, 0x18000
	s_add_i32 s82, 0, 0x1c000
	s_cmp_gt_u32 s25, 4
	global_load_lds_dwordx4 v214, s[44:45]
	s_mov_b32 m0, s56
	s_cselect_b64 s[38:39], -1, 0
	global_load_lds_dwordx4 v215, s[44:45]
	s_and_b64 s[42:43], s[38:39], exec
	s_cselect_b32 s26, -5, 3
	s_add_i32 s42, s26, s25
	s_ashr_i32 s43, s42, 31
	s_add_i32 s84, s85, s7
	s_add_i32 s26, s82, s7
	v_cndmask_b32_e64 v215, v213, v205, s[38:39]
	v_cndmask_b32_e64 v214, v212, v204, s[38:39]
	s_lshl_b64 s[42:43], s[42:43], 7
	s_add_i32 s83, s84, 0x2000
	s_add_i32 s60, s26, 0x2000
	v_lshl_add_u64 v[216:217], v[214:215], 0, s[42:43]
	s_add_u32 s42, s8, s42
	s_waitcnt vmcnt(8)
	s_addc_u32 s43, s9, s43
	s_waitcnt lgkmcnt(0)
	s_add_u32 s34, s34, 0x100
	s_addc_u32 s35, s35, 0
	s_add_i32 s25, s25, 2
	v_lshl_add_u64 v[214:215], v[216:217], 0, s[0:1]
	s_barrier
	s_setprio 1
	s_waitcnt lgkmcnt(0)
	v_mfma_f32_16x16x128_f8f6f4 v[116:119], v[24:31], v[56:63], v[116:119]
	v_mfma_f32_16x16x128_f8f6f4 v[108:111], v[16:23], v[56:63], v[108:111]
	v_mfma_f32_16x16x128_f8f6f4 v[104:107], v[24:31], v[48:55], v[104:107]
	v_mfma_f32_16x16x128_f8f6f4 v[96:99], v[16:23], v[48:55], v[96:99]
	v_mfma_f32_16x16x128_f8f6f4 v[88:91], v[24:31], v[40:47], v[88:91]
	v_mfma_f32_16x16x128_f8f6f4 v[80:83], v[16:23], v[40:47], v[80:83]
	v_mfma_f32_16x16x128_f8f6f4 v[72:75], v[24:31], v[32:39], v[72:75]
	v_mfma_f32_16x16x128_f8f6f4 v[64:67], v[16:23], v[32:39], v[64:67]
	v_mfma_f32_16x16x128_f8f6f4 v[124:127], v[8:15], v[56:63], v[124:127]
	v_mfma_f32_16x16x128_f8f6f4 v[120:123], v[0:7], v[56:63], v[120:123]
	v_mfma_f32_16x16x128_f8f6f4 v[112:115], v[8:15], v[48:55], v[112:115]
	v_mfma_f32_16x16x128_f8f6f4 v[100:103], v[0:7], v[48:55], v[100:103]
	v_mfma_f32_16x16x128_f8f6f4 v[92:95], v[8:15], v[40:47], v[92:95]
	v_mfma_f32_16x16x128_f8f6f4 v[84:87], v[0:7], v[40:47], v[84:87]
	v_mfma_f32_16x16x128_f8f6f4 v[76:79], v[8:15], v[32:39], v[76:79]
	v_mfma_f32_16x16x128_f8f6f4 v[68:71], v[0:7], v[32:39], v[68:71]
	s_setprio 0
	s_barrier
	v_add_u32_e32 v12, s85, v222
	v_add_u32_e32 v28, s82, v222
	ds_read_b128 v[0:3], v12
	ds_read_b128 v[4:7], v12 offset:1024
	ds_read_b128 v[8:11], v12 offset:2048
	ds_read_b128 v[12:15], v12 offset:3072
	ds_read_b128 v[16:19], v28
	ds_read_b128 v[20:23], v28 offset:1024
	ds_read_b128 v[24:27], v28 offset:2048
	ds_read_b128 v[28:31], v28 offset:3072
	s_mov_b32 m0, s57
	v_cndmask_b32_e32 v223, v192, v231, vcc
	ds_read_b128 v[32:35], v226 offset:32768
	ds_read_b128 v[36:39], v226 offset:33792
	ds_read_b128 v[40:43], v226 offset:34816
	ds_read_b128 v[44:47], v226 offset:35840
	ds_read_b128 v[48:51], v226 offset:36864
	ds_read_b128 v[52:55], v226 offset:37888
	ds_read_b128 v[56:59], v226 offset:38912
	ds_read_b128 v[60:63], v226 offset:39936
	v_cndmask_b32_e32 v233, v210, v232, vcc
	global_load_lds_dwordx4 v223, s[44:45]
	s_mov_b32 m0, s58
	s_nop 0
	global_load_lds_dwordx4 v233, s[44:45]
	s_waitcnt vmcnt(8)
	s_waitcnt lgkmcnt(0)
	s_barrier
	s_setprio 1
	s_waitcnt lgkmcnt(0)
	v_mfma_f32_16x16x128_f8f6f4 v[188:191], v[0:7], v[32:39], v[188:191]
	v_mfma_f32_16x16x128_f8f6f4 v[180:183], v[8:15], v[32:39], v[180:183]
	v_mfma_f32_16x16x128_f8f6f4 v[172:175], v[0:7], v[40:47], v[172:175]
	v_mfma_f32_16x16x128_f8f6f4 v[164:167], v[8:15], v[40:47], v[164:167]
	v_mfma_f32_16x16x128_f8f6f4 v[156:159], v[0:7], v[48:55], v[156:159]
	v_mfma_f32_16x16x128_f8f6f4 v[148:151], v[8:15], v[48:55], v[148:151]
	v_mfma_f32_16x16x128_f8f6f4 v[140:143], v[0:7], v[56:63], v[140:143]
	v_mfma_f32_16x16x128_f8f6f4 v[132:135], v[8:15], v[56:63], v[132:135]
	v_mfma_f32_16x16x128_f8f6f4 v[184:187], v[16:23], v[32:39], v[184:187]
	v_mfma_f32_16x16x128_f8f6f4 v[176:179], v[24:31], v[32:39], v[176:179]
	v_mfma_f32_16x16x128_f8f6f4 v[168:171], v[16:23], v[40:47], v[168:171]
	v_mfma_f32_16x16x128_f8f6f4 v[160:163], v[24:31], v[40:47], v[160:163]
	v_mfma_f32_16x16x128_f8f6f4 v[152:155], v[16:23], v[48:55], v[152:155]
	v_mfma_f32_16x16x128_f8f6f4 v[144:147], v[24:31], v[48:55], v[144:147]
	v_mfma_f32_16x16x128_f8f6f4 v[136:139], v[16:23], v[56:63], v[136:139]
	v_mfma_f32_16x16x128_f8f6f4 v[128:131], v[24:31], v[56:63], v[128:131]
	s_setprio 0
	s_barrier
	s_mov_b32 m0, s84
	v_lshl_add_u64 v[234:235], v[216:217], 0, v[194:195]
	ds_read_b128 v[32:35], v226 offset:49152
	ds_read_b128 v[36:39], v226 offset:50176
	ds_read_b128 v[40:43], v226 offset:51200
	ds_read_b128 v[44:47], v226 offset:52224
	ds_read_b128 v[48:51], v226 offset:53248
	ds_read_b128 v[52:55], v226 offset:54272
	ds_read_b128 v[56:59], v226 offset:55296
	ds_read_b128 v[60:63], v226 offset:56320
	global_load_lds_dwordx4 v[234:235], off
	v_lshl_add_u64 v[216:217], v[216:217], 0, v[196:197]
	s_mov_b32 m0, s83
	s_nop 0
	global_load_lds_dwordx4 v[216:217], off
	v_lshl_add_u64 v[216:217], v[214:215], 0, v[194:195]
	s_mov_b32 m0, s26
	v_lshl_add_u64 v[214:215], v[214:215], 0, v[196:197]
	global_load_lds_dwordx4 v[216:217], off
	s_mov_b32 m0, s60
	s_nop 0
	global_load_lds_dwordx4 v[214:215], off
	v_cndmask_b32_e64 v214, v206, v229, s[38:39]
	s_mov_b32 m0, s59
	v_cndmask_b32_e64 v215, v208, v230, s[38:39]
	global_load_lds_dwordx4 v214, s[42:43]
	s_mov_b32 m0, s61
	s_nop 0
	global_load_lds_dwordx4 v215, s[42:43]
	s_waitcnt vmcnt(8)
	s_waitcnt lgkmcnt(0)
	s_barrier
	s_setprio 1
	s_waitcnt lgkmcnt(0)
	v_mfma_f32_16x16x128_f8f6f4 v[116:119], v[0:7], v[32:39], v[116:119]
	v_mfma_f32_16x16x128_f8f6f4 v[108:111], v[8:15], v[32:39], v[108:111]
	v_mfma_f32_16x16x128_f8f6f4 v[104:107], v[0:7], v[40:47], v[104:107]
	v_mfma_f32_16x16x128_f8f6f4 v[96:99], v[8:15], v[40:47], v[96:99]
	v_mfma_f32_16x16x128_f8f6f4 v[88:91], v[0:7], v[48:55], v[88:91]
	v_mfma_f32_16x16x128_f8f6f4 v[80:83], v[8:15], v[48:55], v[80:83]
	v_mfma_f32_16x16x128_f8f6f4 v[72:75], v[0:7], v[56:63], v[72:75]
	v_mfma_f32_16x16x128_f8f6f4 v[64:67], v[8:15], v[56:63], v[64:67]
	v_mfma_f32_16x16x128_f8f6f4 v[124:127], v[16:23], v[32:39], v[124:127]
	v_mfma_f32_16x16x128_f8f6f4 v[120:123], v[24:31], v[32:39], v[120:123]
	v_mfma_f32_16x16x128_f8f6f4 v[112:115], v[16:23], v[40:47], v[112:115]
	v_mfma_f32_16x16x128_f8f6f4 v[100:103], v[24:31], v[40:47], v[100:103]
	v_mfma_f32_16x16x128_f8f6f4 v[92:95], v[16:23], v[48:55], v[92:95]
	v_mfma_f32_16x16x128_f8f6f4 v[84:87], v[24:31], v[48:55], v[84:87]
	v_mfma_f32_16x16x128_f8f6f4 v[76:79], v[16:23], v[56:63], v[76:79]
	v_mfma_f32_16x16x128_f8f6f4 v[68:71], v[24:31], v[56:63], v[68:71]
	s_setprio 0
	s_barrier
	s_andn2_b64 vcc, exec, s[40:41]
	s_cbranch_vccnz .LBB0_1185

.LBB0_1263:
	ds_read_b128 v[24:27], v231
	ds_read_b128 v[28:31], v231 offset:1024
	ds_read_b128 v[16:19], v231 offset:2048
	ds_read_b128 v[20:23], v231 offset:3072
	ds_read_b128 v[8:11], v237
	ds_read_b128 v[12:15], v237 offset:1024
	ds_read_b128 v[0:3], v237 offset:2048
	ds_read_b128 v[4:7], v237 offset:3072
	s_add_i32 m0, s68, 0xc000
	ds_read_b128 v[166:169], v243
	ds_read_b128 v[170:173], v243 offset:1024
	ds_read_b128 v[174:177], v243 offset:2048
	ds_read_b128 v[178:181], v243 offset:3072
	ds_read_b128 v[182:185], v243 offset:4096
	ds_read_b128 v[186:189], v243 offset:5120
	ds_read_b128 v[216:219], v243 offset:6144
	ds_read_b128 v[220:223], v243 offset:7168
	global_load_lds_dwordx4 v[162:163], off
	s_add_i32 m0, s68, 0xe000
	s_nop 0
	global_load_lds_dwordx4 v[164:165], off
	s_waitcnt vmcnt(8)
	s_waitcnt lgkmcnt(0)
	s_barrier
	s_setprio 1
	s_waitcnt lgkmcnt(0)
	v_mfma_f32_16x16x128_f8f6f4 v[156:159], v[24:31], v[166:173], v[156:159]
	v_mfma_f32_16x16x128_f8f6f4 v[152:155], v[16:23], v[166:173], v[152:155]
	v_mfma_f32_16x16x128_f8f6f4 v[140:143], v[24:31], v[174:181], v[140:143]
	v_mfma_f32_16x16x128_f8f6f4 v[136:139], v[16:23], v[174:181], v[136:139]
	v_mfma_f32_16x16x128_f8f6f4 v[124:127], v[24:31], v[182:189], v[124:127]
	v_mfma_f32_16x16x128_f8f6f4 v[120:123], v[16:23], v[182:189], v[120:123]
	v_mfma_f32_16x16x128_f8f6f4 v[108:111], v[24:31], v[216:223], v[108:111]
	v_mfma_f32_16x16x128_f8f6f4 v[104:107], v[16:23], v[216:223], v[104:107]
	v_mfma_f32_16x16x128_f8f6f4 v[148:151], v[8:15], v[166:173], v[148:151]
	v_mfma_f32_16x16x128_f8f6f4 v[144:147], v[0:7], v[166:173], v[144:147]
	v_mfma_f32_16x16x128_f8f6f4 v[132:135], v[8:15], v[174:181], v[132:135]
	v_mfma_f32_16x16x128_f8f6f4 v[128:131], v[0:7], v[174:181], v[128:131]
	v_mfma_f32_16x16x128_f8f6f4 v[116:119], v[8:15], v[182:189], v[116:119]
	v_mfma_f32_16x16x128_f8f6f4 v[112:115], v[0:7], v[182:189], v[112:115]
	v_mfma_f32_16x16x128_f8f6f4 v[100:103], v[8:15], v[216:223], v[100:103]
	v_mfma_f32_16x16x128_f8f6f4 v[96:99], v[0:7], v[216:223], v[96:99]
	s_setprio 0
	s_barrier
	s_cmp_gt_u32 s43, 25
	v_sub_co_u32_e64 v200, s[40:41], s43, 26
	s_cselect_b64 vcc, -1, 0
	v_add_u32_e32 v210, 28, v200
	v_cndmask_b32_e32 v224, v210, v200, vcc
	v_ashrrev_i32_e32 v225, 31, v224
	v_cndmask_b32_e32 v191, v161, v209, vcc
	v_cndmask_b32_e32 v190, v160, v208, vcc
	v_lshlrev_b64 v[224:225], 7, v[224:225]
	v_lshl_add_u64 v[190:191], v[190:191], 0, v[224:225]
	s_add_i32 s44, s24, s66
	v_lshl_add_u64 v[228:229], v[190:191], 0, v[194:195]
	s_mov_b32 m0, s44
	ds_read_b128 v[166:169], v243 offset:16384
	ds_read_b128 v[170:173], v243 offset:17408
	ds_read_b128 v[174:177], v243 offset:18432
	ds_read_b128 v[178:181], v243 offset:19456
	ds_read_b128 v[182:185], v243 offset:20480
	ds_read_b128 v[186:189], v243 offset:21504
	ds_read_b128 v[216:219], v243 offset:22528
	ds_read_b128 v[220:223], v243 offset:23552
	global_load_lds_dwordx4 v[228:229], off
	v_lshl_add_u64 v[228:229], v[190:191], 0, v[198:199]
	s_add_i32 m0, s44, 0x2000
	v_lshl_add_u64 v[190:191], v[190:191], 0, s[0:1]
	s_add_i32 s44, s80, s66
	global_load_lds_dwordx4 v[228:229], off
	v_lshl_add_u64 v[228:229], v[190:191], 0, v[194:195]
	s_mov_b32 m0, s44
	v_lshl_add_u64 v[190:191], v[190:191], 0, v[198:199]
	global_load_lds_dwordx4 v[228:229], off
	s_add_i32 m0, s44, 0x2000
	s_and_b64 s[44:45], vcc, exec
	s_cselect_b32 s45, s63, s39
	s_cselect_b32 s44, s62, s38
	global_load_lds_dwordx4 v[190:191], off
	v_lshl_add_u64 v[190:191], s[44:45], 0, v[224:225]
	v_lshl_add_u64 v[224:225], v[190:191], 0, v[192:193]
	s_mov_b32 m0, s68
	s_nop 0
	global_load_lds_dwordx4 v[224:225], off
	v_lshl_add_u64 v[224:225], v[190:191], 0, v[196:197]
	s_mov_b32 m0, s69
	s_nop 0
	global_load_lds_dwordx4 v[224:225], off
	s_waitcnt vmcnt(8)
	s_waitcnt lgkmcnt(0)
	s_barrier
	s_setprio 1
	s_waitcnt lgkmcnt(0)
	v_mfma_f32_16x16x128_f8f6f4 v[92:95], v[24:31], v[166:173], v[92:95]
	v_mfma_f32_16x16x128_f8f6f4 v[88:91], v[16:23], v[166:173], v[88:91]
	v_mfma_f32_16x16x128_f8f6f4 v[76:79], v[24:31], v[174:181], v[76:79]
	v_mfma_f32_16x16x128_f8f6f4 v[72:75], v[16:23], v[174:181], v[72:75]
	v_mfma_f32_16x16x128_f8f6f4 v[52:55], v[24:31], v[182:189], v[52:55]
	v_mfma_f32_16x16x128_f8f6f4 v[48:51], v[16:23], v[182:189], v[48:51]
	v_mfma_f32_16x16x128_f8f6f4 v[36:39], v[24:31], v[216:223], v[36:39]
	v_mfma_f32_16x16x128_f8f6f4 v[32:35], v[16:23], v[216:223], v[32:35]
	v_mfma_f32_16x16x128_f8f6f4 v[84:87], v[8:15], v[166:173], v[84:87]
	v_mfma_f32_16x16x128_f8f6f4 v[80:83], v[0:7], v[166:173], v[80:83]
	v_mfma_f32_16x16x128_f8f6f4 v[60:63], v[8:15], v[174:181], v[60:63]
	v_mfma_f32_16x16x128_f8f6f4 v[56:59], v[0:7], v[174:181], v[56:59]
	v_mfma_f32_16x16x128_f8f6f4 v[68:71], v[8:15], v[182:189], v[68:71]
	v_mfma_f32_16x16x128_f8f6f4 v[64:67], v[0:7], v[182:189], v[64:67]
	v_mfma_f32_16x16x128_f8f6f4 v[44:47], v[8:15], v[216:223], v[44:47]
	v_mfma_f32_16x16x128_f8f6f4 v[40:43], v[0:7], v[216:223], v[40:43]
	s_setprio 0
	s_barrier
	s_add_i32 s46, 0, 0x18000
	s_add_i32 s47, 0, 0x1c000
	v_add_u32_e32 v0, s46, v215
	v_add_u32_e32 v4, s47, v215
	ds_read_b128 v[16:19], v0
	ds_read_b128 v[20:23], v0 offset:1024
	ds_read_b128 v[24:27], v0 offset:2048
	ds_read_b128 v[28:31], v0 offset:3072
	ds_read_b128 v[8:11], v4
	ds_read_b128 v[12:15], v4 offset:1024
	ds_read_b128 v[0:3], v4 offset:2048
	ds_read_b128 v[4:7], v4 offset:3072
	v_lshl_add_u64 v[190:191], v[190:191], 0, s[0:1]
	s_mov_b32 m0, s70
	v_lshl_add_u64 v[224:225], v[190:191], 0, v[192:193]
	ds_read_b128 v[166:169], v243 offset:32768
	ds_read_b128 v[170:173], v243 offset:33792
	ds_read_b128 v[174:177], v243 offset:34816
	ds_read_b128 v[178:181], v243 offset:35840
	ds_read_b128 v[182:185], v243 offset:36864
	ds_read_b128 v[186:189], v243 offset:37888
	ds_read_b128 v[216:219], v243 offset:38912
	ds_read_b128 v[220:223], v243 offset:39936
	global_load_lds_dwordx4 v[224:225], off
	v_lshl_add_u64 v[190:191], v[190:191], 0, v[196:197]
	s_mov_b32 m0, s71
	s_nop 0
	global_load_lds_dwordx4 v[190:191], off
	s_waitcnt vmcnt(8)
	s_waitcnt lgkmcnt(0)
	s_barrier
	s_setprio 1
	s_waitcnt lgkmcnt(0)
	v_mfma_f32_16x16x128_f8f6f4 v[156:159], v[16:23], v[166:173], v[156:159]
	v_mfma_f32_16x16x128_f8f6f4 v[152:155], v[24:31], v[166:173], v[152:155]
	v_mfma_f32_16x16x128_f8f6f4 v[140:143], v[16:23], v[174:181], v[140:143]
	v_mfma_f32_16x16x128_f8f6f4 v[136:139], v[24:31], v[174:181], v[136:139]
	v_mfma_f32_16x16x128_f8f6f4 v[124:127], v[16:23], v[182:189], v[124:127]
	v_mfma_f32_16x16x128_f8f6f4 v[120:123], v[24:31], v[182:189], v[120:123]
	v_mfma_f32_16x16x128_f8f6f4 v[108:111], v[16:23], v[216:223], v[108:111]
	v_mfma_f32_16x16x128_f8f6f4 v[104:107], v[24:31], v[216:223], v[104:107]
	v_mfma_f32_16x16x128_f8f6f4 v[148:151], v[8:15], v[166:173], v[148:151]
	v_mfma_f32_16x16x128_f8f6f4 v[144:147], v[0:7], v[166:173], v[144:147]
	v_mfma_f32_16x16x128_f8f6f4 v[132:135], v[8:15], v[174:181], v[132:135]
	v_mfma_f32_16x16x128_f8f6f4 v[128:131], v[0:7], v[174:181], v[128:131]
	v_mfma_f32_16x16x128_f8f6f4 v[116:119], v[8:15], v[182:189], v[116:119]
	v_mfma_f32_16x16x128_f8f6f4 v[112:115], v[0:7], v[182:189], v[112:115]
	v_mfma_f32_16x16x128_f8f6f4 v[100:103], v[8:15], v[216:223], v[100:103]
	v_mfma_f32_16x16x128_f8f6f4 v[96:99], v[0:7], v[216:223], v[96:99]
	s_setprio 0
	s_barrier
	s_cmp_gt_u32 s43, 24
	s_cselect_b64 vcc, -1, 0
	s_and_b64 s[44:45], vcc, exec
	s_cselect_b32 s44, 0xffffffe7, 3
	s_add_i32 s44, s44, s43
	s_ashr_i32 s45, s44, 31
	v_cndmask_b32_e32 v191, v161, v209, vcc
	v_cndmask_b32_e32 v190, v160, v208, vcc
	s_lshl_b64 s[44:45], s[44:45], 7
	v_lshl_add_u64 v[190:191], v[190:191], 0, s[44:45]
	s_add_i32 s46, s46, s66
	v_lshl_add_u64 v[224:225], v[190:191], 0, v[194:195]
	s_mov_b32 m0, s46
	ds_read_b128 v[166:169], v243 offset:49152
	ds_read_b128 v[170:173], v243 offset:50176
	ds_read_b128 v[174:177], v243 offset:51200
	ds_read_b128 v[178:181], v243 offset:52224
	ds_read_b128 v[182:185], v243 offset:53248
	ds_read_b128 v[186:189], v243 offset:54272
	ds_read_b128 v[216:219], v243 offset:55296
	ds_read_b128 v[220:223], v243 offset:56320
	global_load_lds_dwordx4 v[224:225], off
	v_lshl_add_u64 v[224:225], v[190:191], 0, v[198:199]
	s_add_i32 m0, s46, 0x2000
	v_lshl_add_u64 v[190:191], v[190:191], 0, s[0:1]
	s_add_i32 s46, s47, s66
	global_load_lds_dwordx4 v[224:225], off
	v_lshl_add_u64 v[224:225], v[190:191], 0, v[194:195]
	s_mov_b32 m0, s46
	v_lshl_add_u64 v[190:191], v[190:191], 0, v[198:199]
	global_load_lds_dwordx4 v[224:225], off
	s_add_i32 m0, s46, 0x2000
	s_and_b64 s[46:47], vcc, exec
	s_cselect_b32 s47, s62, s38
	s_cselect_b32 s46, s63, s39
	s_add_u32 s44, s47, s44
	s_addc_u32 s45, s46, s45
	global_load_lds_dwordx4 v[190:191], off
	v_lshl_add_u64 v[190:191], s[44:45], 0, v[192:193]
	s_mov_b32 m0, s78
	s_nop 0
	global_load_lds_dwordx4 v[190:191], off
	v_lshl_add_u64 v[190:191], s[44:45], 0, v[196:197]
	s_mov_b32 m0, s79
	s_nop 0
	global_load_lds_dwordx4 v[190:191], off
	s_waitcnt vmcnt(8)
	s_waitcnt lgkmcnt(0)
	s_barrier
	s_setprio 1
	s_waitcnt lgkmcnt(0)
	v_mfma_f32_16x16x128_f8f6f4 v[92:95], v[16:23], v[166:173], v[92:95]
	v_mfma_f32_16x16x128_f8f6f4 v[88:91], v[24:31], v[166:173], v[88:91]
	v_mfma_f32_16x16x128_f8f6f4 v[76:79], v[16:23], v[174:181], v[76:79]
	v_mfma_f32_16x16x128_f8f6f4 v[72:75], v[24:31], v[174:181], v[72:75]
	v_mfma_f32_16x16x128_f8f6f4 v[52:55], v[16:23], v[182:189], v[52:55]
	v_mfma_f32_16x16x128_f8f6f4 v[48:51], v[24:31], v[182:189], v[48:51]
	v_mfma_f32_16x16x128_f8f6f4 v[36:39], v[16:23], v[216:223], v[36:39]
	v_mfma_f32_16x16x128_f8f6f4 v[32:35], v[24:31], v[216:223], v[32:35]
	v_mfma_f32_16x16x128_f8f6f4 v[84:87], v[8:15], v[166:173], v[84:87]
	v_mfma_f32_16x16x128_f8f6f4 v[80:83], v[0:7], v[166:173], v[80:83]
	v_mfma_f32_16x16x128_f8f6f4 v[60:63], v[8:15], v[174:181], v[60:63]
	v_mfma_f32_16x16x128_f8f6f4 v[56:59], v[0:7], v[174:181], v[56:59]
	v_mfma_f32_16x16x128_f8f6f4 v[68:71], v[8:15], v[182:189], v[68:71]
	v_mfma_f32_16x16x128_f8f6f4 v[64:67], v[0:7], v[182:189], v[64:67]
	v_mfma_f32_16x16x128_f8f6f4 v[44:47], v[8:15], v[216:223], v[44:47]
	v_mfma_f32_16x16x128_f8f6f4 v[40:43], v[0:7], v[216:223], v[40:43]
	s_setprio 0
	s_barrier
	v_lshl_add_u64 v[162:163], v[162:163], 0, s[34:35]
	v_lshl_add_u64 v[164:165], v[164:165], 0, s[34:35]
	s_add_i32 s43, s43, 2
	s_and_b64 vcc, exec, s[40:41]
	s_cbranch_vccnz .LBB0_1263
	s_andn2_b64 vcc, exec, s[30:31]
	s_cbranch_vccnz .LBB0_1266
	s_barrier

.LBB0_1292:
	v_add_u32_e32 v0, s78, v186
	v_add_u32_e32 v4, s79, v186
	ds_read_b128 v[24:27], v0
	ds_read_b128 v[28:31], v0 offset:1024
	ds_read_b128 v[16:19], v0 offset:2048
	ds_read_b128 v[20:23], v0 offset:3072
	ds_read_b128 v[8:11], v4
	ds_read_b128 v[12:15], v4 offset:1024
	ds_read_b128 v[0:3], v4 offset:2048
	ds_read_b128 v[4:7], v4 offset:3072
	v_lshl_add_u64 v[228:229], s[42:43], 0, v[160:161]
	s_add_i32 m0, s39, 0xc000
	ds_read_b128 v[196:199], v189
	ds_read_b128 v[200:203], v189 offset:1024
	ds_read_b128 v[204:207], v189 offset:2048
	ds_read_b128 v[208:211], v189 offset:3072
	ds_read_b128 v[212:215], v189 offset:4096
	ds_read_b128 v[216:219], v189 offset:5120
	ds_read_b128 v[220:223], v189 offset:6144
	ds_read_b128 v[224:227], v189 offset:7168
	global_load_lds_dwordx4 v[228:229], off
	v_lshl_add_u64 v[228:229], s[42:43], 0, v[178:179]
	s_add_i32 m0, s39, 0xe000
	s_nop 0
	global_load_lds_dwordx4 v[228:229], off
	s_waitcnt vmcnt(8)
	s_waitcnt lgkmcnt(0)
	s_barrier
	s_setprio 1
	s_waitcnt lgkmcnt(0)
	v_mfma_f32_16x16x128_f8f6f4 v[156:159], v[24:31], v[196:203], v[156:159]
	v_mfma_f32_16x16x128_f8f6f4 v[148:151], v[16:23], v[196:203], v[148:151]
	v_mfma_f32_16x16x128_f8f6f4 v[140:143], v[24:31], v[204:211], v[140:143]
	v_mfma_f32_16x16x128_f8f6f4 v[132:135], v[16:23], v[204:211], v[132:135]
	v_mfma_f32_16x16x128_f8f6f4 v[124:127], v[24:31], v[212:219], v[124:127]
	v_mfma_f32_16x16x128_f8f6f4 v[116:119], v[16:23], v[212:219], v[116:119]
	v_mfma_f32_16x16x128_f8f6f4 v[108:111], v[24:31], v[220:227], v[108:111]
	v_mfma_f32_16x16x128_f8f6f4 v[100:103], v[16:23], v[220:227], v[100:103]
	v_mfma_f32_16x16x128_f8f6f4 v[152:155], v[8:15], v[196:203], v[152:155]
	v_mfma_f32_16x16x128_f8f6f4 v[144:147], v[0:7], v[196:203], v[144:147]
	v_mfma_f32_16x16x128_f8f6f4 v[136:139], v[8:15], v[204:211], v[136:139]
	v_mfma_f32_16x16x128_f8f6f4 v[128:131], v[0:7], v[204:211], v[128:131]
	v_mfma_f32_16x16x128_f8f6f4 v[120:123], v[8:15], v[212:219], v[120:123]
	v_mfma_f32_16x16x128_f8f6f4 v[112:115], v[0:7], v[212:219], v[112:115]
	v_mfma_f32_16x16x128_f8f6f4 v[104:107], v[8:15], v[220:227], v[104:107]
	v_mfma_f32_16x16x128_f8f6f4 v[96:99], v[0:7], v[220:227], v[96:99]
	s_setprio 0
	s_barrier
	s_cmp_gt_u32 s31, 5
	v_sub_co_u32_e64 v230, s[44:45], s31, 6
	s_cselect_b64 vcc, -1, 0
	v_add_u32_e32 v231, 8, v230
	v_cndmask_b32_e32 v230, v231, v230, vcc
	v_ashrrev_i32_e32 v231, 31, v230
	v_cndmask_b32_e32 v229, v181, v173, vcc
	v_cndmask_b32_e32 v228, v180, v172, vcc
	v_lshlrev_b64 v[230:231], 7, v[230:231]
	v_lshl_add_u64 v[228:229], v[228:229], 0, v[230:231]
	s_add_i32 s34, s78, s7
	v_lshl_add_u64 v[232:233], v[228:229], 0, v[162:163]
	s_mov_b32 m0, s34
	ds_read_b128 v[196:199], v189 offset:16384
	ds_read_b128 v[200:203], v189 offset:17408
	ds_read_b128 v[204:207], v189 offset:18432
	ds_read_b128 v[208:211], v189 offset:19456
	ds_read_b128 v[212:215], v189 offset:20480
	ds_read_b128 v[216:219], v189 offset:21504
	ds_read_b128 v[220:223], v189 offset:22528
	ds_read_b128 v[224:227], v189 offset:23552
	global_load_lds_dwordx4 v[232:233], off
	v_lshl_add_u64 v[232:233], v[228:229], 0, v[164:165]
	s_add_i32 m0, s34, 0x2000
	v_lshl_add_u64 v[228:229], v[228:229], 0, s[22:23]
	s_add_i32 s34, s79, s7
	global_load_lds_dwordx4 v[232:233], off
	v_lshl_add_u64 v[232:233], v[228:229], 0, v[162:163]
	s_mov_b32 m0, s34
	v_lshl_add_u64 v[228:229], v[228:229], 0, v[164:165]
	global_load_lds_dwordx4 v[232:233], off
	s_add_i32 m0, s34, 0x2000
	s_nop 0
	global_load_lds_dwordx4 v[228:229], off
	v_lshl_add_u64 v[228:229], s[8:9], 0, v[230:231]
	v_cndmask_b32_e32 v230, v174, v192, vcc
	v_readfirstlane_b32 s46, v228
	v_readfirstlane_b32 s47, v229
	s_mov_b32 m0, s39
	v_cndmask_b32_e32 v231, v176, v193, vcc
	s_nop 2
	global_load_lds_dwordx4 v230, s[46:47]
	s_mov_b32 m0, s56
	s_nop 0
	global_load_lds_dwordx4 v231, s[46:47]
	s_waitcnt vmcnt(8)
	s_waitcnt lgkmcnt(0)
	s_barrier
	s_setprio 1
	s_waitcnt lgkmcnt(0)
	v_mfma_f32_16x16x128_f8f6f4 v[84:87], v[24:31], v[196:203], v[84:87]
	v_mfma_f32_16x16x128_f8f6f4 v[76:79], v[16:23], v[196:203], v[76:79]
	v_mfma_f32_16x16x128_f8f6f4 v[72:75], v[24:31], v[204:211], v[72:75]
	v_mfma_f32_16x16x128_f8f6f4 v[64:67], v[16:23], v[204:211], v[64:67]
	v_mfma_f32_16x16x128_f8f6f4 v[56:59], v[24:31], v[212:219], v[56:59]
	v_mfma_f32_16x16x128_f8f6f4 v[48:51], v[16:23], v[212:219], v[48:51]
	v_mfma_f32_16x16x128_f8f6f4 v[40:43], v[24:31], v[220:227], v[40:43]
	v_mfma_f32_16x16x128_f8f6f4 v[32:35], v[16:23], v[220:227], v[32:35]
	v_mfma_f32_16x16x128_f8f6f4 v[92:95], v[8:15], v[196:203], v[92:95]
	v_mfma_f32_16x16x128_f8f6f4 v[88:91], v[0:7], v[196:203], v[88:91]
	v_mfma_f32_16x16x128_f8f6f4 v[80:83], v[8:15], v[204:211], v[80:83]
	v_mfma_f32_16x16x128_f8f6f4 v[68:71], v[0:7], v[204:211], v[68:71]
	v_mfma_f32_16x16x128_f8f6f4 v[60:63], v[8:15], v[212:219], v[60:63]
	v_mfma_f32_16x16x128_f8f6f4 v[52:55], v[0:7], v[212:219], v[52:55]
	v_mfma_f32_16x16x128_f8f6f4 v[44:47], v[8:15], v[220:227], v[44:47]
	v_mfma_f32_16x16x128_f8f6f4 v[36:39], v[0:7], v[220:227], v[36:39]
	s_setprio 0
	s_barrier
	s_add_i32 s34, 0, 0x18000
	s_add_i32 s85, 0, 0x1c000
	v_add_u32_e32 v0, s34, v186
	v_add_u32_e32 v4, s85, v186
	ds_read_b128 v[16:19], v0
	ds_read_b128 v[20:23], v0 offset:1024
	ds_read_b128 v[24:27], v0 offset:2048
	ds_read_b128 v[28:31], v0 offset:3072
	ds_read_b128 v[8:11], v4
	ds_read_b128 v[12:15], v4 offset:1024
	ds_read_b128 v[0:3], v4 offset:2048
	ds_read_b128 v[4:7], v4 offset:3072
	s_mov_b32 m0, s57
	v_cndmask_b32_e32 v228, v160, v194, vcc
	ds_read_b128 v[196:199], v189 offset:32768
	ds_read_b128 v[200:203], v189 offset:33792
	ds_read_b128 v[204:207], v189 offset:34816
	ds_read_b128 v[208:211], v189 offset:35840
	ds_read_b128 v[212:215], v189 offset:36864
	ds_read_b128 v[216:219], v189 offset:37888
	ds_read_b128 v[220:223], v189 offset:38912
	ds_read_b128 v[224:227], v189 offset:39936
	v_cndmask_b32_e32 v229, v178, v195, vcc
	global_load_lds_dwordx4 v228, s[46:47]
	s_mov_b32 m0, s66
	s_nop 0
	global_load_lds_dwordx4 v229, s[46:47]
	s_waitcnt vmcnt(8)
	s_waitcnt lgkmcnt(0)
	s_barrier
	s_setprio 1
	s_waitcnt lgkmcnt(0)
	v_mfma_f32_16x16x128_f8f6f4 v[156:159], v[16:23], v[196:203], v[156:159]
	v_mfma_f32_16x16x128_f8f6f4 v[148:151], v[24:31], v[196:203], v[148:151]
	v_mfma_f32_16x16x128_f8f6f4 v[140:143], v[16:23], v[204:211], v[140:143]
	v_mfma_f32_16x16x128_f8f6f4 v[132:135], v[24:31], v[204:211], v[132:135]
	v_mfma_f32_16x16x128_f8f6f4 v[124:127], v[16:23], v[212:219], v[124:127]
	v_mfma_f32_16x16x128_f8f6f4 v[116:119], v[24:31], v[212:219], v[116:119]
	v_mfma_f32_16x16x128_f8f6f4 v[108:111], v[16:23], v[220:227], v[108:111]
	v_mfma_f32_16x16x128_f8f6f4 v[100:103], v[24:31], v[220:227], v[100:103]
	v_mfma_f32_16x16x128_f8f6f4 v[152:155], v[8:15], v[196:203], v[152:155]
	v_mfma_f32_16x16x128_f8f6f4 v[144:147], v[0:7], v[196:203], v[144:147]
	v_mfma_f32_16x16x128_f8f6f4 v[136:139], v[8:15], v[204:211], v[136:139]
	v_mfma_f32_16x16x128_f8f6f4 v[128:131], v[0:7], v[204:211], v[128:131]
	v_mfma_f32_16x16x128_f8f6f4 v[120:123], v[8:15], v[212:219], v[120:123]
	v_mfma_f32_16x16x128_f8f6f4 v[112:115], v[0:7], v[212:219], v[112:115]
	v_mfma_f32_16x16x128_f8f6f4 v[104:107], v[8:15], v[220:227], v[104:107]
	v_mfma_f32_16x16x128_f8f6f4 v[96:99], v[0:7], v[220:227], v[96:99]
	s_setprio 0
	s_barrier
	s_cmp_gt_u32 s31, 4
	s_cselect_b64 vcc, -1, 0
	s_and_b64 s[46:47], vcc, exec
	s_cselect_b32 s46, -5, 3
	s_add_i32 s46, s46, s31
	s_ashr_i32 s47, s46, 31
	v_cndmask_b32_e32 v229, v181, v173, vcc
	v_cndmask_b32_e32 v228, v180, v172, vcc
	s_lshl_b64 s[46:47], s[46:47], 7
	v_lshl_add_u64 v[228:229], v[228:229], 0, s[46:47]
	s_add_i32 s34, s34, s7
	v_lshl_add_u64 v[230:231], v[228:229], 0, v[162:163]
	s_mov_b32 m0, s34
	ds_read_b128 v[196:199], v189 offset:49152
	ds_read_b128 v[200:203], v189 offset:50176
	ds_read_b128 v[204:207], v189 offset:51200
	ds_read_b128 v[208:211], v189 offset:52224
	ds_read_b128 v[212:215], v189 offset:53248
	ds_read_b128 v[216:219], v189 offset:54272
	ds_read_b128 v[220:223], v189 offset:55296
	ds_read_b128 v[224:227], v189 offset:56320
	global_load_lds_dwordx4 v[230:231], off
	v_lshl_add_u64 v[230:231], v[228:229], 0, v[164:165]
	s_add_i32 m0, s34, 0x2000
	v_lshl_add_u64 v[228:229], v[228:229], 0, s[22:23]
	s_add_i32 s34, s85, s7
	global_load_lds_dwordx4 v[230:231], off
	v_lshl_add_u64 v[230:231], v[228:229], 0, v[162:163]
	s_mov_b32 m0, s34
	v_lshl_add_u64 v[228:229], v[228:229], 0, v[164:165]
	global_load_lds_dwordx4 v[230:231], off
	s_add_i32 m0, s34, 0x2000
	s_add_u32 s46, s8, s46
	global_load_lds_dwordx4 v[228:229], off
	s_addc_u32 s47, s9, s47
	v_cndmask_b32_e32 v228, v174, v192, vcc
	s_mov_b32 m0, s67
	v_cndmask_b32_e32 v229, v176, v193, vcc
	global_load_lds_dwordx4 v228, s[46:47]
	s_mov_b32 m0, s68
	s_nop 0
	global_load_lds_dwordx4 v229, s[46:47]
	s_waitcnt vmcnt(8)
	s_waitcnt lgkmcnt(0)
	s_barrier
	s_setprio 1
	s_waitcnt lgkmcnt(0)
	v_mfma_f32_16x16x128_f8f6f4 v[84:87], v[16:23], v[196:203], v[84:87]
	v_mfma_f32_16x16x128_f8f6f4 v[76:79], v[24:31], v[196:203], v[76:79]
	v_mfma_f32_16x16x128_f8f6f4 v[72:75], v[16:23], v[204:211], v[72:75]
	v_mfma_f32_16x16x128_f8f6f4 v[64:67], v[24:31], v[204:211], v[64:67]
	v_mfma_f32_16x16x128_f8f6f4 v[56:59], v[16:23], v[212:219], v[56:59]
	v_mfma_f32_16x16x128_f8f6f4 v[48:51], v[24:31], v[212:219], v[48:51]
	v_mfma_f32_16x16x128_f8f6f4 v[40:43], v[16:23], v[220:227], v[40:43]
	v_mfma_f32_16x16x128_f8f6f4 v[32:35], v[24:31], v[220:227], v[32:35]
	v_mfma_f32_16x16x128_f8f6f4 v[92:95], v[8:15], v[196:203], v[92:95]
	v_mfma_f32_16x16x128_f8f6f4 v[88:91], v[0:7], v[196:203], v[88:91]
	v_mfma_f32_16x16x128_f8f6f4 v[80:83], v[8:15], v[204:211], v[80:83]
	v_mfma_f32_16x16x128_f8f6f4 v[68:71], v[0:7], v[204:211], v[68:71]
	v_mfma_f32_16x16x128_f8f6f4 v[60:63], v[8:15], v[212:219], v[60:63]
	v_mfma_f32_16x16x128_f8f6f4 v[52:55], v[0:7], v[212:219], v[52:55]
	v_mfma_f32_16x16x128_f8f6f4 v[44:47], v[8:15], v[220:227], v[44:47]
	v_mfma_f32_16x16x128_f8f6f4 v[36:39], v[0:7], v[220:227], v[36:39]
	s_setprio 0
	s_barrier
	s_add_u32 s42, s42, 0x100
	s_addc_u32 s43, s43, 0
	s_add_i32 s31, s31, 2
	s_and_b64 vcc, exec, s[44:45]
	s_cbranch_vccz .LBB0_1295

.LBB0_1373:
	ds_read_b128 v[24:27], v217
	ds_read_b128 v[28:31], v217 offset:1024
	ds_read_b128 v[16:19], v217 offset:2048
	ds_read_b128 v[20:23], v217 offset:3072
	ds_read_b128 v[8:11], v221
	ds_read_b128 v[12:15], v221 offset:1024
	ds_read_b128 v[0:3], v221 offset:2048
	ds_read_b128 v[4:7], v221 offset:3072
	s_add_i32 m0, s70, 0xc000
	ds_read_b128 v[166:169], v225
	ds_read_b128 v[170:173], v225 offset:1024
	ds_read_b128 v[174:177], v225 offset:2048
	ds_read_b128 v[178:181], v225 offset:3072
	ds_read_b128 v[226:229], v225 offset:4096
	ds_read_b128 v[230:233], v225 offset:5120
	ds_read_b128 v[238:241], v225 offset:6144
	ds_read_b128 v[242:245], v225 offset:7168
	global_load_lds_dwordx4 v[162:163], off
	s_add_i32 m0, s70, 0xe000
	s_nop 0
	global_load_lds_dwordx4 v[164:165], off
	s_waitcnt vmcnt(8)
	s_waitcnt lgkmcnt(0)
	s_barrier
	s_setprio 1
	s_waitcnt lgkmcnt(0)
	v_mfma_f32_16x16x128_f8f6f4 v[156:159], v[24:31], v[166:173], v[156:159]
	v_mfma_f32_16x16x128_f8f6f4 v[152:155], v[16:23], v[166:173], v[152:155]
	v_mfma_f32_16x16x128_f8f6f4 v[140:143], v[24:31], v[174:181], v[140:143]
	v_mfma_f32_16x16x128_f8f6f4 v[136:139], v[16:23], v[174:181], v[136:139]
	v_mfma_f32_16x16x128_f8f6f4 v[124:127], v[24:31], v[226:233], v[124:127]
	v_mfma_f32_16x16x128_f8f6f4 v[120:123], v[16:23], v[226:233], v[120:123]
	v_mfma_f32_16x16x128_f8f6f4 v[108:111], v[24:31], v[238:245], v[108:111]
	v_mfma_f32_16x16x128_f8f6f4 v[104:107], v[16:23], v[238:245], v[104:107]
	v_mfma_f32_16x16x128_f8f6f4 v[148:151], v[8:15], v[166:173], v[148:151]
	v_mfma_f32_16x16x128_f8f6f4 v[144:147], v[0:7], v[166:173], v[144:147]
	v_mfma_f32_16x16x128_f8f6f4 v[132:135], v[8:15], v[174:181], v[132:135]
	v_mfma_f32_16x16x128_f8f6f4 v[128:131], v[0:7], v[174:181], v[128:131]
	v_mfma_f32_16x16x128_f8f6f4 v[116:119], v[8:15], v[226:233], v[116:119]
	v_mfma_f32_16x16x128_f8f6f4 v[112:115], v[0:7], v[226:233], v[112:115]
	v_mfma_f32_16x16x128_f8f6f4 v[100:103], v[8:15], v[238:245], v[100:103]
	v_mfma_f32_16x16x128_f8f6f4 v[96:99], v[0:7], v[238:245], v[96:99]
	s_setprio 0
	s_barrier
	s_cmp_gt_u32 s39, 25
	v_sub_co_u32_e64 v192, s[30:31], s39, 26
	s_cselect_b64 vcc, -1, 0
	v_add_u32_e32 v202, 28, v192
	v_cndmask_b32_e32 v208, v202, v192, vcc
	v_ashrrev_i32_e32 v209, 31, v208
	v_cndmask_b32_e32 v183, v161, v201, vcc
	v_cndmask_b32_e32 v182, v160, v200, vcc
	v_lshlrev_b64 v[208:209], 7, v[208:209]
	v_lshl_add_u64 v[182:183], v[182:183], 0, v[208:209]
	s_add_i32 s40, s6, s68
	v_lshl_add_u64 v[210:211], v[182:183], 0, v[186:187]
	s_mov_b32 m0, s40
	ds_read_b128 v[166:169], v225 offset:16384
	ds_read_b128 v[170:173], v225 offset:17408
	ds_read_b128 v[174:177], v225 offset:18432
	ds_read_b128 v[178:181], v225 offset:19456
	ds_read_b128 v[226:229], v225 offset:20480
	ds_read_b128 v[230:233], v225 offset:21504
	ds_read_b128 v[238:241], v225 offset:22528
	ds_read_b128 v[242:245], v225 offset:23552
	global_load_lds_dwordx4 v[210:211], off
	v_lshl_add_u64 v[210:211], v[182:183], 0, v[190:191]
	s_add_i32 m0, s40, 0x2000
	v_lshl_add_u64 v[182:183], v[182:183], 0, s[0:1]
	s_add_i32 s40, s79, s68
	global_load_lds_dwordx4 v[210:211], off
	v_lshl_add_u64 v[210:211], v[182:183], 0, v[186:187]
	s_mov_b32 m0, s40
	v_lshl_add_u64 v[182:183], v[182:183], 0, v[190:191]
	global_load_lds_dwordx4 v[210:211], off
	s_add_i32 m0, s40, 0x2000
	s_and_b64 s[40:41], vcc, exec
	s_cselect_b32 s41, s27, s29
	s_cselect_b32 s40, s26, s28
	global_load_lds_dwordx4 v[182:183], off
	v_lshl_add_u64 v[182:183], s[40:41], 0, v[208:209]
	v_lshl_add_u64 v[208:209], v[182:183], 0, v[184:185]
	s_mov_b32 m0, s70
	s_nop 0
	global_load_lds_dwordx4 v[208:209], off
	v_lshl_add_u64 v[208:209], v[182:183], 0, v[188:189]
	s_mov_b32 m0, s71
	s_nop 0
	global_load_lds_dwordx4 v[208:209], off
	s_waitcnt vmcnt(8)
	s_waitcnt lgkmcnt(0)
	s_barrier
	s_setprio 1
	s_waitcnt lgkmcnt(0)
	v_mfma_f32_16x16x128_f8f6f4 v[92:95], v[24:31], v[166:173], v[92:95]
	v_mfma_f32_16x16x128_f8f6f4 v[88:91], v[16:23], v[166:173], v[88:91]
	v_mfma_f32_16x16x128_f8f6f4 v[76:79], v[24:31], v[174:181], v[76:79]
	v_mfma_f32_16x16x128_f8f6f4 v[72:75], v[16:23], v[174:181], v[72:75]
	v_mfma_f32_16x16x128_f8f6f4 v[52:55], v[24:31], v[226:233], v[52:55]
	v_mfma_f32_16x16x128_f8f6f4 v[48:51], v[16:23], v[226:233], v[48:51]
	v_mfma_f32_16x16x128_f8f6f4 v[36:39], v[24:31], v[238:245], v[36:39]
	v_mfma_f32_16x16x128_f8f6f4 v[32:35], v[16:23], v[238:245], v[32:35]
	v_mfma_f32_16x16x128_f8f6f4 v[84:87], v[8:15], v[166:173], v[84:87]
	v_mfma_f32_16x16x128_f8f6f4 v[80:83], v[0:7], v[166:173], v[80:83]
	v_mfma_f32_16x16x128_f8f6f4 v[60:63], v[8:15], v[174:181], v[60:63]
	v_mfma_f32_16x16x128_f8f6f4 v[56:59], v[0:7], v[174:181], v[56:59]
	v_mfma_f32_16x16x128_f8f6f4 v[68:71], v[8:15], v[226:233], v[68:71]
	v_mfma_f32_16x16x128_f8f6f4 v[64:67], v[0:7], v[226:233], v[64:67]
	v_mfma_f32_16x16x128_f8f6f4 v[44:47], v[8:15], v[238:245], v[44:47]
	v_mfma_f32_16x16x128_f8f6f4 v[40:43], v[0:7], v[238:245], v[40:43]
	s_setprio 0
	s_barrier
	s_add_i32 s42, 0, 0x18000
	s_add_i32 s43, 0, 0x1c000
	v_add_u32_e32 v0, s42, v207
	v_add_u32_e32 v4, s43, v207
	ds_read_b128 v[16:19], v0
	ds_read_b128 v[20:23], v0 offset:1024
	ds_read_b128 v[24:27], v0 offset:2048
	ds_read_b128 v[28:31], v0 offset:3072
	ds_read_b128 v[8:11], v4
	ds_read_b128 v[12:15], v4 offset:1024
	ds_read_b128 v[0:3], v4 offset:2048
	ds_read_b128 v[4:7], v4 offset:3072
	v_lshl_add_u64 v[182:183], v[182:183], 0, s[0:1]
	s_mov_b32 m0, s77
	v_lshl_add_u64 v[208:209], v[182:183], 0, v[184:185]
	ds_read_b128 v[166:169], v225 offset:32768
	ds_read_b128 v[170:173], v225 offset:33792
	ds_read_b128 v[174:177], v225 offset:34816
	ds_read_b128 v[178:181], v225 offset:35840
	ds_read_b128 v[226:229], v225 offset:36864
	ds_read_b128 v[230:233], v225 offset:37888
	ds_read_b128 v[238:241], v225 offset:38912
	ds_read_b128 v[242:245], v225 offset:39936
	global_load_lds_dwordx4 v[208:209], off
	v_lshl_add_u64 v[182:183], v[182:183], 0, v[188:189]
	s_mov_b32 m0, s78
	s_nop 0
	global_load_lds_dwordx4 v[182:183], off
	s_waitcnt vmcnt(8)
	s_waitcnt lgkmcnt(0)
	s_barrier
	s_setprio 1
	s_waitcnt lgkmcnt(0)
	v_mfma_f32_16x16x128_f8f6f4 v[156:159], v[16:23], v[166:173], v[156:159]
	v_mfma_f32_16x16x128_f8f6f4 v[152:155], v[24:31], v[166:173], v[152:155]
	v_mfma_f32_16x16x128_f8f6f4 v[140:143], v[16:23], v[174:181], v[140:143]
	v_mfma_f32_16x16x128_f8f6f4 v[136:139], v[24:31], v[174:181], v[136:139]
	v_mfma_f32_16x16x128_f8f6f4 v[124:127], v[16:23], v[226:233], v[124:127]
	v_mfma_f32_16x16x128_f8f6f4 v[120:123], v[24:31], v[226:233], v[120:123]
	v_mfma_f32_16x16x128_f8f6f4 v[108:111], v[16:23], v[238:245], v[108:111]
	v_mfma_f32_16x16x128_f8f6f4 v[104:107], v[24:31], v[238:245], v[104:107]
	v_mfma_f32_16x16x128_f8f6f4 v[148:151], v[8:15], v[166:173], v[148:151]
	v_mfma_f32_16x16x128_f8f6f4 v[144:147], v[0:7], v[166:173], v[144:147]
	v_mfma_f32_16x16x128_f8f6f4 v[132:135], v[8:15], v[174:181], v[132:135]
	v_mfma_f32_16x16x128_f8f6f4 v[128:131], v[0:7], v[174:181], v[128:131]
	v_mfma_f32_16x16x128_f8f6f4 v[116:119], v[8:15], v[226:233], v[116:119]
	v_mfma_f32_16x16x128_f8f6f4 v[112:115], v[0:7], v[226:233], v[112:115]
	v_mfma_f32_16x16x128_f8f6f4 v[100:103], v[8:15], v[238:245], v[100:103]
	v_mfma_f32_16x16x128_f8f6f4 v[96:99], v[0:7], v[238:245], v[96:99]
	s_setprio 0
	s_barrier
	s_cmp_gt_u32 s39, 24
	s_cselect_b64 vcc, -1, 0
	s_and_b64 s[40:41], vcc, exec
	s_cselect_b32 s40, 0xffffffe7, 3
	s_add_i32 s40, s40, s39
	s_ashr_i32 s41, s40, 31
	v_cndmask_b32_e32 v183, v161, v201, vcc
	v_cndmask_b32_e32 v182, v160, v200, vcc
	s_lshl_b64 s[40:41], s[40:41], 7
	v_lshl_add_u64 v[182:183], v[182:183], 0, s[40:41]
	s_add_i32 s42, s42, s68
	v_lshl_add_u64 v[208:209], v[182:183], 0, v[186:187]
	s_mov_b32 m0, s42
	ds_read_b128 v[166:169], v225 offset:49152
	ds_read_b128 v[170:173], v225 offset:50176
	ds_read_b128 v[174:177], v225 offset:51200
	ds_read_b128 v[178:181], v225 offset:52224
	ds_read_b128 v[226:229], v225 offset:53248
	ds_read_b128 v[230:233], v225 offset:54272
	ds_read_b128 v[238:241], v225 offset:55296
	ds_read_b128 v[242:245], v225 offset:56320
	global_load_lds_dwordx4 v[208:209], off
	v_lshl_add_u64 v[208:209], v[182:183], 0, v[190:191]
	s_add_i32 m0, s42, 0x2000
	v_lshl_add_u64 v[182:183], v[182:183], 0, s[0:1]
	s_add_i32 s42, s43, s68
	global_load_lds_dwordx4 v[208:209], off
	v_lshl_add_u64 v[208:209], v[182:183], 0, v[186:187]
	s_mov_b32 m0, s42
	v_lshl_add_u64 v[182:183], v[182:183], 0, v[190:191]
	global_load_lds_dwordx4 v[208:209], off
	s_add_i32 m0, s42, 0x2000
	s_and_b64 s[42:43], vcc, exec
	s_cselect_b32 s43, s26, s28
	s_cselect_b32 s42, s27, s29
	s_add_u32 s40, s43, s40
	s_addc_u32 s41, s42, s41
	global_load_lds_dwordx4 v[182:183], off
	v_lshl_add_u64 v[182:183], s[40:41], 0, v[184:185]
	s_mov_b32 m0, s54
	s_nop 0
	global_load_lds_dwordx4 v[182:183], off
	v_lshl_add_u64 v[182:183], s[40:41], 0, v[188:189]
	s_mov_b32 m0, s55
	s_nop 0
	global_load_lds_dwordx4 v[182:183], off
	s_waitcnt vmcnt(8)
	s_waitcnt lgkmcnt(0)
	s_barrier
	s_setprio 1
	s_waitcnt lgkmcnt(0)
	v_mfma_f32_16x16x128_f8f6f4 v[92:95], v[16:23], v[166:173], v[92:95]
	v_mfma_f32_16x16x128_f8f6f4 v[88:91], v[24:31], v[166:173], v[88:91]
	v_mfma_f32_16x16x128_f8f6f4 v[76:79], v[16:23], v[174:181], v[76:79]
	v_mfma_f32_16x16x128_f8f6f4 v[72:75], v[24:31], v[174:181], v[72:75]
	v_mfma_f32_16x16x128_f8f6f4 v[52:55], v[16:23], v[226:233], v[52:55]
	v_mfma_f32_16x16x128_f8f6f4 v[48:51], v[24:31], v[226:233], v[48:51]
	v_mfma_f32_16x16x128_f8f6f4 v[36:39], v[16:23], v[238:245], v[36:39]
	v_mfma_f32_16x16x128_f8f6f4 v[32:35], v[24:31], v[238:245], v[32:35]
	v_mfma_f32_16x16x128_f8f6f4 v[84:87], v[8:15], v[166:173], v[84:87]
	v_mfma_f32_16x16x128_f8f6f4 v[80:83], v[0:7], v[166:173], v[80:83]
	v_mfma_f32_16x16x128_f8f6f4 v[60:63], v[8:15], v[174:181], v[60:63]
	v_mfma_f32_16x16x128_f8f6f4 v[56:59], v[0:7], v[174:181], v[56:59]
	v_mfma_f32_16x16x128_f8f6f4 v[68:71], v[8:15], v[226:233], v[68:71]
	v_mfma_f32_16x16x128_f8f6f4 v[64:67], v[0:7], v[226:233], v[64:67]
	v_mfma_f32_16x16x128_f8f6f4 v[44:47], v[8:15], v[238:245], v[44:47]
	v_mfma_f32_16x16x128_f8f6f4 v[40:43], v[0:7], v[238:245], v[40:43]
	s_setprio 0
	s_barrier
	v_lshl_add_u64 v[162:163], v[162:163], 0, s[24:25]
	v_lshl_add_u64 v[164:165], v[164:165], 0, s[24:25]
	s_add_i32 s39, s39, 2
	s_and_b64 vcc, exec, s[30:31]
	s_cbranch_vccnz .LBB0_1373
	s_andn2_b64 vcc, exec, s[22:23]
	s_cbranch_vccnz .LBB0_1376
	s_barrier
